# fused fp8 schedule + prio2 + single hazard pad per epilogue + P10 routing scalar bias load
# baseline (speedup 1.0000x reference)
; #define PG8_STAGE(bufoff, gbase, voff) do { _Pragma("unroll") for (int _i = 0; _i < 2; ++_i) \
;         __builtin_amdgcn_global_load_lds((const unsigned*)((const char*)(gbase) + (voff)[_i]), (PG8_LAS unsigned*)(lds + (bufoff) + ldsw + _i * 8192), 16, 0, 0); } while (0)
; #define PG8_WAIT_V(n) asm volatile("s_waitcnt vmcnt(" #n ")" ::: "memory")
; #define PG8_WAIT_L(n) asm volatile("s_waitcnt lgkmcnt(" #n ")" ::: "memory")
; template <class Epi, class Sched, bool ALIGN_EPI = true, bool F8 = false>
; __device__ __forceinline__ void gemm_phase(PG8_LAS unsigned char* lds, const Sched& S, const Epi& E) {
;     ...
;         for (int t = 0; t < nt; t += 2) {
;             const bool last = (t == nt - 2);
;             if constexpr (Sched::GATHER) { if (last && has_next) S.a_off(nxt, Rs, Cs, voffAn); }
;             const char* a1 = cA + (size_t)(t + 1) * kstep;
;             const char* a2 = last ? nA : cA + (size_t)(t + 2) * kstep; const char* b2 = last ? nB : cB + (size_t)(t + 2) * kstepB;
;             const char* a3 = a2 + kstep; const char* b3 = b2 + kstepB;
;             unsigned vA2[2][2];
; #pragma unroll
;             for (int h = 0; h < 2; ++h)
; #pragma unroll
;                 for (int i = 0; i < 2; ++i) { if constexpr (Sched::GATHER) vA2[h][i] = (last && has_next) ? voffAn[h][i] : voffA[h][i]; else vA2[h][i] = voffA[h][i]; }
;             PG8_LDB(B0, 0, 0); PG8_LDB(B1, 0, 1); PG8_SCHED; PG8_LDA(At, 0, 0); PG8_STAGE(PG8_SA(1, 1), a1, voffA[1]);
;             PG8_WAIT_V(8); PG8_WAIT_L(0); PG8_BAR; PG8_MMA(0, 0, At, B0); PG8_MMA(0, 1, At, B1); PG8_BAR; PG8_SCHED;
;             PG8_LDA(At, 0, 1); PG8_STAGE(PG8_SB(0, 0), b2, voffB[0]); PG8_STAGE(PG8_SB(0, 1), b2, voffB[1]); PG8_STAGE(PG8_SA(0, 0), a2, vA2[0]);
;             PG8_WAIT_V(8); PG8_WAIT_L(0); PG8_BAR; PG8_MMA(1, 0, At, B0); PG8_MMA(1, 1, At, B1); PG8_BAR; PG8_SCHED;
;             PG8_LDB(B0, 1, 0); PG8_LDB(B1, 1, 1); PG8_SCHED; PG8_LDA(At, 1, 0); PG8_STAGE(PG8_SA(0, 1), a2, vA2[1]);
;             PG8_WAIT_V(8); PG8_WAIT_L(0); PG8_BAR; PG8_MMA(0, 0, At, B0); PG8_MMA(0, 1, At, B1); PG8_BAR; PG8_SCHED;
;             PG8_LDA(At, 1, 1); PG8_STAGE(PG8_SB(1, 0), b3, voffB[0]); PG8_STAGE(PG8_SB(1, 1), b3, voffB[1]); PG8_STAGE(PG8_SA(1, 0), a3, vA2[0]);
;             PG8_WAIT_V(8); PG8_WAIT_L(0); PG8_BAR; PG8_MMA(1, 0, At, B0); PG8_MMA(1, 1, At, B1); PG8_BAR; PG8_SCHED;
.Lh1e_9967:
.Lh1_372:
	ds_read_b128 v[18:21], v207
	ds_read_b128 v[22:25], v207 offset:1024
	ds_read_b128 v[26:29], v207 offset:2048
	ds_read_b128 v[30:33], v207 offset:3072
	ds_read_b128 v[2:5], v208
	ds_read_b128 v[6:9], v208 offset:1024
	ds_read_b128 v[10:13], v208 offset:2048
	ds_read_b128 v[14:17], v208 offset:3072
	s_add_u32 s28, s26, 0x8000
	s_addc_u32 s29, s27, 0
	s_cmp_eq_u32 s21, 12
	s_cselect_b32 s40, s22, s28
	s_cselect_b32 s41, s23, s29
	s_cselect_b32 s30, s24, s5
	s_cselect_b32 s31, s25, s19
	s_add_u32 s28, s40, 0x8000
	s_addc_u32 s29, s41, 0
	v_lshl_add_u64 v[244:245], s[26:27], 0, v[190:191]
	s_add_i32 m0, s46, 0xc000
	ds_read_b128 v[212:215], v209
	ds_read_b128 v[216:219], v209 offset:1024
	ds_read_b128 v[220:223], v209 offset:2048
	ds_read_b128 v[224:227], v209 offset:3072
	ds_read_b128 v[228:231], v209 offset:4096
	ds_read_b128 v[232:235], v209 offset:5120
	ds_read_b128 v[236:239], v209 offset:6144
	ds_read_b128 v[240:243], v209 offset:7168
	global_load_lds_dwordx4 v[244:245], off
	v_lshl_add_u64 v[244:245], s[26:27], 0, v[188:189]
	s_add_i32 m0, s46, 0xe000
	s_nop 0
	global_load_lds_dwordx4 v[244:245], off
	s_waitcnt vmcnt(8)
	s_waitcnt lgkmcnt(0)
	s_barrier
	s_setprio 2
	s_waitcnt lgkmcnt(0)
	v_mfma_scale_f32_16x16x128_f8f6f4 v[158:161], v[18:25], v[212:219], v[158:161], v210, v210 op_sel_hi:[0,0,0]
	v_mfma_scale_f32_16x16x128_f8f6f4 v[154:157], v[26:33], v[212:219], v[154:157], v210, v210 op_sel_hi:[0,0,0]
	v_mfma_scale_f32_16x16x128_f8f6f4 v[142:145], v[18:25], v[220:227], v[142:145], v210, v210 op_sel_hi:[0,0,0]
	v_mfma_scale_f32_16x16x128_f8f6f4 v[138:141], v[26:33], v[220:227], v[138:141], v210, v210 op_sel_hi:[0,0,0]
	v_mfma_scale_f32_16x16x128_f8f6f4 v[126:129], v[18:25], v[228:235], v[126:129], v210, v210 op_sel_hi:[0,0,0]
	v_mfma_scale_f32_16x16x128_f8f6f4 v[122:125], v[26:33], v[228:235], v[122:125], v210, v210 op_sel_hi:[0,0,0]
	v_mfma_scale_f32_16x16x128_f8f6f4 v[110:113], v[18:25], v[236:243], v[110:113], v210, v210 op_sel_hi:[0,0,0]
	v_mfma_scale_f32_16x16x128_f8f6f4 v[106:109], v[26:33], v[236:243], v[106:109], v210, v210 op_sel_hi:[0,0,0]
	s_nop 3
	s_setprio 0
	s_setprio 2
	v_mfma_scale_f32_16x16x128_f8f6f4 v[150:153], v[2:9], v[212:219], v[150:153], v210, v210 op_sel_hi:[0,0,0]
	v_mfma_scale_f32_16x16x128_f8f6f4 v[146:149], v[10:17], v[212:219], v[146:149], v210, v210 op_sel_hi:[0,0,0]
	v_mfma_scale_f32_16x16x128_f8f6f4 v[134:137], v[2:9], v[220:227], v[134:137], v210, v210 op_sel_hi:[0,0,0]
	v_mfma_scale_f32_16x16x128_f8f6f4 v[130:133], v[10:17], v[220:227], v[130:133], v210, v210 op_sel_hi:[0,0,0]
	v_mfma_scale_f32_16x16x128_f8f6f4 v[118:121], v[2:9], v[228:235], v[118:121], v210, v210 op_sel_hi:[0,0,0]
	v_mfma_scale_f32_16x16x128_f8f6f4 v[114:117], v[10:17], v[228:235], v[114:117], v210, v210 op_sel_hi:[0,0,0]
	v_mfma_scale_f32_16x16x128_f8f6f4 v[102:105], v[2:9], v[236:243], v[102:105], v210, v210 op_sel_hi:[0,0,0]
	v_mfma_scale_f32_16x16x128_f8f6f4 v[98:101], v[10:17], v[236:243], v[98:101], v210, v210 op_sel_hi:[0,0,0]
	s_nop 3
	s_setprio 0
	s_add_i32 s67, s62, s45
	v_lshl_add_u64 v[244:245], s[30:31], 0, v[164:165]
	s_mov_b32 m0, s67
	ds_read_b128 v[212:215], v209 offset:16384
	ds_read_b128 v[216:219], v209 offset:17408
	ds_read_b128 v[220:223], v209 offset:18432
	ds_read_b128 v[224:227], v209 offset:19456
	ds_read_b128 v[228:231], v209 offset:20480
	ds_read_b128 v[232:235], v209 offset:21504
	ds_read_b128 v[236:239], v209 offset:22528
	ds_read_b128 v[240:243], v209 offset:23552
	global_load_lds_dwordx4 v[244:245], off
	v_lshl_add_u64 v[246:247], s[30:31], 0, v[166:167]
	s_add_i32 m0, s67, 0x2000
	s_add_i32 s67, s63, s45
	global_load_lds_dwordx4 v[246:247], off
	v_lshl_add_u64 v[244:245], v[244:245], 0, s[8:9]
	s_mov_b32 m0, s67
	s_nop 0
	global_load_lds_dwordx4 v[244:245], off
	v_lshl_add_u64 v[244:245], v[246:247], 0, s[8:9]
	s_add_i32 m0, s67, 0x2000
	s_nop 0
	global_load_lds_dwordx4 v[244:245], off
	v_lshl_add_u64 v[244:245], s[40:41], 0, v[174:175]
	s_mov_b32 m0, s46
	s_nop 0
	global_load_lds_dwordx4 v[244:245], off
	v_lshl_add_u64 v[244:245], s[40:41], 0, v[176:177]
	s_mov_b32 m0, s47
	s_nop 0
	global_load_lds_dwordx4 v[244:245], off
	s_waitcnt vmcnt(8)
	s_waitcnt lgkmcnt(0)
	s_barrier
	s_setprio 2
	s_waitcnt lgkmcnt(0)
	v_mfma_scale_f32_16x16x128_f8f6f4 v[94:97], v[18:25], v[212:219], v[94:97], v210, v210 op_sel_hi:[0,0,0]
	v_mfma_scale_f32_16x16x128_f8f6f4 v[90:93], v[26:33], v[212:219], v[90:93], v210, v210 op_sel_hi:[0,0,0]
	v_mfma_scale_f32_16x16x128_f8f6f4 v[78:81], v[18:25], v[220:227], v[78:81], v210, v210 op_sel_hi:[0,0,0]
	v_mfma_scale_f32_16x16x128_f8f6f4 v[74:77], v[26:33], v[220:227], v[74:77], v210, v210 op_sel_hi:[0,0,0]
	v_mfma_scale_f32_16x16x128_f8f6f4 v[62:65], v[18:25], v[228:235], v[62:65], v210, v210 op_sel_hi:[0,0,0]
	v_mfma_scale_f32_16x16x128_f8f6f4 v[58:61], v[26:33], v[228:235], v[58:61], v210, v210 op_sel_hi:[0,0,0]
	v_mfma_scale_f32_16x16x128_f8f6f4 v[46:49], v[18:25], v[236:243], v[46:49], v210, v210 op_sel_hi:[0,0,0]
	v_mfma_scale_f32_16x16x128_f8f6f4 v[42:45], v[26:33], v[236:243], v[42:45], v210, v210 op_sel_hi:[0,0,0]
	s_nop 3
	s_setprio 0
	s_setprio 2
	v_mfma_scale_f32_16x16x128_f8f6f4 v[86:89], v[2:9], v[212:219], v[86:89], v210, v210 op_sel_hi:[0,0,0]
	v_mfma_scale_f32_16x16x128_f8f6f4 v[82:85], v[10:17], v[212:219], v[82:85], v210, v210 op_sel_hi:[0,0,0]
	v_mfma_scale_f32_16x16x128_f8f6f4 v[70:73], v[2:9], v[220:227], v[70:73], v210, v210 op_sel_hi:[0,0,0]
	v_mfma_scale_f32_16x16x128_f8f6f4 v[66:69], v[10:17], v[220:227], v[66:69], v210, v210 op_sel_hi:[0,0,0]
	v_mfma_scale_f32_16x16x128_f8f6f4 v[54:57], v[2:9], v[228:235], v[54:57], v210, v210 op_sel_hi:[0,0,0]
	v_mfma_scale_f32_16x16x128_f8f6f4 v[50:53], v[10:17], v[228:235], v[50:53], v210, v210 op_sel_hi:[0,0,0]
	v_mfma_scale_f32_16x16x128_f8f6f4 v[38:41], v[2:9], v[236:243], v[38:41], v210, v210 op_sel_hi:[0,0,0]
	v_mfma_scale_f32_16x16x128_f8f6f4 v[34:37], v[10:17], v[236:243], v[34:37], v210, v210 op_sel_hi:[0,0,0]
	s_nop 3
	s_setprio 0
	s_add_i32 s67, 0, 0x18000
	s_add_i32 s68, 0, 0x1c000
	v_add_u32_e32 v14, s67, v202
	v_add_u32_e32 v30, s68, v202
	ds_read_b128 v[2:5], v14
	ds_read_b128 v[6:9], v14 offset:1024
	ds_read_b128 v[10:13], v14 offset:2048
	ds_read_b128 v[14:17], v14 offset:3072
	ds_read_b128 v[18:21], v30
	ds_read_b128 v[22:25], v30 offset:1024
	ds_read_b128 v[26:29], v30 offset:2048
	ds_read_b128 v[30:33], v30 offset:3072
	s_mov_b32 m0, s48
	v_lshl_add_u64 v[244:245], s[40:41], 0, v[178:179]
	ds_read_b128 v[212:215], v209 offset:32768
	ds_read_b128 v[216:219], v209 offset:33792
	ds_read_b128 v[220:223], v209 offset:34816
	ds_read_b128 v[224:227], v209 offset:35840
	ds_read_b128 v[228:231], v209 offset:36864
	ds_read_b128 v[232:235], v209 offset:37888
	ds_read_b128 v[236:239], v209 offset:38912
	ds_read_b128 v[240:243], v209 offset:39936
	global_load_lds_dwordx4 v[244:245], off
	v_lshl_add_u64 v[244:245], s[40:41], 0, v[180:181]
	s_mov_b32 m0, s49
	s_nop 0
	global_load_lds_dwordx4 v[244:245], off
	s_waitcnt vmcnt(8)
	s_waitcnt lgkmcnt(0)
	s_barrier
; #define PG8_STAGE(bufoff, gbase, voff) do { _Pragma("unroll") for (int _i = 0; _i < 2; ++_i) \
;         __builtin_amdgcn_global_load_lds((const unsigned*)((const char*)(gbase) + (voff)[_i]), (PG8_LAS unsigned*)(lds + (bufoff) + ldsw + _i * 8192), 16, 0, 0); } while (0)
; #define PG8_WAIT_V(n) asm volatile("s_waitcnt vmcnt(" #n ")" ::: "memory")
; #define PG8_WAIT_L(n) asm volatile("s_waitcnt lgkmcnt(" #n ")" ::: "memory")
; template <class Epi, class Sched, bool ALIGN_EPI = true, bool F8 = false>
; __device__ __forceinline__ void gemm_phase(PG8_LAS unsigned char* lds, const Sched& S, const Epi& E) {
;     ...
;         for (int t = 0; t < nt; t += 2) {
;             const bool last = (t == nt - 2);
;             if constexpr (Sched::GATHER) { if (last && has_next) S.a_off(nxt, Rs, Cs, voffAn); }
;             const char* a1 = cA + (size_t)(t + 1) * kstep;
;             const char* a2 = last ? nA : cA + (size_t)(t + 2) * kstep; const char* b2 = last ? nB : cB + (size_t)(t + 2) * kstepB;
;             const char* a3 = a2 + kstep; const char* b3 = b2 + kstepB;
;             unsigned vA2[2][2];
; #pragma unroll
;             for (int h = 0; h < 2; ++h)
; #pragma unroll
;                 for (int i = 0; i < 2; ++i) { if constexpr (Sched::GATHER) vA2[h][i] = (last && has_next) ? voffAn[h][i] : voffA[h][i]; else vA2[h][i] = voffA[h][i]; }
;             PG8_LDB(B0, 0, 0); PG8_LDB(B1, 0, 1); PG8_SCHED; PG8_LDA(At, 0, 0); PG8_STAGE(PG8_SA(1, 1), a1, voffA[1]);
;             PG8_WAIT_V(8); PG8_WAIT_L(0); PG8_BAR; PG8_MMA(0, 0, At, B0); PG8_MMA(0, 1, At, B1); PG8_BAR; PG8_SCHED;
;             PG8_LDA(At, 0, 1); PG8_STAGE(PG8_SB(0, 0), b2, voffB[0]); PG8_STAGE(PG8_SB(0, 1), b2, voffB[1]); PG8_STAGE(PG8_SA(0, 0), a2, vA2[0]);
;             PG8_WAIT_V(8); PG8_WAIT_L(0); PG8_BAR; PG8_MMA(1, 0, At, B0); PG8_MMA(1, 1, At, B1); PG8_BAR; PG8_SCHED;
;             PG8_LDB(B0, 1, 0); PG8_LDB(B1, 1, 1); PG8_SCHED; PG8_LDA(At, 1, 0); PG8_STAGE(PG8_SA(0, 1), a2, vA2[1]);
;             PG8_WAIT_V(8); PG8_WAIT_L(0); PG8_BAR; PG8_MMA(0, 0, At, B0); PG8_MMA(0, 1, At, B1); PG8_BAR; PG8_SCHED;
;             PG8_LDA(At, 1, 1); PG8_STAGE(PG8_SB(1, 0), b3, voffB[0]); PG8_STAGE(PG8_SB(1, 1), b3, voffB[1]); PG8_STAGE(PG8_SA(1, 0), a3, vA2[0]);
;             PG8_WAIT_V(8); PG8_WAIT_L(0); PG8_BAR; PG8_MMA(1, 0, At, B0); PG8_MMA(1, 1, At, B1); PG8_BAR; PG8_SCHED;
	s_setprio 2
	s_waitcnt lgkmcnt(0)
	v_mfma_scale_f32_16x16x128_f8f6f4 v[158:161], v[2:9], v[212:219], v[158:161], v210, v210 op_sel_hi:[0,0,0]
	v_mfma_scale_f32_16x16x128_f8f6f4 v[154:157], v[10:17], v[212:219], v[154:157], v210, v210 op_sel_hi:[0,0,0]
	v_mfma_scale_f32_16x16x128_f8f6f4 v[142:145], v[2:9], v[220:227], v[142:145], v210, v210 op_sel_hi:[0,0,0]
	v_mfma_scale_f32_16x16x128_f8f6f4 v[138:141], v[10:17], v[220:227], v[138:141], v210, v210 op_sel_hi:[0,0,0]
	v_mfma_scale_f32_16x16x128_f8f6f4 v[126:129], v[2:9], v[228:235], v[126:129], v210, v210 op_sel_hi:[0,0,0]
	v_mfma_scale_f32_16x16x128_f8f6f4 v[122:125], v[10:17], v[228:235], v[122:125], v210, v210 op_sel_hi:[0,0,0]
	v_mfma_scale_f32_16x16x128_f8f6f4 v[110:113], v[2:9], v[236:243], v[110:113], v210, v210 op_sel_hi:[0,0,0]
	v_mfma_scale_f32_16x16x128_f8f6f4 v[106:109], v[10:17], v[236:243], v[106:109], v210, v210 op_sel_hi:[0,0,0]
	s_nop 3
	s_setprio 0
	s_setprio 2
	v_mfma_scale_f32_16x16x128_f8f6f4 v[150:153], v[18:25], v[212:219], v[150:153], v210, v210 op_sel_hi:[0,0,0]
	v_mfma_scale_f32_16x16x128_f8f6f4 v[146:149], v[26:33], v[212:219], v[146:149], v210, v210 op_sel_hi:[0,0,0]
	v_mfma_scale_f32_16x16x128_f8f6f4 v[134:137], v[18:25], v[220:227], v[134:137], v210, v210 op_sel_hi:[0,0,0]
	v_mfma_scale_f32_16x16x128_f8f6f4 v[130:133], v[26:33], v[220:227], v[130:133], v210, v210 op_sel_hi:[0,0,0]
	v_mfma_scale_f32_16x16x128_f8f6f4 v[118:121], v[18:25], v[228:235], v[118:121], v210, v210 op_sel_hi:[0,0,0]
	v_mfma_scale_f32_16x16x128_f8f6f4 v[114:117], v[26:33], v[228:235], v[114:117], v210, v210 op_sel_hi:[0,0,0]
	v_mfma_scale_f32_16x16x128_f8f6f4 v[102:105], v[18:25], v[236:243], v[102:105], v210, v210 op_sel_hi:[0,0,0]
	v_mfma_scale_f32_16x16x128_f8f6f4 v[98:101], v[26:33], v[236:243], v[98:101], v210, v210 op_sel_hi:[0,0,0]
	s_nop 3
	s_setprio 0
	s_add_u32 s30, s30, 0x8000
	s_addc_u32 s31, s31, 0
	s_add_i32 s40, s67, s45
	v_lshl_add_u64 v[244:245], s[30:31], 0, v[164:165]
	s_mov_b32 m0, s40
	ds_read_b128 v[212:215], v209 offset:49152
	ds_read_b128 v[216:219], v209 offset:50176
	ds_read_b128 v[220:223], v209 offset:51200
	ds_read_b128 v[224:227], v209 offset:52224
	ds_read_b128 v[228:231], v209 offset:53248
	ds_read_b128 v[232:235], v209 offset:54272
	ds_read_b128 v[236:239], v209 offset:55296
	ds_read_b128 v[240:243], v209 offset:56320
	global_load_lds_dwordx4 v[244:245], off
	v_lshl_add_u64 v[244:245], s[30:31], 0, v[166:167]
	s_add_i32 m0, s40, 0x2000
	s_add_i32 s40, s68, s45
	global_load_lds_dwordx4 v[244:245], off
	v_lshl_add_u64 v[244:245], s[30:31], 0, v[168:169]
	s_mov_b32 m0, s40
	s_nop 0
	global_load_lds_dwordx4 v[244:245], off
	v_lshl_add_u64 v[244:245], s[30:31], 0, v[172:173]
	s_add_i32 m0, s40, 0x2000
	s_nop 0
	global_load_lds_dwordx4 v[244:245], off
	v_lshl_add_u64 v[244:245], s[28:29], 0, v[174:175]
	s_mov_b32 m0, s52
	s_nop 0
	global_load_lds_dwordx4 v[244:245], off
	v_lshl_add_u64 v[244:245], s[28:29], 0, v[176:177]
	s_mov_b32 m0, s53
	s_nop 0
	global_load_lds_dwordx4 v[244:245], off
	s_waitcnt vmcnt(8)
	s_waitcnt lgkmcnt(0)
	s_barrier
	s_setprio 2
	s_waitcnt lgkmcnt(0)
	v_mfma_scale_f32_16x16x128_f8f6f4 v[94:97], v[2:9], v[212:219], v[94:97], v210, v210 op_sel_hi:[0,0,0]
	v_mfma_scale_f32_16x16x128_f8f6f4 v[90:93], v[10:17], v[212:219], v[90:93], v210, v210 op_sel_hi:[0,0,0]
	v_mfma_scale_f32_16x16x128_f8f6f4 v[78:81], v[2:9], v[220:227], v[78:81], v210, v210 op_sel_hi:[0,0,0]
	v_mfma_scale_f32_16x16x128_f8f6f4 v[74:77], v[10:17], v[220:227], v[74:77], v210, v210 op_sel_hi:[0,0,0]
	v_mfma_scale_f32_16x16x128_f8f6f4 v[62:65], v[2:9], v[228:235], v[62:65], v210, v210 op_sel_hi:[0,0,0]
	v_mfma_scale_f32_16x16x128_f8f6f4 v[58:61], v[10:17], v[228:235], v[58:61], v210, v210 op_sel_hi:[0,0,0]
	v_mfma_scale_f32_16x16x128_f8f6f4 v[46:49], v[2:9], v[236:243], v[46:49], v210, v210 op_sel_hi:[0,0,0]
	v_mfma_scale_f32_16x16x128_f8f6f4 v[42:45], v[10:17], v[236:243], v[42:45], v210, v210 op_sel_hi:[0,0,0]
	s_nop 3
	s_setprio 0
	s_setprio 2
	v_mfma_scale_f32_16x16x128_f8f6f4 v[86:89], v[18:25], v[212:219], v[86:89], v210, v210 op_sel_hi:[0,0,0]
	v_mfma_scale_f32_16x16x128_f8f6f4 v[82:85], v[26:33], v[212:219], v[82:85], v210, v210 op_sel_hi:[0,0,0]
	v_mfma_scale_f32_16x16x128_f8f6f4 v[70:73], v[18:25], v[220:227], v[70:73], v210, v210 op_sel_hi:[0,0,0]
	v_mfma_scale_f32_16x16x128_f8f6f4 v[66:69], v[26:33], v[220:227], v[66:69], v210, v210 op_sel_hi:[0,0,0]
	v_mfma_scale_f32_16x16x128_f8f6f4 v[54:57], v[18:25], v[228:235], v[54:57], v210, v210 op_sel_hi:[0,0,0]
	v_mfma_scale_f32_16x16x128_f8f6f4 v[50:53], v[26:33], v[228:235], v[50:53], v210, v210 op_sel_hi:[0,0,0]
	v_mfma_scale_f32_16x16x128_f8f6f4 v[38:41], v[18:25], v[236:243], v[38:41], v210, v210 op_sel_hi:[0,0,0]
	v_mfma_scale_f32_16x16x128_f8f6f4 v[34:37], v[26:33], v[236:243], v[34:37], v210, v210 op_sel_hi:[0,0,0]
	s_nop 3
	s_setprio 0
	s_add_i32 s21, s21, 2
	s_add_u32 s5, s5, 0x10000
	s_addc_u32 s19, s19, 0
	s_add_u32 s26, s26, 0x10000
	s_addc_u32 s27, s27, 0
	s_cmp_gt_u32 s21, 13
	s_cbranch_scc0 .Lh1_372

; template <class Epi, class Sched, bool ALIGN_EPI = true, bool F8 = false>
; __device__ __forceinline__ void gemm_phase(PG8_LAS unsigned char* lds, const Sched& S, const Epi& E) {
;     ...
;         if constexpr (F8) {
; #pragma unroll
;             for (int a = 0; a < 2; ++a)
; #pragma unroll
;                 for (int b = 0; b < 2; ++b)
;                     asm volatile("s_nop 15\n\ts_nop 7" : "+v"(acc[a][b][0][0]), "+v"(acc[a][b][0][1]), "+v"(acc[a][b][1][0]), "+v"(acc[a][b][1][1]), "+v"(acc[a][b][2][0]), "+v"(acc[a][b][2][1]), "+v"(acc[a][b][3][0]), "+v"(acc[a][b][3][1]));
;     __device__ __forceinline__ void operator()(AccRef acc, const GUnit& u, int wr, int wc, int fr, int fq) const {
;         const int pm = u.x0, pn = u.x1; const int col = pn * 256 + wc * 64 + 16 * fq;
; #pragma unroll
;         for (int ai = 0; ai < 2; ++ai)
; #pragma unroll
;             for (int m = 0; m < 4; ++m) { const int row = pm * 256 + ai * 128 + wr * 64 + m * 16 + fr; bf16* dst;
;                 if (pn < 4) dst = UF + (size_t)row * FW + col;
;                 else { const int g = (col - FW) >> 4, b = row >> 13, t = row & (SEQ - 1); dst = A2 + ((size_t)((g * 4 + b) * NCH + NCTXCH + (t >> 5)) * A2LD + (t & 31) * 16); }
;                 constexpr float SC = S8 ? W8_INV : 1.0f; st16_bf16(dst, acc[ai][0][m][0] * SC, acc[ai][0][m][1] * SC, acc[ai][1][m][0] * SC, acc[ai][1][m][1] * SC); }
.LBB0_375:
	s_lshl_b32 s19, s4, 8
	v_lshl_or_b32 v2, s66, 8, v206
	s_add_i32 s19, s19, s51
	s_cmp_gt_i32 s66, 3
	v_add_u32_e32 v3, 0xfffffc00, v2
	s_cselect_b64 s[26:27], -1, 0
	v_ashrrev_i32_e32 v10, 2, v3
	s_ashr_i32 s4, s19, 13
	v_add_u32_e32 v3, s4, v10
	v_mad_u64_u32 v[4:5], s[4:5], v3, s64, 8
	s_mov_b64 s[4:5], -1
	s_and_b64 vcc, exec, s[26:27]
	s_nop 15
	s_nop 7
	s_cbranch_vccz .LBB0_377
	s_lshr_b32 s4, s19, 5
	s_and_b32 s4, s4, 0xfe
	v_add_u32_e32 v3, s4, v4
	v_mad_i64_i32 v[6:7], s[4:5], v3, s65, v[182:183]
	s_mov_b64 s[4:5], 0

; #define PG8_STAGE(bufoff, gbase, voff) do { _Pragma("unroll") for (int _i = 0; _i < 2; ++_i) \
;         __builtin_amdgcn_global_load_lds((const unsigned*)((const char*)(gbase) + (voff)[_i]), (PG8_LAS unsigned*)(lds + (bufoff) + ldsw + _i * 8192), 16, 0, 0); } while (0)
; #define PG8_WAIT_V(n) asm volatile("s_waitcnt vmcnt(" #n ")" ::: "memory")
; #define PG8_WAIT_L(n) asm volatile("s_waitcnt lgkmcnt(" #n ")" ::: "memory")
; template <class Epi, class Sched, bool ALIGN_EPI = true, bool F8 = false>
; __device__ __forceinline__ void gemm_phase(PG8_LAS unsigned char* lds, const Sched& S, const Epi& E) {
;     ...
;         for (int t = 0; t < nt; t += 2) {
;             const bool last = (t == nt - 2);
;             if constexpr (Sched::GATHER) { if (last && has_next) S.a_off(nxt, Rs, Cs, voffAn); }
;             const char* a1 = cA + (size_t)(t + 1) * kstep;
;             const char* a2 = last ? nA : cA + (size_t)(t + 2) * kstep; const char* b2 = last ? nB : cB + (size_t)(t + 2) * kstepB;
;             const char* a3 = a2 + kstep; const char* b3 = b2 + kstepB;
;             unsigned vA2[2][2];
; #pragma unroll
;             for (int h = 0; h < 2; ++h)
; #pragma unroll
;                 for (int i = 0; i < 2; ++i) { if constexpr (Sched::GATHER) vA2[h][i] = (last && has_next) ? voffAn[h][i] : voffA[h][i]; else vA2[h][i] = voffA[h][i]; }
;             PG8_LDB(B0, 0, 0); PG8_LDB(B1, 0, 1); PG8_SCHED; PG8_LDA(At, 0, 0); PG8_STAGE(PG8_SA(1, 1), a1, voffA[1]);
;             PG8_WAIT_V(8); PG8_WAIT_L(0); PG8_BAR; PG8_MMA(0, 0, At, B0); PG8_MMA(0, 1, At, B1); PG8_BAR; PG8_SCHED;
;             PG8_LDA(At, 0, 1); PG8_STAGE(PG8_SB(0, 0), b2, voffB[0]); PG8_STAGE(PG8_SB(0, 1), b2, voffB[1]); PG8_STAGE(PG8_SA(0, 0), a2, vA2[0]);
;             PG8_WAIT_V(8); PG8_WAIT_L(0); PG8_BAR; PG8_MMA(1, 0, At, B0); PG8_MMA(1, 1, At, B1); PG8_BAR; PG8_SCHED;
;             PG8_LDB(B0, 1, 0); PG8_LDB(B1, 1, 1); PG8_SCHED; PG8_LDA(At, 1, 0); PG8_STAGE(PG8_SA(0, 1), a2, vA2[1]);
;             PG8_WAIT_V(8); PG8_WAIT_L(0); PG8_BAR; PG8_MMA(0, 0, At, B0); PG8_MMA(0, 1, At, B1); PG8_BAR; PG8_SCHED;
;             PG8_LDA(At, 1, 1); PG8_STAGE(PG8_SB(1, 0), b3, voffB[0]); PG8_STAGE(PG8_SB(1, 1), b3, voffB[1]); PG8_STAGE(PG8_SA(1, 0), a3, vA2[0]);
;             PG8_WAIT_V(8); PG8_WAIT_L(0); PG8_BAR; PG8_MMA(1, 0, At, B0); PG8_MMA(1, 1, At, B1); PG8_BAR; PG8_SCHED;
.Lh1e_11141:
.Lh1_428:
	ds_read_b128 v[18:21], v192
	ds_read_b128 v[22:25], v192 offset:1024
	ds_read_b128 v[26:29], v192 offset:2048
	ds_read_b128 v[30:33], v192 offset:3072
	ds_read_b128 v[2:5], v193
	ds_read_b128 v[6:9], v193 offset:1024
	ds_read_b128 v[10:13], v193 offset:2048
	ds_read_b128 v[14:17], v193 offset:3072
	s_add_u32 s26, s24, 0x8000
	s_addc_u32 s27, s25, 0
	s_cmp_eq_u32 s74, 12
	s_cselect_b32 s30, s20, s26
	s_cselect_b32 s31, s21, s27
	s_cselect_b32 s28, s22, s17
	s_cselect_b32 s29, s23, s19
	s_add_u32 s26, s30, 0x8000
	s_addc_u32 s27, s31, 0
	v_lshl_add_u64 v[230:231], s[24:25], 0, v[184:185]
	s_add_i32 m0, s48, 0xc000
	ds_read_b128 v[198:201], v194
	ds_read_b128 v[202:205], v194 offset:1024
	ds_read_b128 v[206:209], v194 offset:2048
	ds_read_b128 v[210:213], v194 offset:3072
	ds_read_b128 v[214:217], v194 offset:4096
	ds_read_b128 v[218:221], v194 offset:5120
	ds_read_b128 v[222:225], v194 offset:6144
	ds_read_b128 v[226:229], v194 offset:7168
	global_load_lds_dwordx4 v[230:231], off
	v_lshl_add_u64 v[230:231], s[24:25], 0, v[182:183]
	s_add_i32 m0, s48, 0xe000
	s_nop 0
	global_load_lds_dwordx4 v[230:231], off
	s_waitcnt vmcnt(8)
	s_waitcnt lgkmcnt(0)
	s_barrier
	s_setprio 2
	s_waitcnt lgkmcnt(0)
	v_mfma_scale_f32_16x16x128_f8f6f4 v[158:161], v[18:25], v[198:205], v[158:161], v195, v195 op_sel_hi:[0,0,0]
	v_mfma_scale_f32_16x16x128_f8f6f4 v[154:157], v[26:33], v[198:205], v[154:157], v195, v195 op_sel_hi:[0,0,0]
	v_mfma_scale_f32_16x16x128_f8f6f4 v[142:145], v[18:25], v[206:213], v[142:145], v195, v195 op_sel_hi:[0,0,0]
	v_mfma_scale_f32_16x16x128_f8f6f4 v[138:141], v[26:33], v[206:213], v[138:141], v195, v195 op_sel_hi:[0,0,0]
	v_mfma_scale_f32_16x16x128_f8f6f4 v[126:129], v[18:25], v[214:221], v[126:129], v195, v195 op_sel_hi:[0,0,0]
	v_mfma_scale_f32_16x16x128_f8f6f4 v[122:125], v[26:33], v[214:221], v[122:125], v195, v195 op_sel_hi:[0,0,0]
	v_mfma_scale_f32_16x16x128_f8f6f4 v[110:113], v[18:25], v[222:229], v[110:113], v195, v195 op_sel_hi:[0,0,0]
	v_mfma_scale_f32_16x16x128_f8f6f4 v[106:109], v[26:33], v[222:229], v[106:109], v195, v195 op_sel_hi:[0,0,0]
	s_nop 3
	s_setprio 0
	s_setprio 2
	v_mfma_scale_f32_16x16x128_f8f6f4 v[150:153], v[2:9], v[198:205], v[150:153], v195, v195 op_sel_hi:[0,0,0]
	v_mfma_scale_f32_16x16x128_f8f6f4 v[146:149], v[10:17], v[198:205], v[146:149], v195, v195 op_sel_hi:[0,0,0]
	v_mfma_scale_f32_16x16x128_f8f6f4 v[134:137], v[2:9], v[206:213], v[134:137], v195, v195 op_sel_hi:[0,0,0]
	v_mfma_scale_f32_16x16x128_f8f6f4 v[130:133], v[10:17], v[206:213], v[130:133], v195, v195 op_sel_hi:[0,0,0]
	v_mfma_scale_f32_16x16x128_f8f6f4 v[118:121], v[2:9], v[214:221], v[118:121], v195, v195 op_sel_hi:[0,0,0]
	v_mfma_scale_f32_16x16x128_f8f6f4 v[114:117], v[10:17], v[214:221], v[114:117], v195, v195 op_sel_hi:[0,0,0]
	v_mfma_scale_f32_16x16x128_f8f6f4 v[102:105], v[2:9], v[222:229], v[102:105], v195, v195 op_sel_hi:[0,0,0]
	v_mfma_scale_f32_16x16x128_f8f6f4 v[98:101], v[10:17], v[222:229], v[98:101], v195, v195 op_sel_hi:[0,0,0]
	s_nop 3
	s_setprio 0
	s_add_i32 s75, s65, s47
	v_lshl_add_u64 v[230:231], s[28:29], 0, v[164:165]
	s_mov_b32 m0, s75
	ds_read_b128 v[198:201], v194 offset:16384
	ds_read_b128 v[202:205], v194 offset:17408
	ds_read_b128 v[206:209], v194 offset:18432
	ds_read_b128 v[210:213], v194 offset:19456
	ds_read_b128 v[214:217], v194 offset:20480
	ds_read_b128 v[218:221], v194 offset:21504
	ds_read_b128 v[222:225], v194 offset:22528
	ds_read_b128 v[226:229], v194 offset:23552
	global_load_lds_dwordx4 v[230:231], off
	v_lshl_add_u64 v[232:233], s[28:29], 0, v[166:167]
	s_add_i32 m0, s75, 0x2000
	s_add_i32 s75, s66, s47
	global_load_lds_dwordx4 v[232:233], off
	v_lshl_add_u64 v[230:231], v[230:231], 0, s[4:5]
	s_mov_b32 m0, s75
	s_nop 0
	global_load_lds_dwordx4 v[230:231], off
	v_lshl_add_u64 v[230:231], v[232:233], 0, s[4:5]
	s_add_i32 m0, s75, 0x2000
	s_nop 0
	global_load_lds_dwordx4 v[230:231], off
	v_lshl_add_u64 v[230:231], s[30:31], 0, v[174:175]
	s_mov_b32 m0, s48
	s_nop 0
	global_load_lds_dwordx4 v[230:231], off
	v_lshl_add_u64 v[230:231], s[30:31], 0, v[176:177]
	s_mov_b32 m0, s49
	s_nop 0
	global_load_lds_dwordx4 v[230:231], off
	s_waitcnt vmcnt(8)
	s_waitcnt lgkmcnt(0)
	s_barrier
	s_setprio 2
	s_waitcnt lgkmcnt(0)
	v_mfma_scale_f32_16x16x128_f8f6f4 v[94:97], v[18:25], v[198:205], v[94:97], v195, v195 op_sel_hi:[0,0,0]
	v_mfma_scale_f32_16x16x128_f8f6f4 v[90:93], v[26:33], v[198:205], v[90:93], v195, v195 op_sel_hi:[0,0,0]
	v_mfma_scale_f32_16x16x128_f8f6f4 v[78:81], v[18:25], v[206:213], v[78:81], v195, v195 op_sel_hi:[0,0,0]
	v_mfma_scale_f32_16x16x128_f8f6f4 v[74:77], v[26:33], v[206:213], v[74:77], v195, v195 op_sel_hi:[0,0,0]
	v_mfma_scale_f32_16x16x128_f8f6f4 v[62:65], v[18:25], v[214:221], v[62:65], v195, v195 op_sel_hi:[0,0,0]
	v_mfma_scale_f32_16x16x128_f8f6f4 v[58:61], v[26:33], v[214:221], v[58:61], v195, v195 op_sel_hi:[0,0,0]
	v_mfma_scale_f32_16x16x128_f8f6f4 v[46:49], v[18:25], v[222:229], v[46:49], v195, v195 op_sel_hi:[0,0,0]
	v_mfma_scale_f32_16x16x128_f8f6f4 v[42:45], v[26:33], v[222:229], v[42:45], v195, v195 op_sel_hi:[0,0,0]
	s_nop 3
	s_setprio 0
	s_setprio 2
	v_mfma_scale_f32_16x16x128_f8f6f4 v[86:89], v[2:9], v[198:205], v[86:89], v195, v195 op_sel_hi:[0,0,0]
	v_mfma_scale_f32_16x16x128_f8f6f4 v[82:85], v[10:17], v[198:205], v[82:85], v195, v195 op_sel_hi:[0,0,0]
	v_mfma_scale_f32_16x16x128_f8f6f4 v[70:73], v[2:9], v[206:213], v[70:73], v195, v195 op_sel_hi:[0,0,0]
	v_mfma_scale_f32_16x16x128_f8f6f4 v[66:69], v[10:17], v[206:213], v[66:69], v195, v195 op_sel_hi:[0,0,0]
	v_mfma_scale_f32_16x16x128_f8f6f4 v[54:57], v[2:9], v[214:221], v[54:57], v195, v195 op_sel_hi:[0,0,0]
	v_mfma_scale_f32_16x16x128_f8f6f4 v[50:53], v[10:17], v[214:221], v[50:53], v195, v195 op_sel_hi:[0,0,0]
	v_mfma_scale_f32_16x16x128_f8f6f4 v[38:41], v[2:9], v[222:229], v[38:41], v195, v195 op_sel_hi:[0,0,0]
	v_mfma_scale_f32_16x16x128_f8f6f4 v[34:37], v[10:17], v[222:229], v[34:37], v195, v195 op_sel_hi:[0,0,0]
	s_nop 3
	s_setprio 0
	s_add_i32 s75, 0, 0x18000
	s_add_i32 s76, 0, 0x1c000
	v_add_u32_e32 v14, s75, v191
	v_add_u32_e32 v30, s76, v191
	ds_read_b128 v[2:5], v14
	ds_read_b128 v[6:9], v14 offset:1024
	ds_read_b128 v[10:13], v14 offset:2048
	ds_read_b128 v[14:17], v14 offset:3072
	ds_read_b128 v[18:21], v30
	ds_read_b128 v[22:25], v30 offset:1024
	ds_read_b128 v[26:29], v30 offset:2048
	ds_read_b128 v[30:33], v30 offset:3072
	s_mov_b32 m0, s50
	v_lshl_add_u64 v[230:231], s[30:31], 0, v[178:179]
	ds_read_b128 v[198:201], v194 offset:32768
	ds_read_b128 v[202:205], v194 offset:33792
	ds_read_b128 v[206:209], v194 offset:34816
	ds_read_b128 v[210:213], v194 offset:35840
	ds_read_b128 v[214:217], v194 offset:36864
	ds_read_b128 v[218:221], v194 offset:37888
	ds_read_b128 v[222:225], v194 offset:38912
	ds_read_b128 v[226:229], v194 offset:39936
	global_load_lds_dwordx4 v[230:231], off
	v_lshl_add_u64 v[230:231], s[30:31], 0, v[180:181]
	s_mov_b32 m0, s51
	s_nop 0
	global_load_lds_dwordx4 v[230:231], off
	s_waitcnt vmcnt(8)
	s_waitcnt lgkmcnt(0)
	s_barrier
; #define PG8_STAGE(bufoff, gbase, voff) do { _Pragma("unroll") for (int _i = 0; _i < 2; ++_i) \
;         __builtin_amdgcn_global_load_lds((const unsigned*)((const char*)(gbase) + (voff)[_i]), (PG8_LAS unsigned*)(lds + (bufoff) + ldsw + _i * 8192), 16, 0, 0); } while (0)
; #define PG8_WAIT_V(n) asm volatile("s_waitcnt vmcnt(" #n ")" ::: "memory")
; #define PG8_WAIT_L(n) asm volatile("s_waitcnt lgkmcnt(" #n ")" ::: "memory")
; template <class Epi, class Sched, bool ALIGN_EPI = true, bool F8 = false>
; __device__ __forceinline__ void gemm_phase(PG8_LAS unsigned char* lds, const Sched& S, const Epi& E) {
;     ...
;         for (int t = 0; t < nt; t += 2) {
;             const bool last = (t == nt - 2);
;             if constexpr (Sched::GATHER) { if (last && has_next) S.a_off(nxt, Rs, Cs, voffAn); }
;             const char* a1 = cA + (size_t)(t + 1) * kstep;
;             const char* a2 = last ? nA : cA + (size_t)(t + 2) * kstep; const char* b2 = last ? nB : cB + (size_t)(t + 2) * kstepB;
;             const char* a3 = a2 + kstep; const char* b3 = b2 + kstepB;
;             unsigned vA2[2][2];
; #pragma unroll
;             for (int h = 0; h < 2; ++h)
; #pragma unroll
;                 for (int i = 0; i < 2; ++i) { if constexpr (Sched::GATHER) vA2[h][i] = (last && has_next) ? voffAn[h][i] : voffA[h][i]; else vA2[h][i] = voffA[h][i]; }
;             PG8_LDB(B0, 0, 0); PG8_LDB(B1, 0, 1); PG8_SCHED; PG8_LDA(At, 0, 0); PG8_STAGE(PG8_SA(1, 1), a1, voffA[1]);
;             PG8_WAIT_V(8); PG8_WAIT_L(0); PG8_BAR; PG8_MMA(0, 0, At, B0); PG8_MMA(0, 1, At, B1); PG8_BAR; PG8_SCHED;
;             PG8_LDA(At, 0, 1); PG8_STAGE(PG8_SB(0, 0), b2, voffB[0]); PG8_STAGE(PG8_SB(0, 1), b2, voffB[1]); PG8_STAGE(PG8_SA(0, 0), a2, vA2[0]);
;             PG8_WAIT_V(8); PG8_WAIT_L(0); PG8_BAR; PG8_MMA(1, 0, At, B0); PG8_MMA(1, 1, At, B1); PG8_BAR; PG8_SCHED;
;             PG8_LDB(B0, 1, 0); PG8_LDB(B1, 1, 1); PG8_SCHED; PG8_LDA(At, 1, 0); PG8_STAGE(PG8_SA(0, 1), a2, vA2[1]);
;             PG8_WAIT_V(8); PG8_WAIT_L(0); PG8_BAR; PG8_MMA(0, 0, At, B0); PG8_MMA(0, 1, At, B1); PG8_BAR; PG8_SCHED;
;             PG8_LDA(At, 1, 1); PG8_STAGE(PG8_SB(1, 0), b3, voffB[0]); PG8_STAGE(PG8_SB(1, 1), b3, voffB[1]); PG8_STAGE(PG8_SA(1, 0), a3, vA2[0]);
;             PG8_WAIT_V(8); PG8_WAIT_L(0); PG8_BAR; PG8_MMA(1, 0, At, B0); PG8_MMA(1, 1, At, B1); PG8_BAR; PG8_SCHED;
	s_setprio 2
	s_waitcnt lgkmcnt(0)
	v_mfma_scale_f32_16x16x128_f8f6f4 v[158:161], v[2:9], v[198:205], v[158:161], v195, v195 op_sel_hi:[0,0,0]
	v_mfma_scale_f32_16x16x128_f8f6f4 v[154:157], v[10:17], v[198:205], v[154:157], v195, v195 op_sel_hi:[0,0,0]
	v_mfma_scale_f32_16x16x128_f8f6f4 v[142:145], v[2:9], v[206:213], v[142:145], v195, v195 op_sel_hi:[0,0,0]
	v_mfma_scale_f32_16x16x128_f8f6f4 v[138:141], v[10:17], v[206:213], v[138:141], v195, v195 op_sel_hi:[0,0,0]
	v_mfma_scale_f32_16x16x128_f8f6f4 v[126:129], v[2:9], v[214:221], v[126:129], v195, v195 op_sel_hi:[0,0,0]
	v_mfma_scale_f32_16x16x128_f8f6f4 v[122:125], v[10:17], v[214:221], v[122:125], v195, v195 op_sel_hi:[0,0,0]
	v_mfma_scale_f32_16x16x128_f8f6f4 v[110:113], v[2:9], v[222:229], v[110:113], v195, v195 op_sel_hi:[0,0,0]
	v_mfma_scale_f32_16x16x128_f8f6f4 v[106:109], v[10:17], v[222:229], v[106:109], v195, v195 op_sel_hi:[0,0,0]
	s_nop 3
	s_setprio 0
	s_setprio 2
	v_mfma_scale_f32_16x16x128_f8f6f4 v[150:153], v[18:25], v[198:205], v[150:153], v195, v195 op_sel_hi:[0,0,0]
	v_mfma_scale_f32_16x16x128_f8f6f4 v[146:149], v[26:33], v[198:205], v[146:149], v195, v195 op_sel_hi:[0,0,0]
	v_mfma_scale_f32_16x16x128_f8f6f4 v[134:137], v[18:25], v[206:213], v[134:137], v195, v195 op_sel_hi:[0,0,0]
	v_mfma_scale_f32_16x16x128_f8f6f4 v[130:133], v[26:33], v[206:213], v[130:133], v195, v195 op_sel_hi:[0,0,0]
	v_mfma_scale_f32_16x16x128_f8f6f4 v[118:121], v[18:25], v[214:221], v[118:121], v195, v195 op_sel_hi:[0,0,0]
	v_mfma_scale_f32_16x16x128_f8f6f4 v[114:117], v[26:33], v[214:221], v[114:117], v195, v195 op_sel_hi:[0,0,0]
	v_mfma_scale_f32_16x16x128_f8f6f4 v[102:105], v[18:25], v[222:229], v[102:105], v195, v195 op_sel_hi:[0,0,0]
	v_mfma_scale_f32_16x16x128_f8f6f4 v[98:101], v[26:33], v[222:229], v[98:101], v195, v195 op_sel_hi:[0,0,0]
	s_nop 3
	s_setprio 0
	s_add_u32 s28, s28, 0x8000
	s_addc_u32 s29, s29, 0
	s_add_i32 s30, s75, s47
	v_lshl_add_u64 v[230:231], s[28:29], 0, v[164:165]
	s_mov_b32 m0, s30
	ds_read_b128 v[198:201], v194 offset:49152
	ds_read_b128 v[202:205], v194 offset:50176
	ds_read_b128 v[206:209], v194 offset:51200
	ds_read_b128 v[210:213], v194 offset:52224
	ds_read_b128 v[214:217], v194 offset:53248
	ds_read_b128 v[218:221], v194 offset:54272
	ds_read_b128 v[222:225], v194 offset:55296
	ds_read_b128 v[226:229], v194 offset:56320
	global_load_lds_dwordx4 v[230:231], off
	v_lshl_add_u64 v[230:231], s[28:29], 0, v[166:167]
	s_add_i32 m0, s30, 0x2000
	s_add_i32 s30, s76, s47
	global_load_lds_dwordx4 v[230:231], off
	v_lshl_add_u64 v[230:231], s[28:29], 0, v[168:169]
	s_mov_b32 m0, s30
	s_nop 0
	global_load_lds_dwordx4 v[230:231], off
	v_lshl_add_u64 v[230:231], s[28:29], 0, v[172:173]
	s_add_i32 m0, s30, 0x2000
	s_nop 0
	global_load_lds_dwordx4 v[230:231], off
	v_lshl_add_u64 v[230:231], s[26:27], 0, v[174:175]
	s_mov_b32 m0, s60
	s_nop 0
	global_load_lds_dwordx4 v[230:231], off
	v_lshl_add_u64 v[230:231], s[26:27], 0, v[176:177]
	s_mov_b32 m0, s61
	s_nop 0
	global_load_lds_dwordx4 v[230:231], off
	s_waitcnt vmcnt(8)
	s_waitcnt lgkmcnt(0)
	s_barrier
	s_setprio 2
	s_waitcnt lgkmcnt(0)
	v_mfma_scale_f32_16x16x128_f8f6f4 v[94:97], v[2:9], v[198:205], v[94:97], v195, v195 op_sel_hi:[0,0,0]
	v_mfma_scale_f32_16x16x128_f8f6f4 v[90:93], v[10:17], v[198:205], v[90:93], v195, v195 op_sel_hi:[0,0,0]
	v_mfma_scale_f32_16x16x128_f8f6f4 v[78:81], v[2:9], v[206:213], v[78:81], v195, v195 op_sel_hi:[0,0,0]
	v_mfma_scale_f32_16x16x128_f8f6f4 v[74:77], v[10:17], v[206:213], v[74:77], v195, v195 op_sel_hi:[0,0,0]
	v_mfma_scale_f32_16x16x128_f8f6f4 v[62:65], v[2:9], v[214:221], v[62:65], v195, v195 op_sel_hi:[0,0,0]
	v_mfma_scale_f32_16x16x128_f8f6f4 v[58:61], v[10:17], v[214:221], v[58:61], v195, v195 op_sel_hi:[0,0,0]
	v_mfma_scale_f32_16x16x128_f8f6f4 v[46:49], v[2:9], v[222:229], v[46:49], v195, v195 op_sel_hi:[0,0,0]
	v_mfma_scale_f32_16x16x128_f8f6f4 v[42:45], v[10:17], v[222:229], v[42:45], v195, v195 op_sel_hi:[0,0,0]
	s_nop 3
	s_setprio 0
	s_setprio 2
	v_mfma_scale_f32_16x16x128_f8f6f4 v[86:89], v[18:25], v[198:205], v[86:89], v195, v195 op_sel_hi:[0,0,0]
	v_mfma_scale_f32_16x16x128_f8f6f4 v[82:85], v[26:33], v[198:205], v[82:85], v195, v195 op_sel_hi:[0,0,0]
	v_mfma_scale_f32_16x16x128_f8f6f4 v[70:73], v[18:25], v[206:213], v[70:73], v195, v195 op_sel_hi:[0,0,0]
	v_mfma_scale_f32_16x16x128_f8f6f4 v[66:69], v[26:33], v[206:213], v[66:69], v195, v195 op_sel_hi:[0,0,0]
	v_mfma_scale_f32_16x16x128_f8f6f4 v[54:57], v[18:25], v[214:221], v[54:57], v195, v195 op_sel_hi:[0,0,0]
	v_mfma_scale_f32_16x16x128_f8f6f4 v[50:53], v[26:33], v[214:221], v[50:53], v195, v195 op_sel_hi:[0,0,0]
	v_mfma_scale_f32_16x16x128_f8f6f4 v[38:41], v[18:25], v[222:229], v[38:41], v195, v195 op_sel_hi:[0,0,0]
	v_mfma_scale_f32_16x16x128_f8f6f4 v[34:37], v[26:33], v[222:229], v[34:37], v195, v195 op_sel_hi:[0,0,0]
	s_nop 3
	s_setprio 0
	s_add_i32 s74, s74, 2
	s_add_u32 s17, s17, 0x10000
	s_addc_u32 s19, s19, 0
	s_add_u32 s24, s24, 0x10000
	s_addc_u32 s25, s25, 0
	s_cmp_gt_u32 s74, 13
	s_cbranch_scc0 .Lh1_428

; __device__ __forceinline__ float fsigmoid(float x) { return __builtin_amdgcn_rcpf(1.0f + __builtin_amdgcn_exp2f(-1.44269504f * x)); }
; template <class Epi, class Sched, bool ALIGN_EPI = true, bool F8 = false>
; __device__ __forceinline__ void gemm_phase(PG8_LAS unsigned char* lds, const Sched& S, const Epi& E) {
;     ...
;         if constexpr (F8) {
; #pragma unroll
;             for (int a = 0; a < 2; ++a)
; #pragma unroll
;                 for (int b = 0; b < 2; ++b)
;                     asm volatile("s_nop 15\n\ts_nop 7" : "+v"(acc[a][b][0][0]), "+v"(acc[a][b][0][1]), "+v"(acc[a][b][1][0]), "+v"(acc[a][b][1][1]), "+v"(acc[a][b][2][0]), "+v"(acc[a][b][2][1]), "+v"(acc[a][b][3][0]), "+v"(acc[a][b][3][1]));
;     __device__ __forceinline__ void operator()(AccRef acc, const GUnit& u, int wr, int wc, int fr, int fq) const {
;         const int pm = u.x0, pn = u.x1; unsigned char* base = (pn < 8 ? GZF : GZS) + (size_t)(pm * 256 + wr * 64 + fr) * D + (pn & 7) * 256 + wc * 64 + 16 * fq;
; #pragma unroll
;         for (int ai = 0; ai < 2; ++ai)
; #pragma unroll
;             for (int m = 0; m < 4; ++m) { u32x4 w;
; #pragma unroll
;                 for (int bj = 0; bj < 2; ++bj)
; #pragma unroll
;                     for (int n = 0; n < 2; ++n) { const f32x4 v = acc[ai][bj][m][n]; w[bj * 2 + n] = pk4_u8(fsigmoid(v[0] * W8_INV), fsigmoid(v[1] * W8_INV), fsigmoid(v[2] * W8_INV), fsigmoid(v[3] * W8_INV)); }
;                 *(u32x4*)(base + (size_t)(ai * 128 + m * 16) * D) = w; }
;     }
.LBB0_431:
	s_nop 15
	s_nop 7
	v_lshl_add_u32 v2, s8, 8, v190
	v_mul_f32_e32 v4, 0x3c800000, v158
	v_mul_f32_e32 v5, 0x3c800000, v159
	v_mul_f32_e32 v6, 0x3c800000, v160
	v_mul_f32_e32 v7, 0x3c800000, v161
	v_mul_f32_e32 v4, 0xbfb8aa3b, v4
	v_mul_f32_e32 v5, 0xbfb8aa3b, v5
	v_mul_f32_e32 v6, 0xbfb8aa3b, v6
	v_mul_f32_e32 v7, 0xbfb8aa3b, v7
	v_exp_f32_e32 v4, v4
	v_exp_f32_e32 v5, v5
	v_exp_f32_e32 v6, v6
	v_exp_f32_e32 v7, v7
	v_add_f32_e32 v4, 1.0, v4
	v_add_f32_e32 v5, 1.0, v5
	v_add_f32_e32 v6, 1.0, v6
	v_add_f32_e32 v7, 1.0, v7
	v_rcp_f32_e32 v4, v4
	v_rcp_f32_e32 v5, v5
	v_rcp_f32_e32 v6, v6
	v_rcp_f32_e32 v7, v7
	v_fmamk_f32 v4, v4, 0x437f0000, v196
	v_fmamk_f32 v5, v5, 0x437f0000, v196
	v_fmamk_f32 v6, v6, 0x437f0000, v196
	v_fmamk_f32 v7, v7, 0x437f0000, v196
	v_perm_b32 v4, v5, v4, s67
	v_perm_b32 v5, v7, v6, s67
	v_mul_f32_e32 v6, 0x3c800000, v154
	v_mul_f32_e32 v7, 0x3c800000, v155
	v_mul_f32_e32 v6, 0xbfb8aa3b, v6
	v_mul_f32_e32 v7, 0xbfb8aa3b, v7
	v_exp_f32_e32 v6, v6
	v_exp_f32_e32 v7, v7
	v_perm_b32 v4, v5, v4, s68
	v_mul_f32_e32 v8, 0x3c800000, v157
	v_add_f32_e32 v5, 1.0, v6
	v_add_f32_e32 v6, 1.0, v7
	v_mul_f32_e32 v7, 0x3c800000, v156
	v_mul_f32_e32 v7, 0xbfb8aa3b, v7
	v_mul_f32_e32 v8, 0xbfb8aa3b, v8
	v_exp_f32_e32 v7, v7
	v_exp_f32_e32 v8, v8
	v_rcp_f32_e32 v5, v5
	v_rcp_f32_e32 v6, v6
	v_add_f32_e32 v7, 1.0, v7
	v_add_f32_e32 v8, 1.0, v8
	v_rcp_f32_e32 v7, v7
	v_rcp_f32_e32 v8, v8
	v_fmamk_f32 v5, v5, 0x437f0000, v196
	v_fmamk_f32 v6, v6, 0x437f0000, v196
	v_fmamk_f32 v7, v7, 0x437f0000, v196
	v_fmamk_f32 v8, v8, 0x437f0000, v196
	v_perm_b32 v5, v6, v5, s67
	v_perm_b32 v6, v8, v7, s67
	v_mul_f32_e32 v7, 0x3c800000, v150
	v_mul_f32_e32 v8, 0x3c800000, v151
	v_mul_f32_e32 v7, 0xbfb8aa3b, v7
	v_mul_f32_e32 v8, 0xbfb8aa3b, v8
	v_exp_f32_e32 v7, v7
	v_exp_f32_e32 v8, v8
	v_perm_b32 v5, v6, v5, s68
	v_mul_f32_e32 v9, 0x3c800000, v153
	v_add_f32_e32 v6, 1.0, v7
	v_add_f32_e32 v7, 1.0, v8
	v_mul_f32_e32 v8, 0x3c800000, v152
	v_mul_f32_e32 v8, 0xbfb8aa3b, v8
	v_mul_f32_e32 v9, 0xbfb8aa3b, v9
	v_exp_f32_e32 v8, v8
	v_exp_f32_e32 v9, v9
	v_rcp_f32_e32 v6, v6
	v_rcp_f32_e32 v7, v7
	v_add_f32_e32 v8, 1.0, v8
	v_add_f32_e32 v9, 1.0, v9
	v_rcp_f32_e32 v8, v8
	v_rcp_f32_e32 v9, v9
	v_fmamk_f32 v6, v6, 0x437f0000, v196
	v_fmamk_f32 v7, v7, 0x437f0000, v196
	v_fmamk_f32 v8, v8, 0x437f0000, v196
	v_fmamk_f32 v9, v9, 0x437f0000, v196
	v_perm_b32 v6, v7, v6, s67
	v_perm_b32 v7, v9, v8, s67
	v_mul_f32_e32 v8, 0x3c800000, v146
	v_mul_f32_e32 v9, 0x3c800000, v147
	v_mul_f32_e32 v8, 0xbfb8aa3b, v8
	v_mul_f32_e32 v9, 0xbfb8aa3b, v9
	v_exp_f32_e32 v8, v8
	v_exp_f32_e32 v9, v9
	v_perm_b32 v6, v7, v6, s68
	v_mul_f32_e32 v10, 0x3c800000, v149
	v_add_f32_e32 v7, 1.0, v8
	v_add_f32_e32 v8, 1.0, v9
	v_mul_f32_e32 v9, 0x3c800000, v148
	v_mul_f32_e32 v9, 0xbfb8aa3b, v9
	v_mul_f32_e32 v10, 0xbfb8aa3b, v10
	v_exp_f32_e32 v9, v9
	v_exp_f32_e32 v10, v10
	v_rcp_f32_e32 v7, v7
	v_rcp_f32_e32 v8, v8
	v_add_f32_e32 v9, 1.0, v9
	v_add_f32_e32 v10, 1.0, v10
	v_rcp_f32_e32 v9, v9
	v_rcp_f32_e32 v10, v10
	s_cmp_lt_i32 s73, 8
	v_ashrrev_i32_e32 v3, 31, v2
	s_cselect_b32 s25, s41, s59
	s_cselect_b32 s24, s40, s53
	v_lshlrev_b64 v[2:3], 11, v[2:3]
	s_lshl_b32 s8, s73, 8
	v_lshl_add_u64 v[2:3], s[24:25], 0, v[2:3]
	s_and_b32 s8, s8, 0x700
	v_lshl_add_u64 v[2:3], v[2:3], 0, s[8:9]
	v_fmamk_f32 v7, v7, 0x437f0000, v196
	v_fmamk_f32 v8, v8, 0x437f0000, v196
	v_fmamk_f32 v9, v9, 0x437f0000, v196
	v_fmamk_f32 v10, v10, 0x437f0000, v196
	v_lshl_add_u64 v[2:3], v[2:3], 0, s[14:15]
	v_perm_b32 v7, v8, v7, s67
	v_perm_b32 v8, v10, v9, s67
	v_lshl_add_u64 v[2:3], v[2:3], 0, v[162:163]
	v_perm_b32 v7, v8, v7, s68
	v_mul_f32_e32 v8, 0x3c800000, v142
	v_mul_f32_e32 v9, 0x3c800000, v143
	flat_store_dwordx4 v[2:3], v[4:7]
	v_mul_f32_e32 v8, 0xbfb8aa3b, v8
	v_mul_f32_e32 v9, 0xbfb8aa3b, v9
	v_mul_f32_e32 v6, 0x3c800000, v144
	v_mul_f32_e32 v7, 0x3c800000, v145
	v_mul_f32_e32 v6, 0xbfb8aa3b, v6
	v_mul_f32_e32 v7, 0xbfb8aa3b, v7
	v_exp_f32_e32 v8, v8
	v_exp_f32_e32 v9, v9
	v_exp_f32_e32 v6, v6
	v_exp_f32_e32 v7, v7
	v_add_f32_e32 v4, 1.0, v8
	v_add_f32_e32 v5, 1.0, v9
	v_add_f32_e32 v6, 1.0, v6
	v_add_f32_e32 v7, 1.0, v7
	v_rcp_f32_e32 v4, v4
	v_rcp_f32_e32 v5, v5
	v_rcp_f32_e32 v6, v6
	v_rcp_f32_e32 v7, v7
	v_fmamk_f32 v4, v4, 0x437f0000, v196
	v_fmamk_f32 v5, v5, 0x437f0000, v196
	v_fmamk_f32 v6, v6, 0x437f0000, v196
	v_fmamk_f32 v7, v7, 0x437f0000, v196
	v_perm_b32 v4, v5, v4, s67
	v_perm_b32 v5, v7, v6, s67
	v_mul_f32_e32 v6, 0x3c800000, v138
	v_mul_f32_e32 v7, 0x3c800000, v139
	v_mul_f32_e32 v6, 0xbfb8aa3b, v6
	v_mul_f32_e32 v7, 0xbfb8aa3b, v7
	v_exp_f32_e32 v6, v6
	v_exp_f32_e32 v7, v7
	v_perm_b32 v4, v5, v4, s68
	v_mul_f32_e32 v8, 0x3c800000, v141
	v_add_f32_e32 v5, 1.0, v6
	v_add_f32_e32 v6, 1.0, v7
	v_mul_f32_e32 v7, 0x3c800000, v140
	v_mul_f32_e32 v7, 0xbfb8aa3b, v7
	v_mul_f32_e32 v8, 0xbfb8aa3b, v8
	v_exp_f32_e32 v7, v7
	v_exp_f32_e32 v8, v8
	v_rcp_f32_e32 v5, v5
	v_rcp_f32_e32 v6, v6
	v_add_f32_e32 v7, 1.0, v7
	v_add_f32_e32 v8, 1.0, v8
	v_rcp_f32_e32 v7, v7
	v_rcp_f32_e32 v8, v8
	v_fmamk_f32 v5, v5, 0x437f0000, v196
	v_fmamk_f32 v6, v6, 0x437f0000, v196
	v_fmamk_f32 v7, v7, 0x437f0000, v196
	v_fmamk_f32 v8, v8, 0x437f0000, v196
	v_perm_b32 v5, v6, v5, s67
	v_perm_b32 v6, v8, v7, s67
	v_mul_f32_e32 v7, 0x3c800000, v134
	v_mul_f32_e32 v8, 0x3c800000, v135
	v_mul_f32_e32 v7, 0xbfb8aa3b, v7
	v_mul_f32_e32 v8, 0xbfb8aa3b, v8
	v_exp_f32_e32 v7, v7
	v_exp_f32_e32 v8, v8
	v_perm_b32 v5, v6, v5, s68
	v_mul_f32_e32 v9, 0x3c800000, v137
	v_add_f32_e32 v6, 1.0, v7
	v_add_f32_e32 v7, 1.0, v8
	v_mul_f32_e32 v8, 0x3c800000, v136
	v_mul_f32_e32 v8, 0xbfb8aa3b, v8
	v_mul_f32_e32 v9, 0xbfb8aa3b, v9
; __device__ __forceinline__ float fsigmoid(float x) { return __builtin_amdgcn_rcpf(1.0f + __builtin_amdgcn_exp2f(-1.44269504f * x)); }
;     __device__ __forceinline__ void operator()(AccRef acc, const GUnit& u, int wr, int wc, int fr, int fq) const {
;         const int pm = u.x0, pn = u.x1; unsigned char* base = (pn < 8 ? GZF : GZS) + (size_t)(pm * 256 + wr * 64 + fr) * D + (pn & 7) * 256 + wc * 64 + 16 * fq;
; #pragma unroll
;         for (int ai = 0; ai < 2; ++ai)
; #pragma unroll
;             for (int m = 0; m < 4; ++m) { u32x4 w;
; #pragma unroll
;                 for (int bj = 0; bj < 2; ++bj)
; #pragma unroll
;                     for (int n = 0; n < 2; ++n) { const f32x4 v = acc[ai][bj][m][n]; w[bj * 2 + n] = pk4_u8(fsigmoid(v[0] * W8_INV), fsigmoid(v[1] * W8_INV), fsigmoid(v[2] * W8_INV), fsigmoid(v[3] * W8_INV)); }
;                 *(u32x4*)(base + (size_t)(ai * 128 + m * 16) * D) = w; }
	v_exp_f32_e32 v8, v8
	v_exp_f32_e32 v9, v9
	v_rcp_f32_e32 v6, v6
	v_rcp_f32_e32 v7, v7
	v_add_f32_e32 v8, 1.0, v8
	v_add_f32_e32 v9, 1.0, v9
	v_rcp_f32_e32 v8, v8
	v_rcp_f32_e32 v9, v9
	v_fmamk_f32 v6, v6, 0x437f0000, v196
	v_fmamk_f32 v7, v7, 0x437f0000, v196
	v_fmamk_f32 v8, v8, 0x437f0000, v196
	v_fmamk_f32 v9, v9, 0x437f0000, v196
	v_perm_b32 v6, v7, v6, s67
	v_perm_b32 v7, v9, v8, s67
	v_mul_f32_e32 v8, 0x3c800000, v130
	v_mul_f32_e32 v9, 0x3c800000, v131
	v_mul_f32_e32 v8, 0xbfb8aa3b, v8
	v_mul_f32_e32 v9, 0xbfb8aa3b, v9
	v_exp_f32_e32 v8, v8
	v_exp_f32_e32 v9, v9
	v_perm_b32 v6, v7, v6, s68
	v_mul_f32_e32 v10, 0x3c800000, v133
	v_add_f32_e32 v7, 1.0, v8
	v_add_f32_e32 v8, 1.0, v9
	v_mul_f32_e32 v9, 0x3c800000, v132
	v_mul_f32_e32 v9, 0xbfb8aa3b, v9
	v_mul_f32_e32 v10, 0xbfb8aa3b, v10
	v_exp_f32_e32 v9, v9
	v_exp_f32_e32 v10, v10
	v_rcp_f32_e32 v7, v7
	v_rcp_f32_e32 v8, v8
	v_add_f32_e32 v9, 1.0, v9
	v_add_f32_e32 v10, 1.0, v10
	v_rcp_f32_e32 v9, v9
	v_rcp_f32_e32 v10, v10
	v_fmamk_f32 v7, v7, 0x437f0000, v196
	v_fmamk_f32 v8, v8, 0x437f0000, v196
	v_fmamk_f32 v9, v9, 0x437f0000, v196
	v_fmamk_f32 v10, v10, 0x437f0000, v196
	v_perm_b32 v7, v8, v7, s67
	v_perm_b32 v8, v10, v9, s67
	v_perm_b32 v7, v8, v7, s68
	v_add_co_u32_e32 v8, vcc, s63, v2
	v_mul_f32_e32 v10, 0x3c800000, v126
	s_nop 0
	v_addc_co_u32_e32 v9, vcc, 0, v3, vcc
	v_mul_f32_e32 v11, 0x3c800000, v127
	flat_store_dwordx4 v[8:9], v[4:7]
	v_mul_f32_e32 v10, 0xbfb8aa3b, v10
	v_mul_f32_e32 v11, 0xbfb8aa3b, v11
	v_mul_f32_e32 v6, 0x3c800000, v128
	v_mul_f32_e32 v7, 0x3c800000, v129
	v_mul_f32_e32 v6, 0xbfb8aa3b, v6
	v_mul_f32_e32 v7, 0xbfb8aa3b, v7
	v_exp_f32_e32 v10, v10
	v_exp_f32_e32 v11, v11
	v_exp_f32_e32 v6, v6
	v_exp_f32_e32 v7, v7
	v_add_f32_e32 v4, 1.0, v10
	v_add_f32_e32 v5, 1.0, v11
	v_add_f32_e32 v6, 1.0, v6
	v_add_f32_e32 v7, 1.0, v7
	v_rcp_f32_e32 v4, v4
	v_rcp_f32_e32 v5, v5
	v_rcp_f32_e32 v6, v6
	v_rcp_f32_e32 v7, v7
	v_fmamk_f32 v4, v4, 0x437f0000, v196
	v_fmamk_f32 v5, v5, 0x437f0000, v196
	v_fmamk_f32 v6, v6, 0x437f0000, v196
	v_fmamk_f32 v7, v7, 0x437f0000, v196
	v_perm_b32 v4, v5, v4, s67
	v_perm_b32 v5, v7, v6, s67
	v_mul_f32_e32 v6, 0x3c800000, v122
	v_mul_f32_e32 v7, 0x3c800000, v123
	v_mul_f32_e32 v6, 0xbfb8aa3b, v6
	v_mul_f32_e32 v7, 0xbfb8aa3b, v7
	v_exp_f32_e32 v6, v6
	v_exp_f32_e32 v7, v7
	v_perm_b32 v4, v5, v4, s68
	v_mul_f32_e32 v8, 0x3c800000, v125
	v_add_f32_e32 v5, 1.0, v6
	v_add_f32_e32 v6, 1.0, v7
	v_mul_f32_e32 v7, 0x3c800000, v124
	v_mul_f32_e32 v7, 0xbfb8aa3b, v7
	v_mul_f32_e32 v8, 0xbfb8aa3b, v8
	v_exp_f32_e32 v7, v7
	v_exp_f32_e32 v8, v8
	v_rcp_f32_e32 v5, v5
	v_rcp_f32_e32 v6, v6
	v_add_f32_e32 v7, 1.0, v7
	v_add_f32_e32 v8, 1.0, v8
	v_rcp_f32_e32 v7, v7
	v_rcp_f32_e32 v8, v8
	v_fmamk_f32 v5, v5, 0x437f0000, v196
	v_fmamk_f32 v6, v6, 0x437f0000, v196
	v_fmamk_f32 v7, v7, 0x437f0000, v196
	v_fmamk_f32 v8, v8, 0x437f0000, v196
	v_perm_b32 v5, v6, v5, s67
	v_perm_b32 v6, v8, v7, s67
	v_mul_f32_e32 v7, 0x3c800000, v118
	v_mul_f32_e32 v8, 0x3c800000, v119
	v_mul_f32_e32 v7, 0xbfb8aa3b, v7
	v_mul_f32_e32 v8, 0xbfb8aa3b, v8
	v_exp_f32_e32 v7, v7
	v_exp_f32_e32 v8, v8
	v_perm_b32 v5, v6, v5, s68
	v_mul_f32_e32 v9, 0x3c800000, v121
	v_add_f32_e32 v6, 1.0, v7
	v_add_f32_e32 v7, 1.0, v8
	v_mul_f32_e32 v8, 0x3c800000, v120
	v_mul_f32_e32 v8, 0xbfb8aa3b, v8
	v_mul_f32_e32 v9, 0xbfb8aa3b, v9
	v_exp_f32_e32 v8, v8
	v_exp_f32_e32 v9, v9
	v_rcp_f32_e32 v6, v6
	v_rcp_f32_e32 v7, v7
	v_add_f32_e32 v8, 1.0, v8
	v_add_f32_e32 v9, 1.0, v9
	v_rcp_f32_e32 v8, v8
	v_rcp_f32_e32 v9, v9
	v_fmamk_f32 v6, v6, 0x437f0000, v196
	v_fmamk_f32 v7, v7, 0x437f0000, v196
	v_fmamk_f32 v8, v8, 0x437f0000, v196
	v_fmamk_f32 v9, v9, 0x437f0000, v196
	v_perm_b32 v6, v7, v6, s67
	v_perm_b32 v7, v9, v8, s67
	v_mul_f32_e32 v8, 0x3c800000, v114
	v_mul_f32_e32 v9, 0x3c800000, v115
	v_mul_f32_e32 v8, 0xbfb8aa3b, v8
	v_mul_f32_e32 v9, 0xbfb8aa3b, v9
	v_exp_f32_e32 v8, v8
	v_exp_f32_e32 v9, v9
	v_perm_b32 v6, v7, v6, s68
	v_mul_f32_e32 v10, 0x3c800000, v117
	v_add_f32_e32 v7, 1.0, v8
	v_add_f32_e32 v8, 1.0, v9
	v_mul_f32_e32 v9, 0x3c800000, v116
	v_mul_f32_e32 v9, 0xbfb8aa3b, v9
	v_mul_f32_e32 v10, 0xbfb8aa3b, v10
	v_exp_f32_e32 v9, v9
	v_exp_f32_e32 v10, v10
	v_rcp_f32_e32 v7, v7
	v_rcp_f32_e32 v8, v8
	v_add_f32_e32 v9, 1.0, v9
	v_add_f32_e32 v10, 1.0, v10
	v_rcp_f32_e32 v9, v9
	v_rcp_f32_e32 v10, v10
	v_fmamk_f32 v7, v7, 0x437f0000, v196
	v_fmamk_f32 v8, v8, 0x437f0000, v196
	v_fmamk_f32 v9, v9, 0x437f0000, v196
	v_fmamk_f32 v10, v10, 0x437f0000, v196
	v_perm_b32 v7, v8, v7, s67
	v_perm_b32 v8, v10, v9, s67
	v_perm_b32 v7, v8, v7, s68
	v_add_co_u32_e32 v8, vcc, s52, v2
	v_mul_f32_e32 v10, 0x3c800000, v110
	s_nop 0
	v_addc_co_u32_e32 v9, vcc, 0, v3, vcc
	v_mul_f32_e32 v11, 0x3c800000, v111
	flat_store_dwordx4 v[8:9], v[4:7]
	v_mul_f32_e32 v10, 0xbfb8aa3b, v10
	v_mul_f32_e32 v11, 0xbfb8aa3b, v11
	v_mul_f32_e32 v6, 0x3c800000, v112
	v_mul_f32_e32 v7, 0x3c800000, v113
	v_mul_f32_e32 v6, 0xbfb8aa3b, v6
	v_mul_f32_e32 v7, 0xbfb8aa3b, v7
	v_exp_f32_e32 v10, v10
	v_exp_f32_e32 v11, v11
	v_exp_f32_e32 v6, v6
	v_exp_f32_e32 v7, v7
	v_add_f32_e32 v4, 1.0, v10
	v_add_f32_e32 v5, 1.0, v11
	v_add_f32_e32 v6, 1.0, v6
	v_add_f32_e32 v7, 1.0, v7
	v_rcp_f32_e32 v4, v4
	v_rcp_f32_e32 v5, v5
	v_rcp_f32_e32 v6, v6
	v_rcp_f32_e32 v7, v7
	v_fmamk_f32 v4, v4, 0x437f0000, v196
	v_fmamk_f32 v5, v5, 0x437f0000, v196
	v_fmamk_f32 v6, v6, 0x437f0000, v196
	v_fmamk_f32 v7, v7, 0x437f0000, v196
	v_perm_b32 v4, v5, v4, s67
	v_perm_b32 v5, v7, v6, s67
	v_mul_f32_e32 v6, 0x3c800000, v106
	v_mul_f32_e32 v7, 0x3c800000, v107
	v_mul_f32_e32 v6, 0xbfb8aa3b, v6
	v_mul_f32_e32 v7, 0xbfb8aa3b, v7
	v_exp_f32_e32 v6, v6
; __device__ __forceinline__ float fsigmoid(float x) { return __builtin_amdgcn_rcpf(1.0f + __builtin_amdgcn_exp2f(-1.44269504f * x)); }
;     __device__ __forceinline__ void operator()(AccRef acc, const GUnit& u, int wr, int wc, int fr, int fq) const {
;         const int pm = u.x0, pn = u.x1; unsigned char* base = (pn < 8 ? GZF : GZS) + (size_t)(pm * 256 + wr * 64 + fr) * D + (pn & 7) * 256 + wc * 64 + 16 * fq;
; #pragma unroll
;         for (int ai = 0; ai < 2; ++ai)
; #pragma unroll
;             for (int m = 0; m < 4; ++m) { u32x4 w;
; #pragma unroll
;                 for (int bj = 0; bj < 2; ++bj)
; #pragma unroll
;                     for (int n = 0; n < 2; ++n) { const f32x4 v = acc[ai][bj][m][n]; w[bj * 2 + n] = pk4_u8(fsigmoid(v[0] * W8_INV), fsigmoid(v[1] * W8_INV), fsigmoid(v[2] * W8_INV), fsigmoid(v[3] * W8_INV)); }
;                 *(u32x4*)(base + (size_t)(ai * 128 + m * 16) * D) = w; }
	v_exp_f32_e32 v7, v7
	v_perm_b32 v4, v5, v4, s68
	v_mul_f32_e32 v8, 0x3c800000, v109
	v_add_f32_e32 v5, 1.0, v6
	v_add_f32_e32 v6, 1.0, v7
	v_mul_f32_e32 v7, 0x3c800000, v108
	v_mul_f32_e32 v7, 0xbfb8aa3b, v7
	v_mul_f32_e32 v8, 0xbfb8aa3b, v8
	v_exp_f32_e32 v7, v7
	v_exp_f32_e32 v8, v8
	v_rcp_f32_e32 v5, v5
	v_rcp_f32_e32 v6, v6
	v_add_f32_e32 v7, 1.0, v7
	v_add_f32_e32 v8, 1.0, v8
	v_rcp_f32_e32 v7, v7
	v_rcp_f32_e32 v8, v8
	v_fmamk_f32 v5, v5, 0x437f0000, v196
	v_fmamk_f32 v6, v6, 0x437f0000, v196
	v_fmamk_f32 v7, v7, 0x437f0000, v196
	v_fmamk_f32 v8, v8, 0x437f0000, v196
	v_perm_b32 v5, v6, v5, s67
	v_perm_b32 v6, v8, v7, s67
	v_mul_f32_e32 v7, 0x3c800000, v102
	v_mul_f32_e32 v8, 0x3c800000, v103
	v_mul_f32_e32 v7, 0xbfb8aa3b, v7
	v_mul_f32_e32 v8, 0xbfb8aa3b, v8
	v_exp_f32_e32 v7, v7
	v_exp_f32_e32 v8, v8
	v_perm_b32 v5, v6, v5, s68
	v_mul_f32_e32 v9, 0x3c800000, v105
	v_add_f32_e32 v6, 1.0, v7
	v_add_f32_e32 v7, 1.0, v8
	v_mul_f32_e32 v8, 0x3c800000, v104
	v_mul_f32_e32 v8, 0xbfb8aa3b, v8
	v_mul_f32_e32 v9, 0xbfb8aa3b, v9
	v_exp_f32_e32 v8, v8
	v_exp_f32_e32 v9, v9
	v_rcp_f32_e32 v6, v6
	v_rcp_f32_e32 v7, v7
	v_add_f32_e32 v8, 1.0, v8
	v_add_f32_e32 v9, 1.0, v9
	v_rcp_f32_e32 v8, v8
	v_rcp_f32_e32 v9, v9
	v_fmamk_f32 v6, v6, 0x437f0000, v196
	v_fmamk_f32 v7, v7, 0x437f0000, v196
	v_fmamk_f32 v8, v8, 0x437f0000, v196
	v_fmamk_f32 v9, v9, 0x437f0000, v196
	v_perm_b32 v6, v7, v6, s67
	v_perm_b32 v7, v9, v8, s67
	v_mul_f32_e32 v8, 0x3c800000, v98
	v_mul_f32_e32 v9, 0x3c800000, v99
	v_mul_f32_e32 v8, 0xbfb8aa3b, v8
	v_mul_f32_e32 v9, 0xbfb8aa3b, v9
	v_exp_f32_e32 v8, v8
	v_exp_f32_e32 v9, v9
	v_perm_b32 v6, v7, v6, s68
	v_mul_f32_e32 v10, 0x3c800000, v101
	v_add_f32_e32 v7, 1.0, v8
	v_add_f32_e32 v8, 1.0, v9
	v_mul_f32_e32 v9, 0x3c800000, v100
	v_mul_f32_e32 v9, 0xbfb8aa3b, v9
	v_mul_f32_e32 v10, 0xbfb8aa3b, v10
	v_exp_f32_e32 v9, v9
	v_exp_f32_e32 v10, v10
	v_rcp_f32_e32 v7, v7
	v_rcp_f32_e32 v8, v8
	v_add_f32_e32 v9, 1.0, v9
	v_add_f32_e32 v10, 1.0, v10
	v_rcp_f32_e32 v9, v9
	v_rcp_f32_e32 v10, v10
	v_fmamk_f32 v7, v7, 0x437f0000, v196
	v_fmamk_f32 v8, v8, 0x437f0000, v196
	v_fmamk_f32 v9, v9, 0x437f0000, v196
	v_fmamk_f32 v10, v10, 0x437f0000, v196
	v_perm_b32 v7, v8, v7, s67
	v_perm_b32 v8, v10, v9, s67
	v_perm_b32 v7, v8, v7, s68
	v_add_co_u32_e32 v8, vcc, s62, v2
	v_mul_f32_e32 v10, 0x3c800000, v94
	s_nop 0
	v_addc_co_u32_e32 v9, vcc, 0, v3, vcc
	v_mul_f32_e32 v11, 0x3c800000, v95
	flat_store_dwordx4 v[8:9], v[4:7]
	v_mul_f32_e32 v10, 0xbfb8aa3b, v10
	v_mul_f32_e32 v11, 0xbfb8aa3b, v11
	v_mul_f32_e32 v6, 0x3c800000, v96
	v_mul_f32_e32 v7, 0x3c800000, v97
	v_mul_f32_e32 v6, 0xbfb8aa3b, v6
	v_mul_f32_e32 v7, 0xbfb8aa3b, v7
	v_exp_f32_e32 v10, v10
	v_exp_f32_e32 v11, v11
	v_exp_f32_e32 v6, v6
	v_exp_f32_e32 v7, v7
	v_add_f32_e32 v4, 1.0, v10
	v_add_f32_e32 v5, 1.0, v11
	v_add_f32_e32 v6, 1.0, v6
	v_add_f32_e32 v7, 1.0, v7
	v_rcp_f32_e32 v4, v4
	v_rcp_f32_e32 v5, v5
	v_rcp_f32_e32 v6, v6
	v_rcp_f32_e32 v7, v7
	v_fmamk_f32 v4, v4, 0x437f0000, v196
	v_fmamk_f32 v5, v5, 0x437f0000, v196
	v_fmamk_f32 v6, v6, 0x437f0000, v196
	v_fmamk_f32 v7, v7, 0x437f0000, v196
	v_perm_b32 v4, v5, v4, s67
	v_perm_b32 v5, v7, v6, s67
	v_mul_f32_e32 v6, 0x3c800000, v90
	v_mul_f32_e32 v7, 0x3c800000, v91
	v_mul_f32_e32 v6, 0xbfb8aa3b, v6
	v_mul_f32_e32 v7, 0xbfb8aa3b, v7
	v_exp_f32_e32 v6, v6
	v_exp_f32_e32 v7, v7
	v_perm_b32 v4, v5, v4, s68
	v_mul_f32_e32 v8, 0x3c800000, v93
	v_add_f32_e32 v5, 1.0, v6
	v_add_f32_e32 v6, 1.0, v7
	v_mul_f32_e32 v7, 0x3c800000, v92
	v_mul_f32_e32 v7, 0xbfb8aa3b, v7
	v_mul_f32_e32 v8, 0xbfb8aa3b, v8
	v_exp_f32_e32 v7, v7
	v_exp_f32_e32 v8, v8
	v_rcp_f32_e32 v5, v5
	v_rcp_f32_e32 v6, v6
	v_add_f32_e32 v7, 1.0, v7
	v_add_f32_e32 v8, 1.0, v8
	v_rcp_f32_e32 v7, v7
	v_rcp_f32_e32 v8, v8
	v_fmamk_f32 v5, v5, 0x437f0000, v196
	v_fmamk_f32 v6, v6, 0x437f0000, v196
	v_fmamk_f32 v7, v7, 0x437f0000, v196
	v_fmamk_f32 v8, v8, 0x437f0000, v196
	v_perm_b32 v5, v6, v5, s67
	v_perm_b32 v6, v8, v7, s67
	v_mul_f32_e32 v7, 0x3c800000, v86
	v_mul_f32_e32 v8, 0x3c800000, v87
	v_mul_f32_e32 v7, 0xbfb8aa3b, v7
	v_mul_f32_e32 v8, 0xbfb8aa3b, v8
	v_exp_f32_e32 v7, v7
	v_exp_f32_e32 v8, v8
	v_perm_b32 v5, v6, v5, s68
	v_mul_f32_e32 v9, 0x3c800000, v89
	v_add_f32_e32 v6, 1.0, v7
	v_add_f32_e32 v7, 1.0, v8
	v_mul_f32_e32 v8, 0x3c800000, v88
	v_mul_f32_e32 v8, 0xbfb8aa3b, v8
	v_mul_f32_e32 v9, 0xbfb8aa3b, v9
	v_exp_f32_e32 v8, v8
	v_exp_f32_e32 v9, v9
	v_rcp_f32_e32 v6, v6
	v_rcp_f32_e32 v7, v7
	v_add_f32_e32 v8, 1.0, v8
	v_add_f32_e32 v9, 1.0, v9
	v_rcp_f32_e32 v8, v8
	v_rcp_f32_e32 v9, v9
	v_fmamk_f32 v6, v6, 0x437f0000, v196
	v_fmamk_f32 v7, v7, 0x437f0000, v196
	v_fmamk_f32 v8, v8, 0x437f0000, v196
	v_fmamk_f32 v9, v9, 0x437f0000, v196
	v_perm_b32 v6, v7, v6, s67
	v_perm_b32 v7, v9, v8, s67
	v_mul_f32_e32 v8, 0x3c800000, v82
	v_mul_f32_e32 v9, 0x3c800000, v83
	v_mul_f32_e32 v8, 0xbfb8aa3b, v8
	v_mul_f32_e32 v9, 0xbfb8aa3b, v9
	v_exp_f32_e32 v8, v8
	v_exp_f32_e32 v9, v9
	v_perm_b32 v6, v7, v6, s68
	v_mul_f32_e32 v10, 0x3c800000, v85
	v_add_f32_e32 v7, 1.0, v8
	v_add_f32_e32 v8, 1.0, v9
	v_mul_f32_e32 v9, 0x3c800000, v84
	v_mul_f32_e32 v9, 0xbfb8aa3b, v9
	v_mul_f32_e32 v10, 0xbfb8aa3b, v10
	v_exp_f32_e32 v9, v9
	v_exp_f32_e32 v10, v10
	v_rcp_f32_e32 v7, v7
	v_rcp_f32_e32 v8, v8
	v_add_f32_e32 v9, 1.0, v9
	v_add_f32_e32 v10, 1.0, v10
	v_rcp_f32_e32 v9, v9
	v_rcp_f32_e32 v10, v10
	v_fmamk_f32 v7, v7, 0x437f0000, v196
	v_fmamk_f32 v8, v8, 0x437f0000, v196
	v_fmamk_f32 v9, v9, 0x437f0000, v196
	v_fmamk_f32 v10, v10, 0x437f0000, v196
	v_perm_b32 v7, v8, v7, s67
	v_perm_b32 v8, v10, v9, s67
	v_perm_b32 v7, v8, v7, s68
	v_add_co_u32_e32 v8, vcc, s69, v2
; __device__ __forceinline__ float fsigmoid(float x) { return __builtin_amdgcn_rcpf(1.0f + __builtin_amdgcn_exp2f(-1.44269504f * x)); }
;     __device__ __forceinline__ void operator()(AccRef acc, const GUnit& u, int wr, int wc, int fr, int fq) const {
;         const int pm = u.x0, pn = u.x1; unsigned char* base = (pn < 8 ? GZF : GZS) + (size_t)(pm * 256 + wr * 64 + fr) * D + (pn & 7) * 256 + wc * 64 + 16 * fq;
; #pragma unroll
;         for (int ai = 0; ai < 2; ++ai)
; #pragma unroll
;             for (int m = 0; m < 4; ++m) { u32x4 w;
; #pragma unroll
;                 for (int bj = 0; bj < 2; ++bj)
; #pragma unroll
;                     for (int n = 0; n < 2; ++n) { const f32x4 v = acc[ai][bj][m][n]; w[bj * 2 + n] = pk4_u8(fsigmoid(v[0] * W8_INV), fsigmoid(v[1] * W8_INV), fsigmoid(v[2] * W8_INV), fsigmoid(v[3] * W8_INV)); }
;                 *(u32x4*)(base + (size_t)(ai * 128 + m * 16) * D) = w; }
	v_mul_f32_e32 v10, 0x3c800000, v78
	s_nop 0
	v_addc_co_u32_e32 v9, vcc, 0, v3, vcc
	v_mul_f32_e32 v11, 0x3c800000, v79
	flat_store_dwordx4 v[8:9], v[4:7]
	v_mul_f32_e32 v10, 0xbfb8aa3b, v10
	v_mul_f32_e32 v11, 0xbfb8aa3b, v11
	v_mul_f32_e32 v6, 0x3c800000, v80
	v_mul_f32_e32 v7, 0x3c800000, v81
	v_mul_f32_e32 v6, 0xbfb8aa3b, v6
	v_mul_f32_e32 v7, 0xbfb8aa3b, v7
	v_exp_f32_e32 v10, v10
	v_exp_f32_e32 v11, v11
	v_exp_f32_e32 v6, v6
	v_exp_f32_e32 v7, v7
	v_add_f32_e32 v4, 1.0, v10
	v_add_f32_e32 v5, 1.0, v11
	v_add_f32_e32 v6, 1.0, v6
	v_add_f32_e32 v7, 1.0, v7
	v_rcp_f32_e32 v4, v4
	v_rcp_f32_e32 v5, v5
	v_rcp_f32_e32 v6, v6
	v_rcp_f32_e32 v7, v7
	v_fmamk_f32 v4, v4, 0x437f0000, v196
	v_fmamk_f32 v5, v5, 0x437f0000, v196
	v_fmamk_f32 v6, v6, 0x437f0000, v196
	v_fmamk_f32 v7, v7, 0x437f0000, v196
	v_perm_b32 v4, v5, v4, s67
	v_perm_b32 v5, v7, v6, s67
	v_mul_f32_e32 v6, 0x3c800000, v74
	v_mul_f32_e32 v7, 0x3c800000, v75
	v_mul_f32_e32 v6, 0xbfb8aa3b, v6
	v_mul_f32_e32 v7, 0xbfb8aa3b, v7
	v_exp_f32_e32 v6, v6
	v_exp_f32_e32 v7, v7
	v_perm_b32 v4, v5, v4, s68
	v_mul_f32_e32 v8, 0x3c800000, v77
	v_add_f32_e32 v5, 1.0, v6
	v_add_f32_e32 v6, 1.0, v7
	v_mul_f32_e32 v7, 0x3c800000, v76
	v_mul_f32_e32 v7, 0xbfb8aa3b, v7
	v_mul_f32_e32 v8, 0xbfb8aa3b, v8
	v_exp_f32_e32 v7, v7
	v_exp_f32_e32 v8, v8
	v_rcp_f32_e32 v5, v5
	v_rcp_f32_e32 v6, v6
	v_add_f32_e32 v7, 1.0, v7
	v_add_f32_e32 v8, 1.0, v8
	v_rcp_f32_e32 v7, v7
	v_rcp_f32_e32 v8, v8
	v_fmamk_f32 v5, v5, 0x437f0000, v196
	v_fmamk_f32 v6, v6, 0x437f0000, v196
	v_fmamk_f32 v7, v7, 0x437f0000, v196
	v_fmamk_f32 v8, v8, 0x437f0000, v196
	v_perm_b32 v5, v6, v5, s67
	v_perm_b32 v6, v8, v7, s67
	v_mul_f32_e32 v7, 0x3c800000, v70
	v_mul_f32_e32 v8, 0x3c800000, v71
	v_mul_f32_e32 v7, 0xbfb8aa3b, v7
	v_mul_f32_e32 v8, 0xbfb8aa3b, v8
	v_exp_f32_e32 v7, v7
	v_exp_f32_e32 v8, v8
	v_perm_b32 v5, v6, v5, s68
	v_mul_f32_e32 v9, 0x3c800000, v73
	v_add_f32_e32 v6, 1.0, v7
	v_add_f32_e32 v7, 1.0, v8
	v_mul_f32_e32 v8, 0x3c800000, v72
	v_mul_f32_e32 v8, 0xbfb8aa3b, v8
	v_mul_f32_e32 v9, 0xbfb8aa3b, v9
	v_exp_f32_e32 v8, v8
	v_exp_f32_e32 v9, v9
	v_rcp_f32_e32 v6, v6
	v_rcp_f32_e32 v7, v7
	v_add_f32_e32 v8, 1.0, v8
	v_add_f32_e32 v9, 1.0, v9
	v_rcp_f32_e32 v8, v8
	v_rcp_f32_e32 v9, v9
	v_fmamk_f32 v6, v6, 0x437f0000, v196
	v_fmamk_f32 v7, v7, 0x437f0000, v196
	v_fmamk_f32 v8, v8, 0x437f0000, v196
	v_fmamk_f32 v9, v9, 0x437f0000, v196
	v_perm_b32 v6, v7, v6, s67
	v_perm_b32 v7, v9, v8, s67
	v_mul_f32_e32 v8, 0x3c800000, v66
	v_mul_f32_e32 v9, 0x3c800000, v67
	v_mul_f32_e32 v8, 0xbfb8aa3b, v8
	v_mul_f32_e32 v9, 0xbfb8aa3b, v9
	v_exp_f32_e32 v8, v8
	v_exp_f32_e32 v9, v9
	v_perm_b32 v6, v7, v6, s68
	v_mul_f32_e32 v10, 0x3c800000, v69
	v_add_f32_e32 v7, 1.0, v8
	v_add_f32_e32 v8, 1.0, v9
	v_mul_f32_e32 v9, 0x3c800000, v68
	v_mul_f32_e32 v9, 0xbfb8aa3b, v9
	v_mul_f32_e32 v10, 0xbfb8aa3b, v10
	v_exp_f32_e32 v9, v9
	v_exp_f32_e32 v10, v10
	v_rcp_f32_e32 v7, v7
	v_rcp_f32_e32 v8, v8
	v_add_f32_e32 v9, 1.0, v9
	v_add_f32_e32 v10, 1.0, v10
	v_rcp_f32_e32 v9, v9
	v_rcp_f32_e32 v10, v10
	v_fmamk_f32 v7, v7, 0x437f0000, v196
	v_fmamk_f32 v8, v8, 0x437f0000, v196
	v_fmamk_f32 v9, v9, 0x437f0000, v196
	v_fmamk_f32 v10, v10, 0x437f0000, v196
	v_perm_b32 v7, v8, v7, s67
	v_perm_b32 v8, v10, v9, s67
	v_perm_b32 v7, v8, v7, s68
	v_add_co_u32_e32 v8, vcc, s70, v2
	v_mul_f32_e32 v10, 0x3c800000, v62
	s_nop 0
	v_addc_co_u32_e32 v9, vcc, 0, v3, vcc
	v_mul_f32_e32 v11, 0x3c800000, v63
	flat_store_dwordx4 v[8:9], v[4:7]
	v_mul_f32_e32 v10, 0xbfb8aa3b, v10
	v_mul_f32_e32 v11, 0xbfb8aa3b, v11
	v_mul_f32_e32 v6, 0x3c800000, v64
	v_mul_f32_e32 v7, 0x3c800000, v65
	v_mul_f32_e32 v6, 0xbfb8aa3b, v6
	v_mul_f32_e32 v7, 0xbfb8aa3b, v7
	v_exp_f32_e32 v10, v10
	v_exp_f32_e32 v11, v11
	v_exp_f32_e32 v6, v6
	v_exp_f32_e32 v7, v7
	v_add_f32_e32 v4, 1.0, v10
	v_add_f32_e32 v5, 1.0, v11
	v_add_f32_e32 v6, 1.0, v6
	v_add_f32_e32 v7, 1.0, v7
	v_rcp_f32_e32 v4, v4
	v_rcp_f32_e32 v5, v5
	v_rcp_f32_e32 v6, v6
	v_rcp_f32_e32 v7, v7
	v_fmamk_f32 v4, v4, 0x437f0000, v196
	v_fmamk_f32 v5, v5, 0x437f0000, v196
	v_fmamk_f32 v6, v6, 0x437f0000, v196
	v_fmamk_f32 v7, v7, 0x437f0000, v196
	v_perm_b32 v4, v5, v4, s67
	v_perm_b32 v5, v7, v6, s67
	v_mul_f32_e32 v6, 0x3c800000, v58
	v_mul_f32_e32 v7, 0x3c800000, v59
	v_mul_f32_e32 v6, 0xbfb8aa3b, v6
	v_mul_f32_e32 v7, 0xbfb8aa3b, v7
	v_exp_f32_e32 v6, v6
	v_exp_f32_e32 v7, v7
	v_perm_b32 v4, v5, v4, s68
	v_mul_f32_e32 v8, 0x3c800000, v61
	v_add_f32_e32 v5, 1.0, v6
	v_add_f32_e32 v6, 1.0, v7
	v_mul_f32_e32 v7, 0x3c800000, v60
	v_mul_f32_e32 v7, 0xbfb8aa3b, v7
	v_mul_f32_e32 v8, 0xbfb8aa3b, v8
	v_exp_f32_e32 v7, v7
	v_exp_f32_e32 v8, v8
	v_rcp_f32_e32 v5, v5
	v_rcp_f32_e32 v6, v6
	v_add_f32_e32 v7, 1.0, v7
	v_add_f32_e32 v8, 1.0, v8
	v_rcp_f32_e32 v7, v7
	v_rcp_f32_e32 v8, v8
	v_fmamk_f32 v5, v5, 0x437f0000, v196
	v_fmamk_f32 v6, v6, 0x437f0000, v196
	v_fmamk_f32 v7, v7, 0x437f0000, v196
	v_fmamk_f32 v8, v8, 0x437f0000, v196
	v_perm_b32 v5, v6, v5, s67
	v_perm_b32 v6, v8, v7, s67
	v_mul_f32_e32 v7, 0x3c800000, v54
	v_mul_f32_e32 v8, 0x3c800000, v55
	v_mul_f32_e32 v7, 0xbfb8aa3b, v7
	v_mul_f32_e32 v8, 0xbfb8aa3b, v8
; __device__ __forceinline__ float fsigmoid(float x) { return __builtin_amdgcn_rcpf(1.0f + __builtin_amdgcn_exp2f(-1.44269504f * x)); }
;     __device__ __forceinline__ void operator()(AccRef acc, const GUnit& u, int wr, int wc, int fr, int fq) const {
;         const int pm = u.x0, pn = u.x1; unsigned char* base = (pn < 8 ? GZF : GZS) + (size_t)(pm * 256 + wr * 64 + fr) * D + (pn & 7) * 256 + wc * 64 + 16 * fq;
; #pragma unroll
;         for (int ai = 0; ai < 2; ++ai)
; #pragma unroll
;             for (int m = 0; m < 4; ++m) { u32x4 w;
; #pragma unroll
;                 for (int bj = 0; bj < 2; ++bj)
; #pragma unroll
;                     for (int n = 0; n < 2; ++n) { const f32x4 v = acc[ai][bj][m][n]; w[bj * 2 + n] = pk4_u8(fsigmoid(v[0] * W8_INV), fsigmoid(v[1] * W8_INV), fsigmoid(v[2] * W8_INV), fsigmoid(v[3] * W8_INV)); }
;                 *(u32x4*)(base + (size_t)(ai * 128 + m * 16) * D) = w; }
	v_exp_f32_e32 v7, v7
	v_exp_f32_e32 v8, v8
	v_perm_b32 v5, v6, v5, s68
	v_mul_f32_e32 v9, 0x3c800000, v57
	v_add_f32_e32 v6, 1.0, v7
	v_add_f32_e32 v7, 1.0, v8
	v_mul_f32_e32 v8, 0x3c800000, v56
	v_mul_f32_e32 v8, 0xbfb8aa3b, v8
	v_mul_f32_e32 v9, 0xbfb8aa3b, v9
	v_exp_f32_e32 v8, v8
	v_exp_f32_e32 v9, v9
	v_rcp_f32_e32 v6, v6
	v_rcp_f32_e32 v7, v7
	v_add_f32_e32 v8, 1.0, v8
	v_add_f32_e32 v9, 1.0, v9
	v_rcp_f32_e32 v8, v8
	v_rcp_f32_e32 v9, v9
	v_fmamk_f32 v6, v6, 0x437f0000, v196
	v_fmamk_f32 v7, v7, 0x437f0000, v196
	v_fmamk_f32 v8, v8, 0x437f0000, v196
	v_fmamk_f32 v9, v9, 0x437f0000, v196
	v_perm_b32 v6, v7, v6, s67
	v_perm_b32 v7, v9, v8, s67
	v_mul_f32_e32 v8, 0x3c800000, v50
	v_mul_f32_e32 v9, 0x3c800000, v51
	v_mul_f32_e32 v8, 0xbfb8aa3b, v8
	v_mul_f32_e32 v9, 0xbfb8aa3b, v9
	v_exp_f32_e32 v8, v8
	v_exp_f32_e32 v9, v9
	v_perm_b32 v6, v7, v6, s68
	v_mul_f32_e32 v10, 0x3c800000, v53
	v_add_f32_e32 v7, 1.0, v8
	v_add_f32_e32 v8, 1.0, v9
	v_mul_f32_e32 v9, 0x3c800000, v52
	v_mul_f32_e32 v9, 0xbfb8aa3b, v9
	v_mul_f32_e32 v10, 0xbfb8aa3b, v10
	v_exp_f32_e32 v9, v9
	v_exp_f32_e32 v10, v10
	v_rcp_f32_e32 v7, v7
	v_rcp_f32_e32 v8, v8
	v_add_f32_e32 v9, 1.0, v9
	v_add_f32_e32 v10, 1.0, v10
	v_rcp_f32_e32 v9, v9
	v_rcp_f32_e32 v10, v10
	v_fmamk_f32 v7, v7, 0x437f0000, v196
	v_fmamk_f32 v8, v8, 0x437f0000, v196
	v_fmamk_f32 v9, v9, 0x437f0000, v196
	v_fmamk_f32 v10, v10, 0x437f0000, v196
	v_perm_b32 v7, v8, v7, s67
	v_perm_b32 v8, v10, v9, s67
	v_perm_b32 v7, v8, v7, s68
	v_add_co_u32_e32 v8, vcc, s71, v2
	v_mul_f32_e32 v10, 0x3c800000, v46
	s_nop 0
	v_addc_co_u32_e32 v9, vcc, 0, v3, vcc
	v_mul_f32_e32 v11, 0x3c800000, v47
	flat_store_dwordx4 v[8:9], v[4:7]
	v_mul_f32_e32 v10, 0xbfb8aa3b, v10
	v_mul_f32_e32 v11, 0xbfb8aa3b, v11
	v_mul_f32_e32 v6, 0x3c800000, v48
	v_mul_f32_e32 v7, 0x3c800000, v49
	v_mul_f32_e32 v6, 0xbfb8aa3b, v6
	v_mul_f32_e32 v7, 0xbfb8aa3b, v7
	v_exp_f32_e32 v10, v10
	v_exp_f32_e32 v11, v11
	v_exp_f32_e32 v6, v6
	v_exp_f32_e32 v7, v7
	v_add_f32_e32 v4, 1.0, v10
	v_add_f32_e32 v5, 1.0, v11
	v_add_f32_e32 v6, 1.0, v6
	v_add_f32_e32 v7, 1.0, v7
	v_rcp_f32_e32 v4, v4
	v_rcp_f32_e32 v5, v5
	v_rcp_f32_e32 v6, v6
	v_rcp_f32_e32 v7, v7
	v_fmamk_f32 v4, v4, 0x437f0000, v196
	v_fmamk_f32 v5, v5, 0x437f0000, v196
	v_fmamk_f32 v6, v6, 0x437f0000, v196
	v_fmamk_f32 v7, v7, 0x437f0000, v196
	v_perm_b32 v4, v5, v4, s67
	v_perm_b32 v5, v7, v6, s67
	v_mul_f32_e32 v6, 0x3c800000, v42
	v_mul_f32_e32 v7, 0x3c800000, v43
	v_mul_f32_e32 v6, 0xbfb8aa3b, v6
	v_mul_f32_e32 v7, 0xbfb8aa3b, v7
	v_exp_f32_e32 v6, v6
	v_exp_f32_e32 v7, v7
	v_perm_b32 v4, v5, v4, s68
	v_mul_f32_e32 v8, 0x3c800000, v45
	v_add_f32_e32 v5, 1.0, v6
	v_add_f32_e32 v6, 1.0, v7
	v_mul_f32_e32 v7, 0x3c800000, v44
	v_mul_f32_e32 v7, 0xbfb8aa3b, v7
	v_mul_f32_e32 v8, 0xbfb8aa3b, v8
	v_exp_f32_e32 v7, v7
	v_exp_f32_e32 v8, v8
	v_rcp_f32_e32 v5, v5
	v_rcp_f32_e32 v6, v6
	v_add_f32_e32 v7, 1.0, v7
	v_add_f32_e32 v8, 1.0, v8
	v_rcp_f32_e32 v7, v7
	v_rcp_f32_e32 v8, v8
	v_fmamk_f32 v5, v5, 0x437f0000, v196
	v_fmamk_f32 v6, v6, 0x437f0000, v196
	v_fmamk_f32 v7, v7, 0x437f0000, v196
	v_fmamk_f32 v8, v8, 0x437f0000, v196
	v_perm_b32 v5, v6, v5, s67
	v_perm_b32 v6, v8, v7, s67
	v_mul_f32_e32 v7, 0x3c800000, v38
	v_mul_f32_e32 v8, 0x3c800000, v39
	v_mul_f32_e32 v7, 0xbfb8aa3b, v7
	v_mul_f32_e32 v8, 0xbfb8aa3b, v8
	v_exp_f32_e32 v7, v7
	v_exp_f32_e32 v8, v8
	v_perm_b32 v5, v6, v5, s68
	v_mul_f32_e32 v9, 0x3c800000, v41
	v_add_f32_e32 v6, 1.0, v7
	v_add_f32_e32 v7, 1.0, v8
	v_mul_f32_e32 v8, 0x3c800000, v40
	v_mul_f32_e32 v8, 0xbfb8aa3b, v8
	v_mul_f32_e32 v9, 0xbfb8aa3b, v9
	v_exp_f32_e32 v8, v8
	v_exp_f32_e32 v9, v9
	v_rcp_f32_e32 v6, v6
	v_rcp_f32_e32 v7, v7
	v_add_f32_e32 v8, 1.0, v8
	v_add_f32_e32 v9, 1.0, v9
	v_rcp_f32_e32 v8, v8
	v_rcp_f32_e32 v9, v9
	v_fmamk_f32 v6, v6, 0x437f0000, v196
	v_fmamk_f32 v7, v7, 0x437f0000, v196
	v_fmamk_f32 v8, v8, 0x437f0000, v196
	v_fmamk_f32 v9, v9, 0x437f0000, v196
	v_perm_b32 v6, v7, v6, s67
	v_perm_b32 v7, v9, v8, s67
	v_mul_f32_e32 v8, 0x3c800000, v34
	v_mul_f32_e32 v9, 0x3c800000, v35
	v_mul_f32_e32 v8, 0xbfb8aa3b, v8
	v_mul_f32_e32 v9, 0xbfb8aa3b, v9
	v_exp_f32_e32 v8, v8
	v_exp_f32_e32 v9, v9
	v_perm_b32 v6, v7, v6, s68
	v_mul_f32_e32 v10, 0x3c800000, v37
	v_add_f32_e32 v7, 1.0, v8
	v_add_f32_e32 v8, 1.0, v9
	v_mul_f32_e32 v9, 0x3c800000, v36
	v_mul_f32_e32 v9, 0xbfb8aa3b, v9
	v_mul_f32_e32 v10, 0xbfb8aa3b, v10
	v_exp_f32_e32 v9, v9
	v_exp_f32_e32 v10, v10
	v_rcp_f32_e32 v7, v7
	v_rcp_f32_e32 v8, v8
	v_add_f32_e32 v9, 1.0, v9
	v_add_f32_e32 v10, 1.0, v10
	v_rcp_f32_e32 v9, v9
	v_rcp_f32_e32 v10, v10
	v_fmamk_f32 v7, v7, 0x437f0000, v196
	v_fmamk_f32 v8, v8, 0x437f0000, v196
	v_fmamk_f32 v9, v9, 0x437f0000, v196
	v_fmamk_f32 v10, v10, 0x437f0000, v196
	v_add_co_u32_e32 v2, vcc, 0x58000, v2
	v_perm_b32 v7, v8, v7, s67
	v_perm_b32 v8, v10, v9, s67
	v_addc_co_u32_e32 v3, vcc, 0, v3, vcc
	v_perm_b32 v7, v8, v7, s68
	s_andn2_b64 vcc, exec, s[0:1]
	s_mov_b64 s[0:1], -1
	flat_store_dwordx4 v[2:3], v[4:7]
	s_cbranch_vccnz .LBB0_420
	s_andn2_b64 vcc, exec, s[10:11]
	s_cbranch_vccnz .LBB0_419
	s_branch .LBB0_419

; #define PG8_STAGE(bufoff, gbase, voff) do { _Pragma("unroll") for (int _i = 0; _i < 2; ++_i) \
;         __builtin_amdgcn_global_load_lds((const unsigned*)((const char*)(gbase) + (voff)[_i]), (PG8_LAS unsigned*)(lds + (bufoff) + ldsw + _i * 8192), 16, 0, 0); } while (0)
; #define PG8_WAIT_V(n) asm volatile("s_waitcnt vmcnt(" #n ")" ::: "memory")
; #define PG8_WAIT_L(n) asm volatile("s_waitcnt lgkmcnt(" #n ")" ::: "memory")
; template <class Epi, class Sched, bool ALIGN_EPI = true, bool F8 = false>
; __device__ __forceinline__ void gemm_phase(PG8_LAS unsigned char* lds, const Sched& S, const Epi& E) {
;     ...
;         for (int t = 0; t < nt; t += 2) {
;             const bool last = (t == nt - 2);
;             if constexpr (Sched::GATHER) { if (last && has_next) S.a_off(nxt, Rs, Cs, voffAn); }
;             const char* a1 = cA + (size_t)(t + 1) * kstep;
;             const char* a2 = last ? nA : cA + (size_t)(t + 2) * kstep; const char* b2 = last ? nB : cB + (size_t)(t + 2) * kstepB;
;             const char* a3 = a2 + kstep; const char* b3 = b2 + kstepB;
;             unsigned vA2[2][2];
; #pragma unroll
;             for (int h = 0; h < 2; ++h)
; #pragma unroll
;                 for (int i = 0; i < 2; ++i) { if constexpr (Sched::GATHER) vA2[h][i] = (last && has_next) ? voffAn[h][i] : voffA[h][i]; else vA2[h][i] = voffA[h][i]; }
;             PG8_LDB(B0, 0, 0); PG8_LDB(B1, 0, 1); PG8_SCHED; PG8_LDA(At, 0, 0); PG8_STAGE(PG8_SA(1, 1), a1, voffA[1]);
;             PG8_WAIT_V(8); PG8_WAIT_L(0); PG8_BAR; PG8_MMA(0, 0, At, B0); PG8_MMA(0, 1, At, B1); PG8_BAR; PG8_SCHED;
;             PG8_LDA(At, 0, 1); PG8_STAGE(PG8_SB(0, 0), b2, voffB[0]); PG8_STAGE(PG8_SB(0, 1), b2, voffB[1]); PG8_STAGE(PG8_SA(0, 0), a2, vA2[0]);
;             PG8_WAIT_V(8); PG8_WAIT_L(0); PG8_BAR; PG8_MMA(1, 0, At, B0); PG8_MMA(1, 1, At, B1); PG8_BAR; PG8_SCHED;
;             PG8_LDB(B0, 1, 0); PG8_LDB(B1, 1, 1); PG8_SCHED; PG8_LDA(At, 1, 0); PG8_STAGE(PG8_SA(0, 1), a2, vA2[1]);
;             PG8_WAIT_V(8); PG8_WAIT_L(0); PG8_BAR; PG8_MMA(0, 0, At, B0); PG8_MMA(0, 1, At, B1); PG8_BAR; PG8_SCHED;
;             PG8_LDA(At, 1, 1); PG8_STAGE(PG8_SB(1, 0), b3, voffB[0]); PG8_STAGE(PG8_SB(1, 1), b3, voffB[1]); PG8_STAGE(PG8_SA(1, 0), a3, vA2[0]);
;             PG8_WAIT_V(8); PG8_WAIT_L(0); PG8_BAR; PG8_MMA(1, 0, At, B0); PG8_MMA(1, 1, At, B1); PG8_BAR; PG8_SCHED;
.Lh1e_23459:
.Lh1_834:
	v_add_u32_e32 v10, s58, v190
	ds_read_b128 v[2:5], v10
	ds_read_b128 v[6:9], v10 offset:1024
	ds_read_b128 v[142:145], v10 offset:2048
	ds_read_b128 v[146:149], v10 offset:3072
	v_add_u32_e32 v10, s59, v190
	ds_read_b128 v[150:153], v10
	ds_read_b128 v[154:157], v10 offset:1024
	ds_read_b128 v[202:205], v10 offset:2048
	ds_read_b128 v[206:209], v10 offset:3072
	s_add_i32 s77, s26, 2
	s_add_u32 s27, s24, 0x8000
	s_addc_u32 s28, s25, 0
	s_cmp_eq_u32 s74, s26
	s_cselect_b32 s30, s20, s27
	s_cselect_b32 s31, s21, s28
	s_cselect_b32 s28, s22, s75
	s_cselect_b32 s29, s23, s76
	s_add_u32 s26, s30, 0x8000
	s_addc_u32 s27, s31, 0
	v_lshl_add_u64 v[12:13], s[24:25], 0, v[182:183]
	s_add_i32 m0, s45, 0xc000
	ds_read_b128 v[210:213], v198
	ds_read_b128 v[214:217], v198 offset:1024
	ds_read_b128 v[218:221], v198 offset:2048
	ds_read_b128 v[222:225], v198 offset:3072
	ds_read_b128 v[226:229], v198 offset:4096
	ds_read_b128 v[230:233], v198 offset:5120
	ds_read_b128 v[234:237], v198 offset:6144
	ds_read_b128 v[238:241], v198 offset:7168
	global_load_lds_dwordx4 v[12:13], off
	v_lshl_add_u64 v[12:13], s[24:25], 0, v[180:181]
	s_add_i32 m0, s45, 0xe000
	s_nop 0
	global_load_lds_dwordx4 v[12:13], off
	s_waitcnt vmcnt(8)
	s_waitcnt lgkmcnt(0)
	s_barrier
	s_setprio 2
	s_waitcnt lgkmcnt(0)
	v_mfma_scale_f32_16x16x128_f8f6f4 v[138:141], v[2:9], v[210:217], v[138:141], v199, v199 op_sel_hi:[0,0,0]
	v_mfma_scale_f32_16x16x128_f8f6f4 v[134:137], v[142:149], v[210:217], v[134:137], v199, v199 op_sel_hi:[0,0,0]
	v_mfma_scale_f32_16x16x128_f8f6f4 v[130:133], v[2:9], v[218:225], v[130:133], v199, v199 op_sel_hi:[0,0,0]
	v_mfma_scale_f32_16x16x128_f8f6f4 v[126:129], v[142:149], v[218:225], v[126:129], v199, v199 op_sel_hi:[0,0,0]
	v_mfma_scale_f32_16x16x128_f8f6f4 v[122:125], v[2:9], v[226:233], v[122:125], v199, v199 op_sel_hi:[0,0,0]
	v_mfma_scale_f32_16x16x128_f8f6f4 v[118:121], v[142:149], v[226:233], v[118:121], v199, v199 op_sel_hi:[0,0,0]
	v_mfma_scale_f32_16x16x128_f8f6f4 v[114:117], v[2:9], v[234:241], v[114:117], v199, v199 op_sel_hi:[0,0,0]
	v_mfma_scale_f32_16x16x128_f8f6f4 v[110:113], v[142:149], v[234:241], v[110:113], v199, v199 op_sel_hi:[0,0,0]
	s_nop 3
	s_setprio 0
	s_setprio 2
	v_mfma_scale_f32_16x16x128_f8f6f4 v[106:109], v[150:157], v[210:217], v[106:109], v199, v199 op_sel_hi:[0,0,0]
	v_mfma_scale_f32_16x16x128_f8f6f4 v[102:105], v[202:209], v[210:217], v[102:105], v199, v199 op_sel_hi:[0,0,0]
	v_mfma_scale_f32_16x16x128_f8f6f4 v[98:101], v[150:157], v[218:225], v[98:101], v199, v199 op_sel_hi:[0,0,0]
	v_mfma_scale_f32_16x16x128_f8f6f4 v[94:97], v[202:209], v[218:225], v[94:97], v199, v199 op_sel_hi:[0,0,0]
	v_mfma_scale_f32_16x16x128_f8f6f4 v[90:93], v[150:157], v[226:233], v[90:93], v199, v199 op_sel_hi:[0,0,0]
	v_mfma_scale_f32_16x16x128_f8f6f4 v[86:89], v[202:209], v[226:233], v[86:89], v199, v199 op_sel_hi:[0,0,0]
	v_mfma_scale_f32_16x16x128_f8f6f4 v[82:85], v[150:157], v[234:241], v[82:85], v199, v199 op_sel_hi:[0,0,0]
	v_mfma_scale_f32_16x16x128_f8f6f4 v[78:81], v[202:209], v[234:241], v[78:81], v199, v199 op_sel_hi:[0,0,0]
	s_nop 3
	s_setprio 0
	s_add_i32 s78, s58, s44
	v_lshl_add_u64 v[12:13], s[28:29], 0, v[158:159]
	s_mov_b32 m0, s78
	ds_read_b128 v[210:213], v198 offset:16384
	ds_read_b128 v[214:217], v198 offset:17408
	ds_read_b128 v[218:221], v198 offset:18432
	ds_read_b128 v[222:225], v198 offset:19456
	ds_read_b128 v[226:229], v198 offset:20480
	ds_read_b128 v[230:233], v198 offset:21504
	ds_read_b128 v[234:237], v198 offset:22528
	ds_read_b128 v[238:241], v198 offset:23552
	global_load_lds_dwordx4 v[12:13], off
	v_lshl_add_u64 v[188:189], s[28:29], 0, v[160:161]
	s_add_i32 m0, s78, 0x2000
	s_add_i32 s78, s59, s44
	global_load_lds_dwordx4 v[188:189], off
	v_lshl_add_u64 v[12:13], v[12:13], 0, s[8:9]
	s_mov_b32 m0, s78
	s_nop 0
	global_load_lds_dwordx4 v[12:13], off
	v_lshl_add_u64 v[12:13], v[188:189], 0, s[8:9]
	s_add_i32 m0, s78, 0x2000
	s_nop 0
	global_load_lds_dwordx4 v[12:13], off
	v_lshl_add_u64 v[12:13], s[30:31], 0, v[162:163]
	s_mov_b32 m0, s45
	s_nop 0
	global_load_lds_dwordx4 v[12:13], off
	v_lshl_add_u64 v[12:13], s[30:31], 0, v[164:165]
	s_mov_b32 m0, s46
	s_nop 0
	global_load_lds_dwordx4 v[12:13], off
	s_waitcnt vmcnt(8)
	s_waitcnt lgkmcnt(0)
	s_barrier
; #define PG8_STAGE(bufoff, gbase, voff) do { _Pragma("unroll") for (int _i = 0; _i < 2; ++_i) \
;         __builtin_amdgcn_global_load_lds((const unsigned*)((const char*)(gbase) + (voff)[_i]), (PG8_LAS unsigned*)(lds + (bufoff) + ldsw + _i * 8192), 16, 0, 0); } while (0)
; #define PG8_WAIT_V(n) asm volatile("s_waitcnt vmcnt(" #n ")" ::: "memory")
; #define PG8_WAIT_L(n) asm volatile("s_waitcnt lgkmcnt(" #n ")" ::: "memory")
; template <class Epi, class Sched, bool ALIGN_EPI = true, bool F8 = false>
; __device__ __forceinline__ void gemm_phase(PG8_LAS unsigned char* lds, const Sched& S, const Epi& E) {
;     ...
;         for (int t = 0; t < nt; t += 2) {
;             const bool last = (t == nt - 2);
;             if constexpr (Sched::GATHER) { if (last && has_next) S.a_off(nxt, Rs, Cs, voffAn); }
;             const char* a1 = cA + (size_t)(t + 1) * kstep;
;             const char* a2 = last ? nA : cA + (size_t)(t + 2) * kstep; const char* b2 = last ? nB : cB + (size_t)(t + 2) * kstepB;
;             const char* a3 = a2 + kstep; const char* b3 = b2 + kstepB;
;             unsigned vA2[2][2];
; #pragma unroll
;             for (int h = 0; h < 2; ++h)
; #pragma unroll
;                 for (int i = 0; i < 2; ++i) { if constexpr (Sched::GATHER) vA2[h][i] = (last && has_next) ? voffAn[h][i] : voffA[h][i]; else vA2[h][i] = voffA[h][i]; }
;             PG8_LDB(B0, 0, 0); PG8_LDB(B1, 0, 1); PG8_SCHED; PG8_LDA(At, 0, 0); PG8_STAGE(PG8_SA(1, 1), a1, voffA[1]);
;             PG8_WAIT_V(8); PG8_WAIT_L(0); PG8_BAR; PG8_MMA(0, 0, At, B0); PG8_MMA(0, 1, At, B1); PG8_BAR; PG8_SCHED;
;             PG8_LDA(At, 0, 1); PG8_STAGE(PG8_SB(0, 0), b2, voffB[0]); PG8_STAGE(PG8_SB(0, 1), b2, voffB[1]); PG8_STAGE(PG8_SA(0, 0), a2, vA2[0]);
;             PG8_WAIT_V(8); PG8_WAIT_L(0); PG8_BAR; PG8_MMA(1, 0, At, B0); PG8_MMA(1, 1, At, B1); PG8_BAR; PG8_SCHED;
;             PG8_LDB(B0, 1, 0); PG8_LDB(B1, 1, 1); PG8_SCHED; PG8_LDA(At, 1, 0); PG8_STAGE(PG8_SA(0, 1), a2, vA2[1]);
;             PG8_WAIT_V(8); PG8_WAIT_L(0); PG8_BAR; PG8_MMA(0, 0, At, B0); PG8_MMA(0, 1, At, B1); PG8_BAR; PG8_SCHED;
;             PG8_LDA(At, 1, 1); PG8_STAGE(PG8_SB(1, 0), b3, voffB[0]); PG8_STAGE(PG8_SB(1, 1), b3, voffB[1]); PG8_STAGE(PG8_SA(1, 0), a3, vA2[0]);
;             PG8_WAIT_V(8); PG8_WAIT_L(0); PG8_BAR; PG8_MMA(1, 0, At, B0); PG8_MMA(1, 1, At, B1); PG8_BAR; PG8_SCHED;
	s_setprio 2
	s_waitcnt lgkmcnt(0)
	v_mfma_scale_f32_16x16x128_f8f6f4 v[74:77], v[2:9], v[210:217], v[74:77], v199, v199 op_sel_hi:[0,0,0]
	v_mfma_scale_f32_16x16x128_f8f6f4 v[70:73], v[142:149], v[210:217], v[70:73], v199, v199 op_sel_hi:[0,0,0]
	v_mfma_scale_f32_16x16x128_f8f6f4 v[66:69], v[2:9], v[218:225], v[66:69], v199, v199 op_sel_hi:[0,0,0]
	v_mfma_scale_f32_16x16x128_f8f6f4 v[62:65], v[142:149], v[218:225], v[62:65], v199, v199 op_sel_hi:[0,0,0]
	v_mfma_scale_f32_16x16x128_f8f6f4 v[58:61], v[2:9], v[226:233], v[58:61], v199, v199 op_sel_hi:[0,0,0]
	v_mfma_scale_f32_16x16x128_f8f6f4 v[54:57], v[142:149], v[226:233], v[54:57], v199, v199 op_sel_hi:[0,0,0]
	v_mfma_scale_f32_16x16x128_f8f6f4 v[50:53], v[2:9], v[234:241], v[50:53], v199, v199 op_sel_hi:[0,0,0]
	v_mfma_scale_f32_16x16x128_f8f6f4 v[46:49], v[142:149], v[234:241], v[46:49], v199, v199 op_sel_hi:[0,0,0]
	s_nop 3
	s_setprio 0
	s_setprio 2
	v_mfma_scale_f32_16x16x128_f8f6f4 v[42:45], v[150:157], v[210:217], v[42:45], v199, v199 op_sel_hi:[0,0,0]
	v_mfma_scale_f32_16x16x128_f8f6f4 v[38:41], v[202:209], v[210:217], v[38:41], v199, v199 op_sel_hi:[0,0,0]
	v_mfma_scale_f32_16x16x128_f8f6f4 v[34:37], v[150:157], v[218:225], v[34:37], v199, v199 op_sel_hi:[0,0,0]
	v_mfma_scale_f32_16x16x128_f8f6f4 v[30:33], v[202:209], v[218:225], v[30:33], v199, v199 op_sel_hi:[0,0,0]
	v_mfma_scale_f32_16x16x128_f8f6f4 v[26:29], v[150:157], v[226:233], v[26:29], v199, v199 op_sel_hi:[0,0,0]
	v_mfma_scale_f32_16x16x128_f8f6f4 v[22:25], v[202:209], v[226:233], v[22:25], v199, v199 op_sel_hi:[0,0,0]
	v_mfma_scale_f32_16x16x128_f8f6f4 v[18:21], v[150:157], v[234:241], v[18:21], v199, v199 op_sel_hi:[0,0,0]
	v_mfma_scale_f32_16x16x128_f8f6f4 v[14:17], v[202:209], v[234:241], v[14:17], v199, v199 op_sel_hi:[0,0,0]
	s_nop 3
	s_setprio 0
	s_add_i32 s78, 0, 0x18000
	s_add_i32 s79, 0, 0x1c000
	v_add_u32_e32 v2, s78, v190
	v_add_u32_e32 v10, s79, v190
	ds_read_b128 v[142:145], v2
	ds_read_b128 v[146:149], v2 offset:1024
	ds_read_b128 v[150:153], v2 offset:2048
	ds_read_b128 v[154:157], v2 offset:3072
	ds_read_b128 v[2:5], v10
	ds_read_b128 v[6:9], v10 offset:1024
	ds_read_b128 v[202:205], v10 offset:2048
	ds_read_b128 v[206:209], v10 offset:3072
	s_mov_b32 m0, s47
	v_lshl_add_u64 v[12:13], s[30:31], 0, v[166:167]
	ds_read_b128 v[210:213], v198 offset:32768
	ds_read_b128 v[214:217], v198 offset:33792
	ds_read_b128 v[218:221], v198 offset:34816
	ds_read_b128 v[222:225], v198 offset:35840
	ds_read_b128 v[226:229], v198 offset:36864
	ds_read_b128 v[230:233], v198 offset:37888
	ds_read_b128 v[234:237], v198 offset:38912
	ds_read_b128 v[238:241], v198 offset:39936
	global_load_lds_dwordx4 v[12:13], off
	v_lshl_add_u64 v[12:13], s[30:31], 0, v[168:169]
	s_mov_b32 m0, s48
	s_nop 0
	global_load_lds_dwordx4 v[12:13], off
	s_waitcnt vmcnt(8)
	s_waitcnt lgkmcnt(0)
	s_barrier
; #define PG8_STAGE(bufoff, gbase, voff) do { _Pragma("unroll") for (int _i = 0; _i < 2; ++_i) \
;         __builtin_amdgcn_global_load_lds((const unsigned*)((const char*)(gbase) + (voff)[_i]), (PG8_LAS unsigned*)(lds + (bufoff) + ldsw + _i * 8192), 16, 0, 0); } while (0)
; #define PG8_WAIT_V(n) asm volatile("s_waitcnt vmcnt(" #n ")" ::: "memory")
; #define PG8_WAIT_L(n) asm volatile("s_waitcnt lgkmcnt(" #n ")" ::: "memory")
; template <class Epi, class Sched, bool ALIGN_EPI = true, bool F8 = false>
; __device__ __forceinline__ void gemm_phase(PG8_LAS unsigned char* lds, const Sched& S, const Epi& E) {
;     ...
;         for (int t = 0; t < nt; t += 2) {
;             const bool last = (t == nt - 2);
;             if constexpr (Sched::GATHER) { if (last && has_next) S.a_off(nxt, Rs, Cs, voffAn); }
;             const char* a1 = cA + (size_t)(t + 1) * kstep;
;             const char* a2 = last ? nA : cA + (size_t)(t + 2) * kstep; const char* b2 = last ? nB : cB + (size_t)(t + 2) * kstepB;
;             const char* a3 = a2 + kstep; const char* b3 = b2 + kstepB;
;             unsigned vA2[2][2];
; #pragma unroll
;             for (int h = 0; h < 2; ++h)
; #pragma unroll
;                 for (int i = 0; i < 2; ++i) { if constexpr (Sched::GATHER) vA2[h][i] = (last && has_next) ? voffAn[h][i] : voffA[h][i]; else vA2[h][i] = voffA[h][i]; }
;             PG8_LDB(B0, 0, 0); PG8_LDB(B1, 0, 1); PG8_SCHED; PG8_LDA(At, 0, 0); PG8_STAGE(PG8_SA(1, 1), a1, voffA[1]);
;             PG8_WAIT_V(8); PG8_WAIT_L(0); PG8_BAR; PG8_MMA(0, 0, At, B0); PG8_MMA(0, 1, At, B1); PG8_BAR; PG8_SCHED;
;             PG8_LDA(At, 0, 1); PG8_STAGE(PG8_SB(0, 0), b2, voffB[0]); PG8_STAGE(PG8_SB(0, 1), b2, voffB[1]); PG8_STAGE(PG8_SA(0, 0), a2, vA2[0]);
;             PG8_WAIT_V(8); PG8_WAIT_L(0); PG8_BAR; PG8_MMA(1, 0, At, B0); PG8_MMA(1, 1, At, B1); PG8_BAR; PG8_SCHED;
;             PG8_LDB(B0, 1, 0); PG8_LDB(B1, 1, 1); PG8_SCHED; PG8_LDA(At, 1, 0); PG8_STAGE(PG8_SA(0, 1), a2, vA2[1]);
;             PG8_WAIT_V(8); PG8_WAIT_L(0); PG8_BAR; PG8_MMA(0, 0, At, B0); PG8_MMA(0, 1, At, B1); PG8_BAR; PG8_SCHED;
;             PG8_LDA(At, 1, 1); PG8_STAGE(PG8_SB(1, 0), b3, voffB[0]); PG8_STAGE(PG8_SB(1, 1), b3, voffB[1]); PG8_STAGE(PG8_SA(1, 0), a3, vA2[0]);
;             PG8_WAIT_V(8); PG8_WAIT_L(0); PG8_BAR; PG8_MMA(1, 0, At, B0); PG8_MMA(1, 1, At, B1); PG8_BAR; PG8_SCHED;
	s_setprio 2
	s_waitcnt lgkmcnt(0)
	v_mfma_scale_f32_16x16x128_f8f6f4 v[138:141], v[142:149], v[210:217], v[138:141], v199, v199 op_sel_hi:[0,0,0]
	v_mfma_scale_f32_16x16x128_f8f6f4 v[134:137], v[150:157], v[210:217], v[134:137], v199, v199 op_sel_hi:[0,0,0]
	v_mfma_scale_f32_16x16x128_f8f6f4 v[130:133], v[142:149], v[218:225], v[130:133], v199, v199 op_sel_hi:[0,0,0]
	v_mfma_scale_f32_16x16x128_f8f6f4 v[126:129], v[150:157], v[218:225], v[126:129], v199, v199 op_sel_hi:[0,0,0]
	v_mfma_scale_f32_16x16x128_f8f6f4 v[122:125], v[142:149], v[226:233], v[122:125], v199, v199 op_sel_hi:[0,0,0]
	v_mfma_scale_f32_16x16x128_f8f6f4 v[118:121], v[150:157], v[226:233], v[118:121], v199, v199 op_sel_hi:[0,0,0]
	v_mfma_scale_f32_16x16x128_f8f6f4 v[114:117], v[142:149], v[234:241], v[114:117], v199, v199 op_sel_hi:[0,0,0]
	v_mfma_scale_f32_16x16x128_f8f6f4 v[110:113], v[150:157], v[234:241], v[110:113], v199, v199 op_sel_hi:[0,0,0]
	s_nop 3
	s_setprio 0
	s_setprio 2
	v_mfma_scale_f32_16x16x128_f8f6f4 v[106:109], v[2:9], v[210:217], v[106:109], v199, v199 op_sel_hi:[0,0,0]
	v_mfma_scale_f32_16x16x128_f8f6f4 v[102:105], v[202:209], v[210:217], v[102:105], v199, v199 op_sel_hi:[0,0,0]
	v_mfma_scale_f32_16x16x128_f8f6f4 v[98:101], v[2:9], v[218:225], v[98:101], v199, v199 op_sel_hi:[0,0,0]
	v_mfma_scale_f32_16x16x128_f8f6f4 v[94:97], v[202:209], v[218:225], v[94:97], v199, v199 op_sel_hi:[0,0,0]
	v_mfma_scale_f32_16x16x128_f8f6f4 v[90:93], v[2:9], v[226:233], v[90:93], v199, v199 op_sel_hi:[0,0,0]
	v_mfma_scale_f32_16x16x128_f8f6f4 v[86:89], v[202:209], v[226:233], v[86:89], v199, v199 op_sel_hi:[0,0,0]
	v_mfma_scale_f32_16x16x128_f8f6f4 v[82:85], v[2:9], v[234:241], v[82:85], v199, v199 op_sel_hi:[0,0,0]
	v_mfma_scale_f32_16x16x128_f8f6f4 v[78:81], v[202:209], v[234:241], v[78:81], v199, v199 op_sel_hi:[0,0,0]
	s_nop 3
	s_setprio 0
	s_add_u32 s28, s28, 0x8000
	s_addc_u32 s29, s29, 0
	s_add_i32 s30, s78, s44
	v_lshl_add_u64 v[12:13], s[28:29], 0, v[158:159]
	s_mov_b32 m0, s30
	ds_read_b128 v[210:213], v198 offset:49152
	ds_read_b128 v[214:217], v198 offset:50176
	ds_read_b128 v[218:221], v198 offset:51200
	ds_read_b128 v[222:225], v198 offset:52224
	ds_read_b128 v[226:229], v198 offset:53248
	ds_read_b128 v[230:233], v198 offset:54272
	ds_read_b128 v[234:237], v198 offset:55296
	ds_read_b128 v[238:241], v198 offset:56320
	global_load_lds_dwordx4 v[12:13], off
	v_lshl_add_u64 v[12:13], s[28:29], 0, v[160:161]
	s_add_i32 m0, s30, 0x2000
	s_add_i32 s30, s79, s44
	global_load_lds_dwordx4 v[12:13], off
	v_lshl_add_u64 v[12:13], s[28:29], 0, v[172:173]
	s_mov_b32 m0, s30
	s_nop 0
	global_load_lds_dwordx4 v[12:13], off
	v_lshl_add_u64 v[12:13], s[28:29], 0, v[174:175]
	s_add_i32 m0, s30, 0x2000
	s_nop 0
	global_load_lds_dwordx4 v[12:13], off
	v_lshl_add_u64 v[12:13], s[26:27], 0, v[162:163]
	s_mov_b32 m0, s50
	s_nop 0
	global_load_lds_dwordx4 v[12:13], off
	v_lshl_add_u64 v[12:13], s[26:27], 0, v[164:165]
	s_mov_b32 m0, s51
	s_nop 0
	global_load_lds_dwordx4 v[12:13], off
	s_waitcnt vmcnt(8)
	s_waitcnt lgkmcnt(0)
	s_barrier
	s_setprio 2
	s_waitcnt lgkmcnt(0)
	v_mfma_scale_f32_16x16x128_f8f6f4 v[74:77], v[142:149], v[210:217], v[74:77], v199, v199 op_sel_hi:[0,0,0]
	v_mfma_scale_f32_16x16x128_f8f6f4 v[70:73], v[150:157], v[210:217], v[70:73], v199, v199 op_sel_hi:[0,0,0]
	v_mfma_scale_f32_16x16x128_f8f6f4 v[66:69], v[142:149], v[218:225], v[66:69], v199, v199 op_sel_hi:[0,0,0]
	v_mfma_scale_f32_16x16x128_f8f6f4 v[62:65], v[150:157], v[218:225], v[62:65], v199, v199 op_sel_hi:[0,0,0]
	v_mfma_scale_f32_16x16x128_f8f6f4 v[58:61], v[142:149], v[226:233], v[58:61], v199, v199 op_sel_hi:[0,0,0]
	v_mfma_scale_f32_16x16x128_f8f6f4 v[54:57], v[150:157], v[226:233], v[54:57], v199, v199 op_sel_hi:[0,0,0]
	v_mfma_scale_f32_16x16x128_f8f6f4 v[50:53], v[142:149], v[234:241], v[50:53], v199, v199 op_sel_hi:[0,0,0]
	v_mfma_scale_f32_16x16x128_f8f6f4 v[46:49], v[150:157], v[234:241], v[46:49], v199, v199 op_sel_hi:[0,0,0]
	s_nop 3
	s_setprio 0
	s_setprio 2
	v_mfma_scale_f32_16x16x128_f8f6f4 v[42:45], v[2:9], v[210:217], v[42:45], v199, v199 op_sel_hi:[0,0,0]
	v_mfma_scale_f32_16x16x128_f8f6f4 v[38:41], v[202:209], v[210:217], v[38:41], v199, v199 op_sel_hi:[0,0,0]
	v_mfma_scale_f32_16x16x128_f8f6f4 v[34:37], v[2:9], v[218:225], v[34:37], v199, v199 op_sel_hi:[0,0,0]
	v_mfma_scale_f32_16x16x128_f8f6f4 v[30:33], v[202:209], v[218:225], v[30:33], v199, v199 op_sel_hi:[0,0,0]
	v_mfma_scale_f32_16x16x128_f8f6f4 v[26:29], v[2:9], v[226:233], v[26:29], v199, v199 op_sel_hi:[0,0,0]
	v_mfma_scale_f32_16x16x128_f8f6f4 v[22:25], v[202:209], v[226:233], v[22:25], v199, v199 op_sel_hi:[0,0,0]
	v_mfma_scale_f32_16x16x128_f8f6f4 v[18:21], v[2:9], v[234:241], v[18:21], v199, v199 op_sel_hi:[0,0,0]
	v_mfma_scale_f32_16x16x128_f8f6f4 v[14:17], v[202:209], v[234:241], v[14:17], v199, v199 op_sel_hi:[0,0,0]
	s_nop 3
	s_setprio 0
	s_add_u32 s75, s75, 0x10000
	s_addc_u32 s76, s76, 0
	s_add_u32 s24, s24, 0x10000
	s_addc_u32 s25, s25, 0
	s_cmp_ge_i32 s77, s72
	s_mov_b32 s26, s77
	s_cbranch_scc0 .Lh1_834

; __device__ __forceinline__ f32x4 u8x4_f32(unsigned w) { return (f32x4){(float)(w & 0xffu), (float)((w >> 8) & 0xffu), (float)((w >> 16) & 0xffu), (float)(w >> 24)}; }
; __device__ __forceinline__ unsigned pk4_fp8(float a, float b, float c, float d) { int w = 0; w = __builtin_amdgcn_cvt_pk_fp8_f32(clamp8(a), clamp8(b), w, false); w = __builtin_amdgcn_cvt_pk_fp8_f32(clamp8(c), clamp8(d), w, true); return (unsigned)w; }
; __host__ __device__ __forceinline__ size_t tiled_off(size_t r, int kb, int ktiles) { return (((r >> 8) * ktiles + (kb >> 7)) << 15) + ((r & 255) << 7) + (kb & 127); }
; template <class Epi, class Sched, bool ALIGN_EPI = true, bool F8 = false>
; __device__ __forceinline__ void gemm_phase(PG8_LAS unsigned char* lds, const Sched& S, const Epi& E) {
;     ...
;         if constexpr (F8) {
; #pragma unroll
;             for (int a = 0; a < 2; ++a)
; #pragma unroll
;                 for (int b = 0; b < 2; ++b)
;                     asm volatile("s_nop 15\n\ts_nop 7" : "+v"(acc[a][b][0][0]), "+v"(acc[a][b][0][1]), "+v"(acc[a][b][1][0]), "+v"(acc[a][b][1][1]), "+v"(acc[a][b][2][0]), "+v"(acc[a][b][2][1]), "+v"(acc[a][b][3][0]), "+v"(acc[a][b][3][1]));
;     __device__ __forceinline__ void operator()(f32x4 (&acc)[2][2][4][2], const GUnit& u, int wr, int wc, int fr, int fq) const {
;     ...
;         for (int ai = 0; ai < 2; ++ai) {
;             u32x4 qf[4];
; #pragma unroll
;             for (int m = 0; m < 4; ++m) qf[m] = __builtin_nontemporal_load((const u32x4*)(GZF + off0 + (size_t)(ai * 128 + m * 16) * D));
; #pragma unroll
;             for (int m = 0; m < 4; ++m) { u32x4 w;
; #pragma unroll
;                 for (int q = 0; q < 4; ++q) { const f32x4 f = u8x4_f32(qf[m][q]); const f32x4 a = acc[ai][q >> 1][m][q & 1]; f32x4 v;
; #pragma unroll
;                     for (int j = 0; j < 4; ++j) v[j] = a[j] * (fmaxf(f[j], 0.5f) * (W8_INV / 255.0f));
;                     w[q] = pk4_fp8(v[0], v[1], v[2], v[3]); }
;                 *(u32x4*)(M8 + tiled_off((size_t)(u.x0 * 256 + wr * 64 + fr + ai * 128 + m * 16), u.x1 * 256 + wc * 64 + 16 * fq, D / 128)) = w; }
;             asm volatile("" ::: "memory");
;         }
.LBB0_837:
	s_lshl_b32 s28, s71, 8
	v_add_u32_e32 v144, s28, v177
	v_ashrrev_i32_e32 v145, 31, v144
	s_lshl_b32 s26, s70, 8
	v_lshlrev_b64 v[2:3], 11, v[144:145]
	s_ashr_i32 s27, s26, 31
	v_lshl_add_u64 v[142:143], v[2:3], 0, s[26:27]
	v_or_b32_e32 v142, v142, v176
	s_cmp_lg_u32 s73, 0
	s_cselect_b64 s[24:25], -1, 0
	s_cmp_eq_u32 s73, 0
	v_lshl_add_u64 v[12:13], s[6:7], 0, v[142:143]
	s_nop 15
	s_nop 7
	s_cbranch_scc1 .LBB0_845
	flat_load_dwordx4 v[146:149], v[12:13] nt
	v_add_co_u32_e32 v2, vcc, 0x8000, v12
	v_mov_b32_e32 v151, 0
	s_nop 0
	v_addc_co_u32_e32 v3, vcc, 0, v13, vcc
	v_add_co_u32_e32 v4, vcc, 0x10000, v12
	v_mov_b32_e32 v150, 0
	s_nop 0
	v_addc_co_u32_e32 v5, vcc, 0, v13, vcc
	flat_load_dwordx4 v[154:157], v[2:3] nt
	flat_load_dwordx4 v[6:9], v[4:5] nt
	v_add_co_u32_e32 v188, vcc, 0x18000, v12
	v_mov_b32_e32 v152, 0
	s_nop 0
	v_addc_co_u32_e32 v189, vcc, 0, v13, vcc
	flat_load_dwordx4 v[2:5], v[188:189] nt
	s_or_b32 s26, s26, s53
	s_ashr_i32 s26, s26, 7
	s_ashr_i32 s27, s26, 31
	s_waitcnt vmcnt(0) lgkmcnt(0)
	v_cvt_f32_ubyte0_e32 v189, v147
	v_cvt_f32_ubyte1_e32 v201, v147
	v_max_f32_e32 v189, 0.5, v189
	v_max_f32_e32 v201, 0.5, v201
	v_mul_f32_e32 v189, 0x38808081, v189
	v_mul_f32_e32 v201, 0x38808081, v201
	v_cvt_f32_ubyte0_e32 v10, v146
	v_cvt_f32_ubyte1_e32 v153, v146
	v_cvt_f32_ubyte0_e32 v203, v148
	v_cvt_f32_ubyte1_e32 v204, v148
	v_mul_f32_e32 v189, v134, v189
	v_mul_f32_e32 v201, v135, v201
	v_cvt_f32_ubyte2_e32 v202, v147
	v_cvt_f32_ubyte3_e32 v147, v147
	v_max_f32_e32 v10, 0.5, v10
	v_max_f32_e32 v153, 0.5, v153
	v_max_f32_e32 v203, 0.5, v203
	v_max_f32_e32 v204, 0.5, v204
	v_med3_f32 v189, v189, s60, v200
	v_med3_f32 v201, v201, s60, v200
	v_cvt_f32_ubyte2_e32 v205, v148
	v_cvt_f32_ubyte3_e32 v148, v148
	v_max_f32_e32 v202, 0.5, v202
	v_max_f32_e32 v147, 0.5, v147
	v_mul_f32_e32 v10, 0x38808081, v10
	v_mul_f32_e32 v153, 0x38808081, v153
	v_mul_f32_e32 v203, 0x38808081, v203
	v_mul_f32_e32 v204, 0x38808081, v204
	v_cvt_pk_fp8_f32 v151, v189, v201
	v_max_f32_e32 v148, 0.5, v148
	v_mul_f32_e32 v202, 0x38808081, v202
	v_mul_f32_e32 v147, 0x38808081, v147
	v_mul_f32_e32 v10, v138, v10
	v_mul_f32_e32 v153, v139, v153
	v_mul_f32_e32 v203, v106, v203
	v_mul_f32_e32 v204, v107, v204
	v_cvt_f32_ubyte2_e32 v188, v146
	v_cvt_f32_ubyte3_e32 v146, v146
	v_mul_f32_e32 v148, 0x38808081, v148
	v_mul_f32_e32 v202, v136, v202
	v_mul_f32_e32 v147, v137, v147
	v_med3_f32 v10, v10, s60, v200
	v_med3_f32 v153, v153, s60, v200
	v_med3_f32 v203, v203, s60, v200
	v_med3_f32 v204, v204, s60, v200
	v_cvt_f32_ubyte0_e32 v206, v149
	v_cvt_f32_ubyte1_e32 v207, v149
	v_max_f32_e32 v188, 0.5, v188
	v_max_f32_e32 v146, 0.5, v146
	v_max_f32_e32 v205, 0.5, v205
	v_mul_f32_e32 v148, v109, v148
	v_med3_f32 v202, v202, s60, v200
	v_med3_f32 v147, v147, s60, v200
	v_cvt_pk_fp8_f32 v150, v10, v153
	v_cvt_pk_fp8_f32 v152, v203, v204
	v_mul_f32_e32 v188, 0x38808081, v188
	v_mul_f32_e32 v146, 0x38808081, v146
	v_mul_f32_e32 v205, 0x38808081, v205
	v_med3_f32 v10, v148, s60, v200
	v_cvt_pk_fp8_f32 v151, v202, v147 op_sel:[0,0,1]
	v_max_f32_e32 v147, 0.5, v206
	v_max_f32_e32 v148, 0.5, v207
	v_mul_f32_e32 v188, v140, v188
	v_mul_f32_e32 v146, v141, v146
	v_mul_f32_e32 v205, v108, v205
	v_mul_f32_e32 v147, 0x38808081, v147
	v_mul_f32_e32 v148, 0x38808081, v148
	v_med3_f32 v188, v188, s60, v200
	v_med3_f32 v146, v146, s60, v200
	v_med3_f32 v205, v205, s60, v200
	v_mul_f32_e32 v147, v102, v147
	v_mul_f32_e32 v148, v103, v148
	v_cvt_pk_fp8_f32 v150, v188, v146 op_sel:[0,0,1]
	v_cvt_pk_fp8_f32 v152, v205, v10 op_sel:[0,0,1]
	v_cvt_f32_ubyte2_e32 v10, v149
	v_cvt_f32_ubyte3_e32 v146, v149
	v_med3_f32 v147, v147, s60, v200
	v_med3_f32 v148, v148, s60, v200
	v_mov_b32_e32 v153, 0
	v_max_f32_e32 v10, 0.5, v10
	v_max_f32_e32 v146, 0.5, v146
	v_cvt_pk_fp8_f32 v153, v147, v148
	v_mul_f32_e32 v10, 0x38808081, v10
	v_mul_f32_e32 v146, 0x38808081, v146
	v_mul_f32_e32 v10, v104, v10
	v_mul_f32_e32 v146, v105, v146
	v_med3_f32 v10, v10, s60, v200
	v_med3_f32 v146, v146, s60, v200
	v_cvt_pk_fp8_f32 v153, v10, v146 op_sel:[0,0,1]
	v_lshrrev_b64 v[146:147], 4, v[144:145]
	v_and_b32_e32 v147, 0x1ffff, v147
	v_and_b32_e32 v146, -16, v146
	v_lshl_add_u64 v[146:147], v[146:147], 0, s[26:27]
	v_lshlrev_b64 v[146:147], 15, v[146:147]
	v_lshlrev_b32_e32 v10, 7, v144
	v_and_b32_e32 v10, 0x6780, v10
	v_lshl_add_u64 v[144:145], s[12:13], 0, v[146:147]
	v_lshl_add_u64 v[144:145], v[144:145], 0, v[10:11]
	v_lshl_add_u64 v[144:145], v[144:145], 0, v[178:179]
	flat_store_dwordx4 v[144:145], v[150:153]
	v_cvt_f32_ubyte0_e32 v10, v154
	v_cvt_f32_ubyte1_e32 v144, v154
	v_max_f32_e32 v10, 0.5, v10
	v_max_f32_e32 v144, 0.5, v144
	v_mul_f32_e32 v10, 0x38808081, v10
	v_mul_f32_e32 v144, 0x38808081, v144
	v_mul_f32_e32 v10, v130, v10
	v_mul_f32_e32 v144, v131, v144
	v_cvt_f32_ubyte2_e32 v145, v154
	v_cvt_f32_ubyte3_e32 v146, v154
	v_med3_f32 v10, v10, s60, v200
	v_med3_f32 v147, v144, s60, v200
	v_mov_b32_e32 v144, v11
	v_max_f32_e32 v145, 0.5, v145
	v_max_f32_e32 v146, 0.5, v146
	v_cvt_pk_fp8_f32 v144, v10, v147
	v_mul_f32_e32 v145, 0x38808081, v145
	v_mul_f32_e32 v146, 0x38808081, v146
	v_mul_f32_e32 v145, v132, v145
	v_mul_f32_e32 v10, v133, v146
	v_med3_f32 v145, v145, s60, v200
	v_med3_f32 v10, v10, s60, v200
	v_cvt_pk_fp8_f32 v144, v145, v10 op_sel:[0,0,1]
	v_cvt_f32_ubyte0_e32 v10, v155
	v_cvt_f32_ubyte1_e32 v145, v155
	v_max_f32_e32 v10, 0.5, v10
	v_max_f32_e32 v145, 0.5, v145
	v_mul_f32_e32 v10, 0x38808081, v10
	v_mul_f32_e32 v145, 0x38808081, v145
	v_mul_f32_e32 v10, v126, v10
	v_mul_f32_e32 v145, v127, v145
	v_cvt_f32_ubyte2_e32 v146, v155
	v_cvt_f32_ubyte3_e32 v147, v155
; __device__ __forceinline__ f32x4 u8x4_f32(unsigned w) { return (f32x4){(float)(w & 0xffu), (float)((w >> 8) & 0xffu), (float)((w >> 16) & 0xffu), (float)(w >> 24)}; }
; __device__ __forceinline__ unsigned pk4_fp8(float a, float b, float c, float d) { int w = 0; w = __builtin_amdgcn_cvt_pk_fp8_f32(clamp8(a), clamp8(b), w, false); w = __builtin_amdgcn_cvt_pk_fp8_f32(clamp8(c), clamp8(d), w, true); return (unsigned)w; }
; __host__ __device__ __forceinline__ size_t tiled_off(size_t r, int kb, int ktiles) { return (((r >> 8) * ktiles + (kb >> 7)) << 15) + ((r & 255) << 7) + (kb & 127); }
;     __device__ __forceinline__ void operator()(f32x4 (&acc)[2][2][4][2], const GUnit& u, int wr, int wc, int fr, int fq) const {
;     ...
; #pragma unroll
;             for (int m = 0; m < 4; ++m) { u32x4 w;
; #pragma unroll
;                 for (int q = 0; q < 4; ++q) { const f32x4 f = u8x4_f32(qf[m][q]); const f32x4 a = acc[ai][q >> 1][m][q & 1]; f32x4 v;
; #pragma unroll
;                     for (int j = 0; j < 4; ++j) v[j] = a[j] * (fmaxf(f[j], 0.5f) * (W8_INV / 255.0f));
;                     w[q] = pk4_fp8(v[0], v[1], v[2], v[3]); }
;                 *(u32x4*)(M8 + tiled_off((size_t)(u.x0 * 256 + wr * 64 + fr + ai * 128 + m * 16), u.x1 * 256 + wc * 64 + 16 * fq, D / 128)) = w; }
	v_med3_f32 v10, v10, s60, v200
	v_med3_f32 v148, v145, s60, v200
	v_mov_b32_e32 v145, v11
	v_max_f32_e32 v146, 0.5, v146
	v_max_f32_e32 v147, 0.5, v147
	v_cvt_pk_fp8_f32 v145, v10, v148
	v_mul_f32_e32 v146, 0x38808081, v146
	v_mul_f32_e32 v147, 0x38808081, v147
	v_mul_f32_e32 v146, v128, v146
	v_mul_f32_e32 v10, v129, v147
	v_med3_f32 v146, v146, s60, v200
	v_med3_f32 v10, v10, s60, v200
	v_cvt_pk_fp8_f32 v145, v146, v10 op_sel:[0,0,1]
	v_cvt_f32_ubyte0_e32 v10, v156
	v_cvt_f32_ubyte1_e32 v146, v156
	v_max_f32_e32 v10, 0.5, v10
	v_max_f32_e32 v146, 0.5, v146
	v_mul_f32_e32 v10, 0x38808081, v10
	v_mul_f32_e32 v146, 0x38808081, v146
	v_mul_f32_e32 v10, v98, v10
	v_mul_f32_e32 v146, v99, v146
	v_cvt_f32_ubyte2_e32 v147, v156
	v_cvt_f32_ubyte3_e32 v148, v156
	v_med3_f32 v10, v10, s60, v200
	v_med3_f32 v149, v146, s60, v200
	v_mov_b32_e32 v146, v11
	v_max_f32_e32 v147, 0.5, v147
	v_max_f32_e32 v148, 0.5, v148
	v_cvt_pk_fp8_f32 v146, v10, v149
	v_mul_f32_e32 v147, 0x38808081, v147
	v_mul_f32_e32 v148, 0x38808081, v148
	v_mul_f32_e32 v147, v100, v147
	v_mul_f32_e32 v10, v101, v148
	v_med3_f32 v147, v147, s60, v200
	v_med3_f32 v10, v10, s60, v200
	v_cvt_pk_fp8_f32 v146, v147, v10 op_sel:[0,0,1]
	v_cvt_f32_ubyte0_e32 v10, v157
	v_cvt_f32_ubyte1_e32 v147, v157
	v_max_f32_e32 v10, 0.5, v10
	v_max_f32_e32 v147, 0.5, v147
	v_mul_f32_e32 v10, 0x38808081, v10
	v_mul_f32_e32 v147, 0x38808081, v147
	v_mul_f32_e32 v10, v94, v10
	v_mul_f32_e32 v147, v95, v147
	v_cvt_f32_ubyte2_e32 v148, v157
	v_cvt_f32_ubyte3_e32 v149, v157
	v_med3_f32 v10, v10, s60, v200
	v_med3_f32 v150, v147, s60, v200
	v_mov_b32_e32 v147, v11
	v_max_f32_e32 v148, 0.5, v148
	v_max_f32_e32 v149, 0.5, v149
	v_cvt_pk_fp8_f32 v147, v10, v150
	v_mul_f32_e32 v148, 0x38808081, v148
	v_mul_f32_e32 v149, 0x38808081, v149
	v_mul_f32_e32 v148, v96, v148
	v_mul_f32_e32 v10, v97, v149
	v_med3_f32 v148, v148, s60, v200
	v_med3_f32 v10, v10, s60, v200
	v_cvt_pk_fp8_f32 v147, v148, v10 op_sel:[0,0,1]
	v_add_u32_e32 v148, s28, v191
	v_ashrrev_i32_e32 v149, 31, v148
	v_lshrrev_b64 v[150:151], 4, v[148:149]
	v_and_b32_e32 v151, 0x1ffff, v151
	v_and_b32_e32 v150, -16, v150
	v_lshl_add_u64 v[150:151], v[150:151], 0, s[26:27]
	v_lshlrev_b64 v[150:151], 15, v[150:151]
	v_lshlrev_b32_e32 v10, 7, v148
	v_and_b32_e32 v10, 0x7f80, v10
	v_lshl_add_u64 v[148:149], s[12:13], 0, v[150:151]
	v_lshl_add_u64 v[148:149], v[148:149], 0, v[10:11]
	v_lshl_add_u64 v[148:149], v[148:149], 0, v[178:179]
	flat_store_dwordx4 v[148:149], v[144:147]
	v_cvt_f32_ubyte0_e32 v10, v6
	v_max_f32_e32 v10, 0.5, v10
	v_cvt_f32_ubyte1_e32 v144, v6
	v_max_f32_e32 v144, 0.5, v144
	v_cvt_f32_ubyte2_e32 v145, v6
	v_cvt_f32_ubyte3_e32 v6, v6
	v_mul_f32_e32 v10, 0x38808081, v10
	v_mul_f32_e32 v144, 0x38808081, v144
	v_mul_f32_e32 v10, v122, v10
	v_mul_f32_e32 v144, v123, v144
	v_max_f32_e32 v6, 0.5, v6
	v_mul_f32_e32 v146, 0x38808081, v6
	v_med3_f32 v10, v10, s60, v200
	v_med3_f32 v144, v144, s60, v200
	v_mov_b32_e32 v6, v11
	v_max_f32_e32 v145, 0.5, v145
	v_cvt_pk_fp8_f32 v6, v10, v144
	v_mul_f32_e32 v145, 0x38808081, v145
	v_mul_f32_e32 v145, v124, v145
	v_mul_f32_e32 v10, v125, v146
	v_med3_f32 v144, v145, s60, v200
	v_med3_f32 v10, v10, s60, v200
	v_cvt_pk_fp8_f32 v6, v144, v10 op_sel:[0,0,1]
	v_cvt_f32_ubyte0_e32 v10, v7
	v_cvt_f32_ubyte1_e32 v144, v7
	v_max_f32_e32 v10, 0.5, v10
	v_max_f32_e32 v144, 0.5, v144
	v_cvt_f32_ubyte2_e32 v145, v7
	v_cvt_f32_ubyte3_e32 v7, v7
	v_mul_f32_e32 v10, 0x38808081, v10
	v_mul_f32_e32 v144, 0x38808081, v144
	v_mul_f32_e32 v10, v118, v10
	v_mul_f32_e32 v144, v119, v144
	v_max_f32_e32 v7, 0.5, v7
	v_mul_f32_e32 v146, 0x38808081, v7
	v_med3_f32 v10, v10, s60, v200
	v_med3_f32 v144, v144, s60, v200
	v_mov_b32_e32 v7, v11
	v_max_f32_e32 v145, 0.5, v145
	v_cvt_pk_fp8_f32 v7, v10, v144
	v_mul_f32_e32 v145, 0x38808081, v145
	v_mul_f32_e32 v145, v120, v145
	v_mul_f32_e32 v10, v121, v146
	v_med3_f32 v144, v145, s60, v200
	v_med3_f32 v10, v10, s60, v200
	v_cvt_pk_fp8_f32 v7, v144, v10 op_sel:[0,0,1]
	v_cvt_f32_ubyte0_e32 v10, v8
	v_cvt_f32_ubyte1_e32 v144, v8
	v_max_f32_e32 v10, 0.5, v10
	v_max_f32_e32 v144, 0.5, v144
	v_cvt_f32_ubyte2_e32 v145, v8
	v_cvt_f32_ubyte3_e32 v8, v8
	v_mul_f32_e32 v10, 0x38808081, v10
	v_mul_f32_e32 v144, 0x38808081, v144
	v_mul_f32_e32 v10, v90, v10
	v_mul_f32_e32 v144, v91, v144
	v_max_f32_e32 v8, 0.5, v8
	v_mul_f32_e32 v146, 0x38808081, v8
	v_med3_f32 v10, v10, s60, v200
	v_med3_f32 v144, v144, s60, v200
	v_mov_b32_e32 v8, v11
	v_max_f32_e32 v145, 0.5, v145
	v_cvt_pk_fp8_f32 v8, v10, v144
	v_mul_f32_e32 v145, 0x38808081, v145
	v_mul_f32_e32 v145, v92, v145
	v_mul_f32_e32 v10, v93, v146
	v_med3_f32 v144, v145, s60, v200
	v_med3_f32 v10, v10, s60, v200
	v_cvt_pk_fp8_f32 v8, v144, v10 op_sel:[0,0,1]
	v_cvt_f32_ubyte0_e32 v10, v9
	v_cvt_f32_ubyte1_e32 v144, v9
	v_max_f32_e32 v10, 0.5, v10
	v_max_f32_e32 v144, 0.5, v144
	v_cvt_f32_ubyte2_e32 v145, v9
	v_cvt_f32_ubyte3_e32 v9, v9
	v_mul_f32_e32 v10, 0x38808081, v10
	v_mul_f32_e32 v144, 0x38808081, v144
	v_mul_f32_e32 v10, v86, v10
	v_mul_f32_e32 v144, v87, v144
	v_max_f32_e32 v9, 0.5, v9
	v_mul_f32_e32 v146, 0x38808081, v9
	v_med3_f32 v10, v10, s60, v200
	v_med3_f32 v144, v144, s60, v200
	v_mov_b32_e32 v9, v11
	v_max_f32_e32 v145, 0.5, v145
	v_cvt_pk_fp8_f32 v9, v10, v144
	v_mul_f32_e32 v145, 0x38808081, v145
	v_mul_f32_e32 v145, v88, v145
	v_mul_f32_e32 v10, v89, v146
	v_med3_f32 v144, v145, s60, v200
	v_med3_f32 v10, v10, s60, v200
	v_cvt_pk_fp8_f32 v9, v144, v10 op_sel:[0,0,1]
	v_add_u32_e32 v144, s28, v192
	v_ashrrev_i32_e32 v145, 31, v144
	v_lshrrev_b64 v[146:147], 4, v[144:145]
	v_and_b32_e32 v147, 0x1ffff, v147
	v_and_b32_e32 v146, -16, v146
; __device__ __forceinline__ f32x4 u8x4_f32(unsigned w) { return (f32x4){(float)(w & 0xffu), (float)((w >> 8) & 0xffu), (float)((w >> 16) & 0xffu), (float)(w >> 24)}; }
; __device__ __forceinline__ unsigned pk4_fp8(float a, float b, float c, float d) { int w = 0; w = __builtin_amdgcn_cvt_pk_fp8_f32(clamp8(a), clamp8(b), w, false); w = __builtin_amdgcn_cvt_pk_fp8_f32(clamp8(c), clamp8(d), w, true); return (unsigned)w; }
; __host__ __device__ __forceinline__ size_t tiled_off(size_t r, int kb, int ktiles) { return (((r >> 8) * ktiles + (kb >> 7)) << 15) + ((r & 255) << 7) + (kb & 127); }
;     __device__ __forceinline__ void operator()(f32x4 (&acc)[2][2][4][2], const GUnit& u, int wr, int wc, int fr, int fq) const {
;     ...
;         for (int ai = 0; ai < 2; ++ai) {
;             u32x4 qf[4];
; #pragma unroll
;             for (int m = 0; m < 4; ++m) qf[m] = __builtin_nontemporal_load((const u32x4*)(GZF + off0 + (size_t)(ai * 128 + m * 16) * D));
; #pragma unroll
;             for (int m = 0; m < 4; ++m) { u32x4 w;
; #pragma unroll
;                 for (int q = 0; q < 4; ++q) { const f32x4 f = u8x4_f32(qf[m][q]); const f32x4 a = acc[ai][q >> 1][m][q & 1]; f32x4 v;
; #pragma unroll
;                     for (int j = 0; j < 4; ++j) v[j] = a[j] * (fmaxf(f[j], 0.5f) * (W8_INV / 255.0f));
;                     w[q] = pk4_fp8(v[0], v[1], v[2], v[3]); }
;                 *(u32x4*)(M8 + tiled_off((size_t)(u.x0 * 256 + wr * 64 + fr + ai * 128 + m * 16), u.x1 * 256 + wc * 64 + 16 * fq, D / 128)) = w; }
	v_lshl_add_u64 v[146:147], v[146:147], 0, s[26:27]
	v_lshlrev_b64 v[146:147], 15, v[146:147]
	v_lshlrev_b32_e32 v10, 7, v144
	v_and_b32_e32 v10, 0x7f80, v10
	v_lshl_add_u64 v[144:145], s[12:13], 0, v[146:147]
	v_lshl_add_u64 v[144:145], v[144:145], 0, v[10:11]
	v_lshl_add_u64 v[144:145], v[144:145], 0, v[178:179]
	flat_store_dwordx4 v[144:145], v[6:9]
	s_nop 1
	v_cvt_f32_ubyte0_e32 v6, v2
	v_cvt_f32_ubyte1_e32 v7, v2
	v_max_f32_e32 v6, 0.5, v6
	v_max_f32_e32 v7, 0.5, v7
	v_cvt_f32_ubyte2_e32 v8, v2
	v_cvt_f32_ubyte3_e32 v2, v2
	v_mul_f32_e32 v6, 0x38808081, v6
	v_mul_f32_e32 v7, 0x38808081, v7
	v_mul_f32_e32 v6, v114, v6
	v_mul_f32_e32 v7, v115, v7
	v_max_f32_e32 v2, 0.5, v2
	v_mul_f32_e32 v9, 0x38808081, v2
	v_med3_f32 v6, v6, s60, v200
	v_med3_f32 v7, v7, s60, v200
	v_mov_b32_e32 v2, v11
	v_max_f32_e32 v8, 0.5, v8
	v_cvt_pk_fp8_f32 v2, v6, v7
	v_mul_f32_e32 v8, 0x38808081, v8
	v_mul_f32_e32 v8, v116, v8
	v_mul_f32_e32 v6, v117, v9
	v_med3_f32 v7, v8, s60, v200
	v_med3_f32 v6, v6, s60, v200
	v_cvt_pk_fp8_f32 v2, v7, v6 op_sel:[0,0,1]
	v_cvt_f32_ubyte0_e32 v6, v3
	v_cvt_f32_ubyte1_e32 v7, v3
	v_max_f32_e32 v6, 0.5, v6
	v_max_f32_e32 v7, 0.5, v7
	v_cvt_f32_ubyte2_e32 v8, v3
	v_cvt_f32_ubyte3_e32 v3, v3
	v_mul_f32_e32 v6, 0x38808081, v6
	v_mul_f32_e32 v7, 0x38808081, v7
	v_mul_f32_e32 v6, v110, v6
	v_mul_f32_e32 v7, v111, v7
	v_max_f32_e32 v3, 0.5, v3
	v_mul_f32_e32 v9, 0x38808081, v3
	v_med3_f32 v6, v6, s60, v200
	v_med3_f32 v7, v7, s60, v200
	v_mov_b32_e32 v3, v11
	v_max_f32_e32 v8, 0.5, v8
	v_cvt_pk_fp8_f32 v3, v6, v7
	v_mul_f32_e32 v8, 0x38808081, v8
	v_mul_f32_e32 v8, v112, v8
	v_mul_f32_e32 v6, v113, v9
	v_med3_f32 v7, v8, s60, v200
	v_med3_f32 v6, v6, s60, v200
	v_cvt_pk_fp8_f32 v3, v7, v6 op_sel:[0,0,1]
	v_cvt_f32_ubyte0_e32 v6, v4
	v_cvt_f32_ubyte1_e32 v7, v4
	v_max_f32_e32 v6, 0.5, v6
	v_max_f32_e32 v7, 0.5, v7
	v_cvt_f32_ubyte2_e32 v8, v4
	v_cvt_f32_ubyte3_e32 v4, v4
	v_mul_f32_e32 v6, 0x38808081, v6
	v_mul_f32_e32 v7, 0x38808081, v7
	v_mul_f32_e32 v6, v82, v6
	v_mul_f32_e32 v7, v83, v7
	v_max_f32_e32 v4, 0.5, v4
	v_mul_f32_e32 v9, 0x38808081, v4
	v_med3_f32 v6, v6, s60, v200
	v_med3_f32 v7, v7, s60, v200
	v_mov_b32_e32 v4, v11
	v_max_f32_e32 v8, 0.5, v8
	v_cvt_pk_fp8_f32 v4, v6, v7
	v_mul_f32_e32 v8, 0x38808081, v8
	v_mul_f32_e32 v8, v84, v8
	v_mul_f32_e32 v6, v85, v9
	v_med3_f32 v7, v8, s60, v200
	v_med3_f32 v6, v6, s60, v200
	v_cvt_pk_fp8_f32 v4, v7, v6 op_sel:[0,0,1]
	v_cvt_f32_ubyte0_e32 v6, v5
	v_cvt_f32_ubyte1_e32 v7, v5
	v_max_f32_e32 v6, 0.5, v6
	v_max_f32_e32 v7, 0.5, v7
	v_cvt_f32_ubyte2_e32 v8, v5
	v_cvt_f32_ubyte3_e32 v5, v5
	v_mul_f32_e32 v6, 0x38808081, v6
	v_mul_f32_e32 v7, 0x38808081, v7
	v_mul_f32_e32 v6, v78, v6
	v_mul_f32_e32 v7, v79, v7
	v_max_f32_e32 v5, 0.5, v5
	v_mul_f32_e32 v9, 0x38808081, v5
	v_med3_f32 v6, v6, s60, v200
	v_med3_f32 v7, v7, s60, v200
	v_mov_b32_e32 v5, v11
	v_max_f32_e32 v8, 0.5, v8
	v_cvt_pk_fp8_f32 v5, v6, v7
	v_mul_f32_e32 v8, 0x38808081, v8
	v_mul_f32_e32 v8, v80, v8
	v_mul_f32_e32 v6, v81, v9
	v_med3_f32 v7, v8, s60, v200
	v_med3_f32 v6, v6, s60, v200
	v_cvt_pk_fp8_f32 v5, v7, v6 op_sel:[0,0,1]
	v_add_u32_e32 v6, s28, v193
	v_ashrrev_i32_e32 v7, 31, v6
	v_lshrrev_b64 v[8:9], 4, v[6:7]
	v_and_b32_e32 v9, 0x1ffff, v9
	v_and_b32_e32 v8, -16, v8
	v_lshl_add_u64 v[8:9], v[8:9], 0, s[26:27]
	v_lshlrev_b64 v[8:9], 15, v[8:9]
	v_lshlrev_b32_e32 v6, 7, v6
	v_and_b32_e32 v10, 0x7f80, v6
	v_lshl_add_u64 v[6:7], s[12:13], 0, v[8:9]
	v_lshl_add_u64 v[6:7], v[6:7], 0, v[10:11]
	v_lshl_add_u64 v[6:7], v[6:7], 0, v[178:179]
	flat_store_dwordx4 v[6:7], v[2:5]
	s_nop 1
	v_add_co_u32_e32 v2, vcc, s61, v12
	s_nop 1
	v_addc_co_u32_e32 v3, vcc, 0, v13, vcc
	flat_load_dwordx4 v[144:147], v[2:3] nt
	v_add_co_u32_e32 v2, vcc, s62, v12
	s_waitcnt vmcnt(0) lgkmcnt(0)
	v_cvt_f32_ubyte0_e32 v10, v144
	v_addc_co_u32_e32 v3, vcc, 0, v13, vcc
	flat_load_dwordx4 v[148:151], v[2:3] nt
	v_cvt_f32_ubyte1_e32 v152, v144
	v_max_f32_e32 v10, 0.5, v10
	v_max_f32_e32 v152, 0.5, v152
	v_cvt_f32_ubyte2_e32 v153, v144
	v_cvt_f32_ubyte3_e32 v144, v144
	v_mul_f32_e32 v10, 0x38808081, v10
	v_mul_f32_e32 v152, 0x38808081, v152
	v_mul_f32_e32 v10, v74, v10
	v_mul_f32_e32 v152, v75, v152
	v_max_f32_e32 v144, 0.5, v144
	v_mul_f32_e32 v154, 0x38808081, v144
	v_med3_f32 v10, v10, s60, v200
	v_med3_f32 v152, v152, s60, v200
	v_mov_b32_e32 v144, v11
	v_max_f32_e32 v153, 0.5, v153
	v_cvt_pk_fp8_f32 v144, v10, v152
	v_mul_f32_e32 v153, 0x38808081, v153
	v_add_co_u32_e32 v2, vcc, s63, v12
	v_mul_f32_e32 v153, v76, v153
	v_mul_f32_e32 v10, v77, v154
	v_addc_co_u32_e32 v3, vcc, 0, v13, vcc
	v_med3_f32 v152, v153, s60, v200
	v_med3_f32 v10, v10, s60, v200
	v_add_co_u32_e32 v4, vcc, s64, v12
	v_cvt_pk_fp8_f32 v144, v152, v10 op_sel:[0,0,1]
	v_cvt_f32_ubyte0_e32 v10, v145
	v_cvt_f32_ubyte1_e32 v152, v145
	v_addc_co_u32_e32 v5, vcc, 0, v13, vcc
	v_max_f32_e32 v10, 0.5, v10
	v_max_f32_e32 v152, 0.5, v152
	flat_load_dwordx4 v[6:9], v[2:3] nt
	s_nop 0
	flat_load_dwordx4 v[2:5], v[4:5] nt
	v_cvt_f32_ubyte2_e32 v153, v145
	v_cvt_f32_ubyte3_e32 v145, v145
	v_mul_f32_e32 v10, 0x38808081, v10
	v_mul_f32_e32 v152, 0x38808081, v152
	v_mul_f32_e32 v10, v70, v10
	v_mul_f32_e32 v152, v71, v152
	v_max_f32_e32 v145, 0.5, v145
	v_mul_f32_e32 v154, 0x38808081, v145
	v_med3_f32 v10, v10, s60, v200
	v_med3_f32 v152, v152, s60, v200
	v_mov_b32_e32 v145, v11
	v_max_f32_e32 v153, 0.5, v153
	v_cvt_pk_fp8_f32 v145, v10, v152
	v_mul_f32_e32 v153, 0x38808081, v153
	v_mul_f32_e32 v153, v72, v153
	v_mul_f32_e32 v10, v73, v154
	v_med3_f32 v152, v153, s60, v200
	v_med3_f32 v10, v10, s60, v200
	v_cvt_pk_fp8_f32 v145, v152, v10 op_sel:[0,0,1]
	v_cvt_f32_ubyte0_e32 v10, v146
; __device__ __forceinline__ f32x4 u8x4_f32(unsigned w) { return (f32x4){(float)(w & 0xffu), (float)((w >> 8) & 0xffu), (float)((w >> 16) & 0xffu), (float)(w >> 24)}; }
; __device__ __forceinline__ unsigned pk4_fp8(float a, float b, float c, float d) { int w = 0; w = __builtin_amdgcn_cvt_pk_fp8_f32(clamp8(a), clamp8(b), w, false); w = __builtin_amdgcn_cvt_pk_fp8_f32(clamp8(c), clamp8(d), w, true); return (unsigned)w; }
; __host__ __device__ __forceinline__ size_t tiled_off(size_t r, int kb, int ktiles) { return (((r >> 8) * ktiles + (kb >> 7)) << 15) + ((r & 255) << 7) + (kb & 127); }
;     __device__ __forceinline__ void operator()(f32x4 (&acc)[2][2][4][2], const GUnit& u, int wr, int wc, int fr, int fq) const {
;     ...
; #pragma unroll
;             for (int m = 0; m < 4; ++m) { u32x4 w;
; #pragma unroll
;                 for (int q = 0; q < 4; ++q) { const f32x4 f = u8x4_f32(qf[m][q]); const f32x4 a = acc[ai][q >> 1][m][q & 1]; f32x4 v;
; #pragma unroll
;                     for (int j = 0; j < 4; ++j) v[j] = a[j] * (fmaxf(f[j], 0.5f) * (W8_INV / 255.0f));
;                     w[q] = pk4_fp8(v[0], v[1], v[2], v[3]); }
;                 *(u32x4*)(M8 + tiled_off((size_t)(u.x0 * 256 + wr * 64 + fr + ai * 128 + m * 16), u.x1 * 256 + wc * 64 + 16 * fq, D / 128)) = w; }
	v_cvt_f32_ubyte1_e32 v152, v146
	v_max_f32_e32 v10, 0.5, v10
	v_max_f32_e32 v152, 0.5, v152
	v_cvt_f32_ubyte2_e32 v153, v146
	v_cvt_f32_ubyte3_e32 v146, v146
	v_mul_f32_e32 v10, 0x38808081, v10
	v_mul_f32_e32 v152, 0x38808081, v152
	v_mul_f32_e32 v10, v42, v10
	v_mul_f32_e32 v152, v43, v152
	v_max_f32_e32 v146, 0.5, v146
	v_mul_f32_e32 v154, 0x38808081, v146
	v_med3_f32 v10, v10, s60, v200
	v_med3_f32 v152, v152, s60, v200
	v_mov_b32_e32 v146, v11
	v_max_f32_e32 v153, 0.5, v153
	v_cvt_pk_fp8_f32 v146, v10, v152
	v_mul_f32_e32 v153, 0x38808081, v153
	v_mul_f32_e32 v153, v44, v153
	v_mul_f32_e32 v10, v45, v154
	v_med3_f32 v152, v153, s60, v200
	v_med3_f32 v10, v10, s60, v200
	v_cvt_pk_fp8_f32 v146, v152, v10 op_sel:[0,0,1]
	v_cvt_f32_ubyte0_e32 v10, v147
	v_cvt_f32_ubyte1_e32 v152, v147
	v_max_f32_e32 v10, 0.5, v10
	v_max_f32_e32 v152, 0.5, v152
	v_cvt_f32_ubyte2_e32 v153, v147
	v_cvt_f32_ubyte3_e32 v147, v147
	v_mul_f32_e32 v10, 0x38808081, v10
	v_mul_f32_e32 v152, 0x38808081, v152
	v_mul_f32_e32 v10, v38, v10
	v_mul_f32_e32 v152, v39, v152
	v_max_f32_e32 v147, 0.5, v147
	v_mul_f32_e32 v154, 0x38808081, v147
	v_med3_f32 v10, v10, s60, v200
	v_med3_f32 v152, v152, s60, v200
	v_mov_b32_e32 v147, v11
	v_max_f32_e32 v153, 0.5, v153
	v_cvt_pk_fp8_f32 v147, v10, v152
	v_mul_f32_e32 v153, 0x38808081, v153
	v_mul_f32_e32 v153, v40, v153
	v_mul_f32_e32 v10, v41, v154
	v_med3_f32 v152, v153, s60, v200
	v_med3_f32 v10, v10, s60, v200
	v_cvt_pk_fp8_f32 v147, v152, v10 op_sel:[0,0,1]
	v_add_u32_e32 v152, s28, v194
	v_ashrrev_i32_e32 v153, 31, v152
	v_lshrrev_b64 v[154:155], 4, v[152:153]
	v_and_b32_e32 v155, 0x1ffff, v155
	v_and_b32_e32 v154, -16, v154
	v_lshl_add_u64 v[154:155], v[154:155], 0, s[26:27]
	v_lshlrev_b64 v[154:155], 15, v[154:155]
	v_lshlrev_b32_e32 v10, 7, v152
	v_and_b32_e32 v10, 0x7f80, v10
	v_lshl_add_u64 v[152:153], s[12:13], 0, v[154:155]
	v_lshl_add_u64 v[152:153], v[152:153], 0, v[10:11]
	v_lshl_add_u64 v[152:153], v[152:153], 0, v[178:179]
	flat_store_dwordx4 v[152:153], v[144:147]
	s_waitcnt vmcnt(0) lgkmcnt(0)
	v_cvt_f32_ubyte0_e32 v10, v148
	v_max_f32_e32 v10, 0.5, v10
	v_cvt_f32_ubyte1_e32 v144, v148
	v_max_f32_e32 v144, 0.5, v144
	v_mul_f32_e32 v10, 0x38808081, v10
	v_mul_f32_e32 v144, 0x38808081, v144
	v_mul_f32_e32 v10, v66, v10
	v_mul_f32_e32 v144, v67, v144
	v_cvt_f32_ubyte2_e32 v145, v148
	v_cvt_f32_ubyte3_e32 v146, v148
	v_med3_f32 v10, v10, s60, v200
	v_med3_f32 v147, v144, s60, v200
	v_mov_b32_e32 v144, v11
	v_max_f32_e32 v145, 0.5, v145
	v_max_f32_e32 v146, 0.5, v146
	v_cvt_pk_fp8_f32 v144, v10, v147
	v_mul_f32_e32 v145, 0x38808081, v145
	v_mul_f32_e32 v146, 0x38808081, v146
	v_mul_f32_e32 v145, v68, v145
	v_mul_f32_e32 v10, v69, v146
	v_med3_f32 v145, v145, s60, v200
	v_med3_f32 v10, v10, s60, v200
	v_cvt_pk_fp8_f32 v144, v145, v10 op_sel:[0,0,1]
	v_cvt_f32_ubyte0_e32 v10, v149
	v_cvt_f32_ubyte1_e32 v145, v149
	v_max_f32_e32 v10, 0.5, v10
	v_max_f32_e32 v145, 0.5, v145
	v_mul_f32_e32 v10, 0x38808081, v10
	v_mul_f32_e32 v145, 0x38808081, v145
	v_mul_f32_e32 v10, v62, v10
	v_mul_f32_e32 v145, v63, v145
	v_cvt_f32_ubyte2_e32 v146, v149
	v_cvt_f32_ubyte3_e32 v147, v149
	v_med3_f32 v10, v10, s60, v200
	v_med3_f32 v148, v145, s60, v200
	v_mov_b32_e32 v145, v11
	v_max_f32_e32 v146, 0.5, v146
	v_max_f32_e32 v147, 0.5, v147
	v_cvt_pk_fp8_f32 v145, v10, v148
	v_mul_f32_e32 v146, 0x38808081, v146
	v_mul_f32_e32 v147, 0x38808081, v147
	v_mul_f32_e32 v146, v64, v146
	v_mul_f32_e32 v10, v65, v147
	v_med3_f32 v146, v146, s60, v200
	v_med3_f32 v10, v10, s60, v200
	v_cvt_pk_fp8_f32 v145, v146, v10 op_sel:[0,0,1]
	v_cvt_f32_ubyte0_e32 v10, v150
	v_cvt_f32_ubyte1_e32 v146, v150
	v_max_f32_e32 v10, 0.5, v10
	v_max_f32_e32 v146, 0.5, v146
	v_mul_f32_e32 v10, 0x38808081, v10
	v_mul_f32_e32 v146, 0x38808081, v146
	v_mul_f32_e32 v10, v34, v10
	v_mul_f32_e32 v146, v35, v146
	v_cvt_f32_ubyte2_e32 v147, v150
	v_cvt_f32_ubyte3_e32 v148, v150
	v_med3_f32 v10, v10, s60, v200
	v_med3_f32 v149, v146, s60, v200
	v_mov_b32_e32 v146, v11
	v_max_f32_e32 v147, 0.5, v147
	v_max_f32_e32 v148, 0.5, v148
	v_cvt_pk_fp8_f32 v146, v10, v149
	v_mul_f32_e32 v147, 0x38808081, v147
	v_mul_f32_e32 v148, 0x38808081, v148
	v_mul_f32_e32 v147, v36, v147
	v_mul_f32_e32 v10, v37, v148
	v_med3_f32 v147, v147, s60, v200
	v_med3_f32 v10, v10, s60, v200
	v_cvt_pk_fp8_f32 v146, v147, v10 op_sel:[0,0,1]
	v_cvt_f32_ubyte0_e32 v10, v151
	v_cvt_f32_ubyte1_e32 v147, v151
	v_max_f32_e32 v10, 0.5, v10
	v_max_f32_e32 v147, 0.5, v147
	v_mul_f32_e32 v10, 0x38808081, v10
	v_mul_f32_e32 v147, 0x38808081, v147
	v_mul_f32_e32 v10, v30, v10
	v_mul_f32_e32 v147, v31, v147
	v_cvt_f32_ubyte2_e32 v148, v151
	v_cvt_f32_ubyte3_e32 v149, v151
	v_med3_f32 v10, v10, s60, v200
	v_med3_f32 v150, v147, s60, v200
	v_mov_b32_e32 v147, v11
	v_max_f32_e32 v148, 0.5, v148
	v_max_f32_e32 v149, 0.5, v149
	v_cvt_pk_fp8_f32 v147, v10, v150
	v_mul_f32_e32 v148, 0x38808081, v148
	v_mul_f32_e32 v149, 0x38808081, v149
	v_mul_f32_e32 v148, v32, v148
	v_mul_f32_e32 v10, v33, v149
	v_med3_f32 v148, v148, s60, v200
	v_med3_f32 v10, v10, s60, v200
	v_cvt_pk_fp8_f32 v147, v148, v10 op_sel:[0,0,1]
	v_add_u32_e32 v148, s28, v195
	v_ashrrev_i32_e32 v149, 31, v148
	v_lshrrev_b64 v[150:151], 4, v[148:149]
	v_and_b32_e32 v151, 0x1ffff, v151
	v_and_b32_e32 v150, -16, v150
	v_lshl_add_u64 v[150:151], v[150:151], 0, s[26:27]
	v_lshlrev_b64 v[150:151], 15, v[150:151]
	v_lshlrev_b32_e32 v10, 7, v148
	v_and_b32_e32 v10, 0x7f80, v10
	v_lshl_add_u64 v[148:149], s[12:13], 0, v[150:151]
	v_lshl_add_u64 v[148:149], v[148:149], 0, v[10:11]
	v_lshl_add_u64 v[148:149], v[148:149], 0, v[178:179]
	flat_store_dwordx4 v[148:149], v[144:147]
; __device__ __forceinline__ f32x4 u8x4_f32(unsigned w) { return (f32x4){(float)(w & 0xffu), (float)((w >> 8) & 0xffu), (float)((w >> 16) & 0xffu), (float)(w >> 24)}; }
; __device__ __forceinline__ unsigned pk4_fp8(float a, float b, float c, float d) { int w = 0; w = __builtin_amdgcn_cvt_pk_fp8_f32(clamp8(a), clamp8(b), w, false); w = __builtin_amdgcn_cvt_pk_fp8_f32(clamp8(c), clamp8(d), w, true); return (unsigned)w; }
; __host__ __device__ __forceinline__ size_t tiled_off(size_t r, int kb, int ktiles) { return (((r >> 8) * ktiles + (kb >> 7)) << 15) + ((r & 255) << 7) + (kb & 127); }
;     __device__ __forceinline__ void operator()(f32x4 (&acc)[2][2][4][2], const GUnit& u, int wr, int wc, int fr, int fq) const {
;     ...
; #pragma unroll
;             for (int m = 0; m < 4; ++m) { u32x4 w;
; #pragma unroll
;                 for (int q = 0; q < 4; ++q) { const f32x4 f = u8x4_f32(qf[m][q]); const f32x4 a = acc[ai][q >> 1][m][q & 1]; f32x4 v;
; #pragma unroll
;                     for (int j = 0; j < 4; ++j) v[j] = a[j] * (fmaxf(f[j], 0.5f) * (W8_INV / 255.0f));
;                     w[q] = pk4_fp8(v[0], v[1], v[2], v[3]); }
;                 *(u32x4*)(M8 + tiled_off((size_t)(u.x0 * 256 + wr * 64 + fr + ai * 128 + m * 16), u.x1 * 256 + wc * 64 + 16 * fq, D / 128)) = w; }
	v_cvt_f32_ubyte0_e32 v10, v6
	v_max_f32_e32 v10, 0.5, v10
	v_cvt_f32_ubyte1_e32 v144, v6
	v_max_f32_e32 v144, 0.5, v144
	v_cvt_f32_ubyte2_e32 v145, v6
	v_cvt_f32_ubyte3_e32 v6, v6
	v_mul_f32_e32 v10, 0x38808081, v10
	v_mul_f32_e32 v144, 0x38808081, v144
	v_mul_f32_e32 v10, v58, v10
	v_mul_f32_e32 v144, v59, v144
	v_max_f32_e32 v6, 0.5, v6
	v_mul_f32_e32 v146, 0x38808081, v6
	v_med3_f32 v10, v10, s60, v200
	v_med3_f32 v144, v144, s60, v200
	v_mov_b32_e32 v6, v11
	v_max_f32_e32 v145, 0.5, v145
	v_cvt_pk_fp8_f32 v6, v10, v144
	v_mul_f32_e32 v145, 0x38808081, v145
	v_mul_f32_e32 v145, v60, v145
	v_mul_f32_e32 v10, v61, v146
	v_med3_f32 v144, v145, s60, v200
	v_med3_f32 v10, v10, s60, v200
	v_cvt_pk_fp8_f32 v6, v144, v10 op_sel:[0,0,1]
	v_cvt_f32_ubyte0_e32 v10, v7
	v_cvt_f32_ubyte1_e32 v144, v7
	v_max_f32_e32 v10, 0.5, v10
	v_max_f32_e32 v144, 0.5, v144
	v_cvt_f32_ubyte2_e32 v145, v7
	v_cvt_f32_ubyte3_e32 v7, v7
	v_mul_f32_e32 v10, 0x38808081, v10
	v_mul_f32_e32 v144, 0x38808081, v144
	v_mul_f32_e32 v10, v54, v10
	v_mul_f32_e32 v144, v55, v144
	v_max_f32_e32 v7, 0.5, v7
	v_mul_f32_e32 v146, 0x38808081, v7
	v_med3_f32 v10, v10, s60, v200
	v_med3_f32 v144, v144, s60, v200
	v_mov_b32_e32 v7, v11
	v_max_f32_e32 v145, 0.5, v145
	v_cvt_pk_fp8_f32 v7, v10, v144
	v_mul_f32_e32 v145, 0x38808081, v145
	v_mul_f32_e32 v145, v56, v145
	v_mul_f32_e32 v10, v57, v146
	v_med3_f32 v144, v145, s60, v200
	v_med3_f32 v10, v10, s60, v200
	v_cvt_pk_fp8_f32 v7, v144, v10 op_sel:[0,0,1]
	v_cvt_f32_ubyte0_e32 v10, v8
	v_cvt_f32_ubyte1_e32 v144, v8
	v_max_f32_e32 v10, 0.5, v10
	v_max_f32_e32 v144, 0.5, v144
	v_cvt_f32_ubyte2_e32 v145, v8
	v_cvt_f32_ubyte3_e32 v8, v8
	v_mul_f32_e32 v10, 0x38808081, v10
	v_mul_f32_e32 v144, 0x38808081, v144
	v_mul_f32_e32 v10, v26, v10
	v_mul_f32_e32 v144, v27, v144
	v_max_f32_e32 v8, 0.5, v8
	v_mul_f32_e32 v146, 0x38808081, v8
	v_med3_f32 v10, v10, s60, v200
	v_med3_f32 v144, v144, s60, v200
	v_mov_b32_e32 v8, v11
	v_max_f32_e32 v145, 0.5, v145
	v_cvt_pk_fp8_f32 v8, v10, v144
	v_mul_f32_e32 v145, 0x38808081, v145
	v_mul_f32_e32 v145, v28, v145
	v_mul_f32_e32 v10, v29, v146
	v_med3_f32 v144, v145, s60, v200
	v_med3_f32 v10, v10, s60, v200
	v_cvt_pk_fp8_f32 v8, v144, v10 op_sel:[0,0,1]
	v_cvt_f32_ubyte0_e32 v10, v9
	v_cvt_f32_ubyte1_e32 v144, v9
	v_max_f32_e32 v10, 0.5, v10
	v_max_f32_e32 v144, 0.5, v144
	v_cvt_f32_ubyte2_e32 v145, v9
	v_cvt_f32_ubyte3_e32 v9, v9
	v_mul_f32_e32 v10, 0x38808081, v10
	v_mul_f32_e32 v144, 0x38808081, v144
	v_mul_f32_e32 v10, v22, v10
	v_mul_f32_e32 v144, v23, v144
	v_max_f32_e32 v9, 0.5, v9
	v_mul_f32_e32 v146, 0x38808081, v9
	v_med3_f32 v10, v10, s60, v200
	v_med3_f32 v144, v144, s60, v200
	v_mov_b32_e32 v9, v11
	v_max_f32_e32 v145, 0.5, v145
	v_cvt_pk_fp8_f32 v9, v10, v144
	v_mul_f32_e32 v145, 0x38808081, v145
	v_mul_f32_e32 v145, v24, v145
	v_mul_f32_e32 v10, v25, v146
	v_med3_f32 v144, v145, s60, v200
	v_med3_f32 v10, v10, s60, v200
	v_cvt_pk_fp8_f32 v9, v144, v10 op_sel:[0,0,1]
	v_add_u32_e32 v144, s28, v196
	v_ashrrev_i32_e32 v145, 31, v144
	v_lshrrev_b64 v[146:147], 4, v[144:145]
	v_and_b32_e32 v147, 0x1ffff, v147
	v_and_b32_e32 v146, -16, v146
	v_lshl_add_u64 v[146:147], v[146:147], 0, s[26:27]
	v_lshlrev_b64 v[146:147], 15, v[146:147]
	v_lshlrev_b32_e32 v10, 7, v144
	v_and_b32_e32 v10, 0x7f80, v10
	v_lshl_add_u64 v[144:145], s[12:13], 0, v[146:147]
	v_lshl_add_u64 v[144:145], v[144:145], 0, v[10:11]
	v_lshl_add_u64 v[144:145], v[144:145], 0, v[178:179]
	flat_store_dwordx4 v[144:145], v[6:9]
	s_nop 1
	v_cvt_f32_ubyte0_e32 v6, v2
	v_cvt_f32_ubyte1_e32 v7, v2
	v_max_f32_e32 v6, 0.5, v6
	v_max_f32_e32 v7, 0.5, v7
	v_cvt_f32_ubyte2_e32 v8, v2
	v_cvt_f32_ubyte3_e32 v2, v2
	v_mul_f32_e32 v6, 0x38808081, v6
	v_mul_f32_e32 v7, 0x38808081, v7
	v_mul_f32_e32 v6, v50, v6
	v_mul_f32_e32 v7, v51, v7
	v_max_f32_e32 v2, 0.5, v2
	v_mul_f32_e32 v9, 0x38808081, v2
	v_med3_f32 v6, v6, s60, v200
	v_med3_f32 v7, v7, s60, v200
	v_mov_b32_e32 v2, v11
	v_max_f32_e32 v8, 0.5, v8
	v_cvt_pk_fp8_f32 v2, v6, v7
	v_mul_f32_e32 v8, 0x38808081, v8
	v_mul_f32_e32 v8, v52, v8
	v_mul_f32_e32 v6, v53, v9
	v_med3_f32 v7, v8, s60, v200
	v_med3_f32 v6, v6, s60, v200
	v_cvt_pk_fp8_f32 v2, v7, v6 op_sel:[0,0,1]
	v_cvt_f32_ubyte0_e32 v6, v3
	v_cvt_f32_ubyte1_e32 v7, v3
	v_max_f32_e32 v6, 0.5, v6
	v_max_f32_e32 v7, 0.5, v7
	v_cvt_f32_ubyte2_e32 v8, v3
	v_cvt_f32_ubyte3_e32 v3, v3
	v_mul_f32_e32 v6, 0x38808081, v6
	v_mul_f32_e32 v7, 0x38808081, v7
	v_mul_f32_e32 v6, v46, v6
	v_mul_f32_e32 v7, v47, v7
	v_max_f32_e32 v3, 0.5, v3
	v_mul_f32_e32 v9, 0x38808081, v3
	v_med3_f32 v6, v6, s60, v200
	v_med3_f32 v7, v7, s60, v200
	v_mov_b32_e32 v3, v11
	v_max_f32_e32 v8, 0.5, v8
	v_cvt_pk_fp8_f32 v3, v6, v7
	v_mul_f32_e32 v8, 0x38808081, v8
	v_mul_f32_e32 v8, v48, v8
	v_mul_f32_e32 v6, v49, v9
	v_med3_f32 v7, v8, s60, v200
	v_med3_f32 v6, v6, s60, v200
	v_cvt_pk_fp8_f32 v3, v7, v6 op_sel:[0,0,1]
	v_cvt_f32_ubyte0_e32 v6, v4
	v_cvt_f32_ubyte1_e32 v7, v4
	v_max_f32_e32 v6, 0.5, v6
	v_max_f32_e32 v7, 0.5, v7
	v_cvt_f32_ubyte2_e32 v8, v4
	v_cvt_f32_ubyte3_e32 v4, v4
	v_mul_f32_e32 v6, 0x38808081, v6
	v_mul_f32_e32 v7, 0x38808081, v7
	v_mul_f32_e32 v6, v18, v6
	v_mul_f32_e32 v7, v19, v7
	v_max_f32_e32 v4, 0.5, v4
	v_mul_f32_e32 v9, 0x38808081, v4
	v_med3_f32 v6, v6, s60, v200
	v_med3_f32 v7, v7, s60, v200
	v_mov_b32_e32 v4, v11
	v_max_f32_e32 v8, 0.5, v8
	v_cvt_pk_fp8_f32 v4, v6, v7
	v_mul_f32_e32 v8, 0x38808081, v8
	v_mul_f32_e32 v8, v20, v8
	v_mul_f32_e32 v6, v21, v9
	v_med3_f32 v7, v8, s60, v200
	v_med3_f32 v6, v6, s60, v200
	v_cvt_pk_fp8_f32 v4, v7, v6 op_sel:[0,0,1]
	v_cvt_f32_ubyte0_e32 v6, v5
	v_cvt_f32_ubyte1_e32 v7, v5
	v_max_f32_e32 v6, 0.5, v6
	v_max_f32_e32 v7, 0.5, v7
	v_cvt_f32_ubyte2_e32 v8, v5
	v_cvt_f32_ubyte3_e32 v5, v5
	v_mul_f32_e32 v6, 0x38808081, v6
	v_mul_f32_e32 v7, 0x38808081, v7
	v_mul_f32_e32 v6, v14, v6
	v_mul_f32_e32 v7, v15, v7
	v_max_f32_e32 v5, 0.5, v5
	v_mul_f32_e32 v9, 0x38808081, v5
	v_med3_f32 v6, v6, s60, v200
	v_med3_f32 v7, v7, s60, v200
	v_mov_b32_e32 v5, v11
	v_max_f32_e32 v8, 0.5, v8
	v_cvt_pk_fp8_f32 v5, v6, v7
	v_mul_f32_e32 v8, 0x38808081, v8
	v_mul_f32_e32 v8, v16, v8
	v_mul_f32_e32 v6, v17, v9
	v_med3_f32 v7, v8, s60, v200
	v_med3_f32 v6, v6, s60, v200
	v_cvt_pk_fp8_f32 v5, v7, v6 op_sel:[0,0,1]
	v_add_u32_e32 v6, s28, v197
	v_ashrrev_i32_e32 v7, 31, v6
	v_lshrrev_b64 v[8:9], 4, v[6:7]
	v_and_b32_e32 v9, 0x1ffff, v9
	v_and_b32_e32 v8, -16, v8
	v_lshl_add_u64 v[8:9], v[8:9], 0, s[26:27]
	v_lshlrev_b64 v[8:9], 15, v[8:9]
	v_lshlrev_b32_e32 v6, 7, v6
	v_and_b32_e32 v10, 0x7f80, v6
	v_lshl_add_u64 v[6:7], s[12:13], 0, v[8:9]
	v_lshl_add_u64 v[6:7], v[6:7], 0, v[10:11]
	v_lshl_add_u64 v[6:7], v[6:7], 0, v[178:179]
	flat_store_dwordx4 v[6:7], v[2:5]
	s_cbranch_execnz .LBB0_840

; #define PG8_STAGE(bufoff, gbase, voff) do { _Pragma("unroll") for (int _i = 0; _i < 2; ++_i) \
;         __builtin_amdgcn_global_load_lds((const unsigned*)((const char*)(gbase) + (voff)[_i]), (PG8_LAS unsigned*)(lds + (bufoff) + ldsw + _i * 8192), 16, 0, 0); } while (0)
; #define PG8_WAIT_V(n) asm volatile("s_waitcnt vmcnt(" #n ")" ::: "memory")
; #define PG8_WAIT_L(n) asm volatile("s_waitcnt lgkmcnt(" #n ")" ::: "memory")
; template <class Epi, class Sched, bool ALIGN_EPI = true, bool F8 = false>
; __device__ __forceinline__ void gemm_phase(PG8_LAS unsigned char* lds, const Sched& S, const Epi& E) {
;     ...
;         for (int t = 0; t < nt; t += 2) {
;             const bool last = (t == nt - 2);
;             if constexpr (Sched::GATHER) { if (last && has_next) S.a_off(nxt, Rs, Cs, voffAn); }
;             const char* a1 = cA + (size_t)(t + 1) * kstep;
;             const char* a2 = last ? nA : cA + (size_t)(t + 2) * kstep; const char* b2 = last ? nB : cB + (size_t)(t + 2) * kstepB;
;             const char* a3 = a2 + kstep; const char* b3 = b2 + kstepB;
;             unsigned vA2[2][2];
; #pragma unroll
;             for (int h = 0; h < 2; ++h)
; #pragma unroll
;                 for (int i = 0; i < 2; ++i) { if constexpr (Sched::GATHER) vA2[h][i] = (last && has_next) ? voffAn[h][i] : voffA[h][i]; else vA2[h][i] = voffA[h][i]; }
;             PG8_LDB(B0, 0, 0); PG8_LDB(B1, 0, 1); PG8_SCHED; PG8_LDA(At, 0, 0); PG8_STAGE(PG8_SA(1, 1), a1, voffA[1]);
;             PG8_WAIT_V(8); PG8_WAIT_L(0); PG8_BAR; PG8_MMA(0, 0, At, B0); PG8_MMA(0, 1, At, B1); PG8_BAR; PG8_SCHED;
;             PG8_LDA(At, 0, 1); PG8_STAGE(PG8_SB(0, 0), b2, voffB[0]); PG8_STAGE(PG8_SB(0, 1), b2, voffB[1]); PG8_STAGE(PG8_SA(0, 0), a2, vA2[0]);
;             PG8_WAIT_V(8); PG8_WAIT_L(0); PG8_BAR; PG8_MMA(1, 0, At, B0); PG8_MMA(1, 1, At, B1); PG8_BAR; PG8_SCHED;
;             PG8_LDB(B0, 1, 0); PG8_LDB(B1, 1, 1); PG8_SCHED; PG8_LDA(At, 1, 0); PG8_STAGE(PG8_SA(0, 1), a2, vA2[1]);
;             PG8_WAIT_V(8); PG8_WAIT_L(0); PG8_BAR; PG8_MMA(0, 0, At, B0); PG8_MMA(0, 1, At, B1); PG8_BAR; PG8_SCHED;
;             PG8_LDA(At, 1, 1); PG8_STAGE(PG8_SB(1, 0), b3, voffB[0]); PG8_STAGE(PG8_SB(1, 1), b3, voffB[1]); PG8_STAGE(PG8_SA(1, 0), a3, vA2[0]);
;             PG8_WAIT_V(8); PG8_WAIT_L(0); PG8_BAR; PG8_MMA(1, 0, At, B0); PG8_MMA(1, 1, At, B1); PG8_BAR; PG8_SCHED;
.Lh1e_26630:
.Lh1_911:
	ds_read_b128 v[18:21], v191
	ds_read_b128 v[22:25], v191 offset:1024
	ds_read_b128 v[26:29], v191 offset:2048
	ds_read_b128 v[30:33], v191 offset:3072
	ds_read_b128 v[2:5], v192
	ds_read_b128 v[6:9], v192 offset:1024
	ds_read_b128 v[10:13], v192 offset:2048
	ds_read_b128 v[14:17], v192 offset:3072
	s_add_u32 s30, s28, 0x8000
	s_addc_u32 s31, s29, 0
	s_cmp_eq_u32 s65, 12
	s_cselect_b32 s42, s22, s30
	s_cselect_b32 s43, s23, s31
	s_cselect_b32 s40, s24, s19
	s_cselect_b32 s41, s25, s21
	s_add_u32 s30, s42, 0x8000
	s_addc_u32 s31, s43, 0
	v_lshl_add_u64 v[228:229], s[28:29], 0, v[182:183]
	s_add_i32 m0, s27, 0xc000
	ds_read_b128 v[196:199], v193
	ds_read_b128 v[200:203], v193 offset:1024
	ds_read_b128 v[204:207], v193 offset:2048
	ds_read_b128 v[208:211], v193 offset:3072
	ds_read_b128 v[212:215], v193 offset:4096
	ds_read_b128 v[216:219], v193 offset:5120
	ds_read_b128 v[220:223], v193 offset:6144
	ds_read_b128 v[224:227], v193 offset:7168
	global_load_lds_dwordx4 v[228:229], off
	v_lshl_add_u64 v[228:229], s[28:29], 0, v[180:181]
	s_add_i32 m0, s27, 0xe000
	s_nop 0
	global_load_lds_dwordx4 v[228:229], off
	s_waitcnt vmcnt(8)
	s_waitcnt lgkmcnt(0)
	s_barrier
	s_setprio 2
	s_waitcnt lgkmcnt(0)
	v_mfma_scale_f32_16x16x128_f8f6f4 v[158:161], v[18:25], v[196:203], v[158:161], v194, v194 op_sel_hi:[0,0,0]
	v_mfma_scale_f32_16x16x128_f8f6f4 v[154:157], v[26:33], v[196:203], v[154:157], v194, v194 op_sel_hi:[0,0,0]
	v_mfma_scale_f32_16x16x128_f8f6f4 v[150:153], v[18:25], v[204:211], v[150:153], v194, v194 op_sel_hi:[0,0,0]
	v_mfma_scale_f32_16x16x128_f8f6f4 v[146:149], v[26:33], v[204:211], v[146:149], v194, v194 op_sel_hi:[0,0,0]
	v_mfma_scale_f32_16x16x128_f8f6f4 v[130:133], v[18:25], v[212:219], v[130:133], v194, v194 op_sel_hi:[0,0,0]
	v_mfma_scale_f32_16x16x128_f8f6f4 v[122:125], v[26:33], v[212:219], v[122:125], v194, v194 op_sel_hi:[0,0,0]
	v_mfma_scale_f32_16x16x128_f8f6f4 v[114:117], v[18:25], v[220:227], v[114:117], v194, v194 op_sel_hi:[0,0,0]
	v_mfma_scale_f32_16x16x128_f8f6f4 v[106:109], v[26:33], v[220:227], v[106:109], v194, v194 op_sel_hi:[0,0,0]
	s_nop 3
	s_setprio 0
	s_setprio 2
	v_mfma_scale_f32_16x16x128_f8f6f4 v[142:145], v[2:9], v[196:203], v[142:145], v194, v194 op_sel_hi:[0,0,0]
	v_mfma_scale_f32_16x16x128_f8f6f4 v[138:141], v[10:17], v[196:203], v[138:141], v194, v194 op_sel_hi:[0,0,0]
	v_mfma_scale_f32_16x16x128_f8f6f4 v[134:137], v[2:9], v[204:211], v[134:137], v194, v194 op_sel_hi:[0,0,0]
	v_mfma_scale_f32_16x16x128_f8f6f4 v[126:129], v[10:17], v[204:211], v[126:129], v194, v194 op_sel_hi:[0,0,0]
	v_mfma_scale_f32_16x16x128_f8f6f4 v[118:121], v[2:9], v[212:219], v[118:121], v194, v194 op_sel_hi:[0,0,0]
	v_mfma_scale_f32_16x16x128_f8f6f4 v[110:113], v[10:17], v[212:219], v[110:113], v194, v194 op_sel_hi:[0,0,0]
	v_mfma_scale_f32_16x16x128_f8f6f4 v[102:105], v[2:9], v[220:227], v[102:105], v194, v194 op_sel_hi:[0,0,0]
	v_mfma_scale_f32_16x16x128_f8f6f4 v[98:101], v[10:17], v[220:227], v[98:101], v194, v194 op_sel_hi:[0,0,0]
	s_nop 3
	s_setprio 0
	s_add_i32 s66, s60, s48
	v_lshl_add_u64 v[228:229], s[40:41], 0, v[162:163]
	s_mov_b32 m0, s66
	ds_read_b128 v[196:199], v193 offset:16384
	ds_read_b128 v[200:203], v193 offset:17408
	ds_read_b128 v[204:207], v193 offset:18432
	ds_read_b128 v[208:211], v193 offset:19456
	ds_read_b128 v[212:215], v193 offset:20480
	ds_read_b128 v[216:219], v193 offset:21504
	ds_read_b128 v[220:223], v193 offset:22528
	ds_read_b128 v[224:227], v193 offset:23552
	global_load_lds_dwordx4 v[228:229], off
	v_lshl_add_u64 v[230:231], s[40:41], 0, v[164:165]
	s_add_i32 m0, s66, 0x2000
	s_add_i32 s66, s61, s48
	global_load_lds_dwordx4 v[230:231], off
	v_lshl_add_u64 v[228:229], v[228:229], 0, s[6:7]
	s_mov_b32 m0, s66
	s_nop 0
	global_load_lds_dwordx4 v[228:229], off
	v_lshl_add_u64 v[228:229], v[230:231], 0, s[6:7]
	s_add_i32 m0, s66, 0x2000
	s_nop 0
	global_load_lds_dwordx4 v[228:229], off
	v_lshl_add_u64 v[228:229], s[42:43], 0, v[166:167]
	s_mov_b32 m0, s27
	s_nop 0
	global_load_lds_dwordx4 v[228:229], off
	v_lshl_add_u64 v[228:229], s[42:43], 0, v[168:169]
	s_mov_b32 m0, s49
	s_nop 0
	global_load_lds_dwordx4 v[228:229], off
	s_waitcnt vmcnt(8)
	s_waitcnt lgkmcnt(0)
	s_barrier
	s_setprio 2
	s_waitcnt lgkmcnt(0)
	v_mfma_scale_f32_16x16x128_f8f6f4 v[94:97], v[18:25], v[196:203], v[94:97], v194, v194 op_sel_hi:[0,0,0]
	v_mfma_scale_f32_16x16x128_f8f6f4 v[90:93], v[26:33], v[196:203], v[90:93], v194, v194 op_sel_hi:[0,0,0]
	v_mfma_scale_f32_16x16x128_f8f6f4 v[82:85], v[18:25], v[204:211], v[82:85], v194, v194 op_sel_hi:[0,0,0]
	v_mfma_scale_f32_16x16x128_f8f6f4 v[74:77], v[26:33], v[204:211], v[74:77], v194, v194 op_sel_hi:[0,0,0]
	v_mfma_scale_f32_16x16x128_f8f6f4 v[66:69], v[18:25], v[212:219], v[66:69], v194, v194 op_sel_hi:[0,0,0]
	v_mfma_scale_f32_16x16x128_f8f6f4 v[58:61], v[26:33], v[212:219], v[58:61], v194, v194 op_sel_hi:[0,0,0]
	v_mfma_scale_f32_16x16x128_f8f6f4 v[50:53], v[18:25], v[220:227], v[50:53], v194, v194 op_sel_hi:[0,0,0]
	v_mfma_scale_f32_16x16x128_f8f6f4 v[42:45], v[26:33], v[220:227], v[42:45], v194, v194 op_sel_hi:[0,0,0]
	s_nop 3
	s_setprio 0
	s_setprio 2
	v_mfma_scale_f32_16x16x128_f8f6f4 v[86:89], v[2:9], v[196:203], v[86:89], v194, v194 op_sel_hi:[0,0,0]
	v_mfma_scale_f32_16x16x128_f8f6f4 v[78:81], v[10:17], v[196:203], v[78:81], v194, v194 op_sel_hi:[0,0,0]
	v_mfma_scale_f32_16x16x128_f8f6f4 v[70:73], v[2:9], v[204:211], v[70:73], v194, v194 op_sel_hi:[0,0,0]
	v_mfma_scale_f32_16x16x128_f8f6f4 v[62:65], v[10:17], v[204:211], v[62:65], v194, v194 op_sel_hi:[0,0,0]
	v_mfma_scale_f32_16x16x128_f8f6f4 v[54:57], v[2:9], v[212:219], v[54:57], v194, v194 op_sel_hi:[0,0,0]
	v_mfma_scale_f32_16x16x128_f8f6f4 v[46:49], v[10:17], v[212:219], v[46:49], v194, v194 op_sel_hi:[0,0,0]
	v_mfma_scale_f32_16x16x128_f8f6f4 v[38:41], v[2:9], v[220:227], v[38:41], v194, v194 op_sel_hi:[0,0,0]
	v_mfma_scale_f32_16x16x128_f8f6f4 v[34:37], v[10:17], v[220:227], v[34:37], v194, v194 op_sel_hi:[0,0,0]
	s_nop 3
	s_setprio 0
	s_add_i32 s66, 0, 0x18000
	s_add_i32 s67, 0, 0x1c000
	v_add_u32_e32 v14, s66, v189
	v_add_u32_e32 v30, s67, v189
	ds_read_b128 v[2:5], v14
	ds_read_b128 v[6:9], v14 offset:1024
	ds_read_b128 v[10:13], v14 offset:2048
	ds_read_b128 v[14:17], v14 offset:3072
	ds_read_b128 v[18:21], v30
	ds_read_b128 v[22:25], v30 offset:1024
	ds_read_b128 v[26:29], v30 offset:2048
	ds_read_b128 v[30:33], v30 offset:3072
	s_mov_b32 m0, s50
	v_lshl_add_u64 v[228:229], s[42:43], 0, v[172:173]
	ds_read_b128 v[196:199], v193 offset:32768
	ds_read_b128 v[200:203], v193 offset:33792
	ds_read_b128 v[204:207], v193 offset:34816
	ds_read_b128 v[208:211], v193 offset:35840
	ds_read_b128 v[212:215], v193 offset:36864
	ds_read_b128 v[216:219], v193 offset:37888
	ds_read_b128 v[220:223], v193 offset:38912
	ds_read_b128 v[224:227], v193 offset:39936
	global_load_lds_dwordx4 v[228:229], off
	v_lshl_add_u64 v[228:229], s[42:43], 0, v[174:175]
	s_mov_b32 m0, s51
	s_nop 0
	global_load_lds_dwordx4 v[228:229], off
	s_waitcnt vmcnt(8)
	s_waitcnt lgkmcnt(0)
	s_barrier
; #define PG8_STAGE(bufoff, gbase, voff) do { _Pragma("unroll") for (int _i = 0; _i < 2; ++_i) \
;         __builtin_amdgcn_global_load_lds((const unsigned*)((const char*)(gbase) + (voff)[_i]), (PG8_LAS unsigned*)(lds + (bufoff) + ldsw + _i * 8192), 16, 0, 0); } while (0)
; #define PG8_WAIT_V(n) asm volatile("s_waitcnt vmcnt(" #n ")" ::: "memory")
; #define PG8_WAIT_L(n) asm volatile("s_waitcnt lgkmcnt(" #n ")" ::: "memory")
; template <class Epi, class Sched, bool ALIGN_EPI = true, bool F8 = false>
; __device__ __forceinline__ void gemm_phase(PG8_LAS unsigned char* lds, const Sched& S, const Epi& E) {
;     ...
;         for (int t = 0; t < nt; t += 2) {
;             const bool last = (t == nt - 2);
;             if constexpr (Sched::GATHER) { if (last && has_next) S.a_off(nxt, Rs, Cs, voffAn); }
;             const char* a1 = cA + (size_t)(t + 1) * kstep;
;             const char* a2 = last ? nA : cA + (size_t)(t + 2) * kstep; const char* b2 = last ? nB : cB + (size_t)(t + 2) * kstepB;
;             const char* a3 = a2 + kstep; const char* b3 = b2 + kstepB;
;             unsigned vA2[2][2];
; #pragma unroll
;             for (int h = 0; h < 2; ++h)
; #pragma unroll
;                 for (int i = 0; i < 2; ++i) { if constexpr (Sched::GATHER) vA2[h][i] = (last && has_next) ? voffAn[h][i] : voffA[h][i]; else vA2[h][i] = voffA[h][i]; }
;             PG8_LDB(B0, 0, 0); PG8_LDB(B1, 0, 1); PG8_SCHED; PG8_LDA(At, 0, 0); PG8_STAGE(PG8_SA(1, 1), a1, voffA[1]);
;             PG8_WAIT_V(8); PG8_WAIT_L(0); PG8_BAR; PG8_MMA(0, 0, At, B0); PG8_MMA(0, 1, At, B1); PG8_BAR; PG8_SCHED;
;             PG8_LDA(At, 0, 1); PG8_STAGE(PG8_SB(0, 0), b2, voffB[0]); PG8_STAGE(PG8_SB(0, 1), b2, voffB[1]); PG8_STAGE(PG8_SA(0, 0), a2, vA2[0]);
;             PG8_WAIT_V(8); PG8_WAIT_L(0); PG8_BAR; PG8_MMA(1, 0, At, B0); PG8_MMA(1, 1, At, B1); PG8_BAR; PG8_SCHED;
;             PG8_LDB(B0, 1, 0); PG8_LDB(B1, 1, 1); PG8_SCHED; PG8_LDA(At, 1, 0); PG8_STAGE(PG8_SA(0, 1), a2, vA2[1]);
;             PG8_WAIT_V(8); PG8_WAIT_L(0); PG8_BAR; PG8_MMA(0, 0, At, B0); PG8_MMA(0, 1, At, B1); PG8_BAR; PG8_SCHED;
;             PG8_LDA(At, 1, 1); PG8_STAGE(PG8_SB(1, 0), b3, voffB[0]); PG8_STAGE(PG8_SB(1, 1), b3, voffB[1]); PG8_STAGE(PG8_SA(1, 0), a3, vA2[0]);
;             PG8_WAIT_V(8); PG8_WAIT_L(0); PG8_BAR; PG8_MMA(1, 0, At, B0); PG8_MMA(1, 1, At, B1); PG8_BAR; PG8_SCHED;
	s_setprio 2
	s_waitcnt lgkmcnt(0)
	v_mfma_scale_f32_16x16x128_f8f6f4 v[158:161], v[2:9], v[196:203], v[158:161], v194, v194 op_sel_hi:[0,0,0]
	v_mfma_scale_f32_16x16x128_f8f6f4 v[154:157], v[10:17], v[196:203], v[154:157], v194, v194 op_sel_hi:[0,0,0]
	v_mfma_scale_f32_16x16x128_f8f6f4 v[150:153], v[2:9], v[204:211], v[150:153], v194, v194 op_sel_hi:[0,0,0]
	v_mfma_scale_f32_16x16x128_f8f6f4 v[146:149], v[10:17], v[204:211], v[146:149], v194, v194 op_sel_hi:[0,0,0]
	v_mfma_scale_f32_16x16x128_f8f6f4 v[130:133], v[2:9], v[212:219], v[130:133], v194, v194 op_sel_hi:[0,0,0]
	v_mfma_scale_f32_16x16x128_f8f6f4 v[122:125], v[10:17], v[212:219], v[122:125], v194, v194 op_sel_hi:[0,0,0]
	v_mfma_scale_f32_16x16x128_f8f6f4 v[114:117], v[2:9], v[220:227], v[114:117], v194, v194 op_sel_hi:[0,0,0]
	v_mfma_scale_f32_16x16x128_f8f6f4 v[106:109], v[10:17], v[220:227], v[106:109], v194, v194 op_sel_hi:[0,0,0]
	s_nop 3
	s_setprio 0
	s_setprio 2
	v_mfma_scale_f32_16x16x128_f8f6f4 v[142:145], v[18:25], v[196:203], v[142:145], v194, v194 op_sel_hi:[0,0,0]
	v_mfma_scale_f32_16x16x128_f8f6f4 v[138:141], v[26:33], v[196:203], v[138:141], v194, v194 op_sel_hi:[0,0,0]
	v_mfma_scale_f32_16x16x128_f8f6f4 v[134:137], v[18:25], v[204:211], v[134:137], v194, v194 op_sel_hi:[0,0,0]
	v_mfma_scale_f32_16x16x128_f8f6f4 v[126:129], v[26:33], v[204:211], v[126:129], v194, v194 op_sel_hi:[0,0,0]
	v_mfma_scale_f32_16x16x128_f8f6f4 v[118:121], v[18:25], v[212:219], v[118:121], v194, v194 op_sel_hi:[0,0,0]
	v_mfma_scale_f32_16x16x128_f8f6f4 v[110:113], v[26:33], v[212:219], v[110:113], v194, v194 op_sel_hi:[0,0,0]
	v_mfma_scale_f32_16x16x128_f8f6f4 v[102:105], v[18:25], v[220:227], v[102:105], v194, v194 op_sel_hi:[0,0,0]
	v_mfma_scale_f32_16x16x128_f8f6f4 v[98:101], v[26:33], v[220:227], v[98:101], v194, v194 op_sel_hi:[0,0,0]
	s_nop 3
	s_setprio 0
	s_add_u32 s40, s40, 0x8000
	s_addc_u32 s41, s41, 0
	s_add_i32 s42, s66, s48
	v_lshl_add_u64 v[228:229], s[40:41], 0, v[162:163]
	s_mov_b32 m0, s42
	ds_read_b128 v[196:199], v193 offset:49152
	ds_read_b128 v[200:203], v193 offset:50176
	ds_read_b128 v[204:207], v193 offset:51200
	ds_read_b128 v[208:211], v193 offset:52224
	ds_read_b128 v[212:215], v193 offset:53248
	ds_read_b128 v[216:219], v193 offset:54272
	ds_read_b128 v[220:223], v193 offset:55296
	ds_read_b128 v[224:227], v193 offset:56320
	global_load_lds_dwordx4 v[228:229], off
	v_lshl_add_u64 v[228:229], s[40:41], 0, v[164:165]
	s_add_i32 m0, s42, 0x2000
	s_add_i32 s42, s67, s48
	global_load_lds_dwordx4 v[228:229], off
	v_lshl_add_u64 v[228:229], s[40:41], 0, v[176:177]
	s_mov_b32 m0, s42
	s_nop 0
	global_load_lds_dwordx4 v[228:229], off
	v_lshl_add_u64 v[228:229], s[40:41], 0, v[178:179]
	s_add_i32 m0, s42, 0x2000
	s_nop 0
	global_load_lds_dwordx4 v[228:229], off
	v_lshl_add_u64 v[228:229], s[30:31], 0, v[166:167]
	s_mov_b32 m0, s53
	s_nop 0
	global_load_lds_dwordx4 v[228:229], off
	v_lshl_add_u64 v[228:229], s[30:31], 0, v[168:169]
	s_mov_b32 m0, s58
	s_nop 0
	global_load_lds_dwordx4 v[228:229], off
	s_waitcnt vmcnt(8)
	s_waitcnt lgkmcnt(0)
	s_barrier
	s_setprio 2
	s_waitcnt lgkmcnt(0)
	v_mfma_scale_f32_16x16x128_f8f6f4 v[94:97], v[2:9], v[196:203], v[94:97], v194, v194 op_sel_hi:[0,0,0]
	v_mfma_scale_f32_16x16x128_f8f6f4 v[90:93], v[10:17], v[196:203], v[90:93], v194, v194 op_sel_hi:[0,0,0]
	v_mfma_scale_f32_16x16x128_f8f6f4 v[82:85], v[2:9], v[204:211], v[82:85], v194, v194 op_sel_hi:[0,0,0]
	v_mfma_scale_f32_16x16x128_f8f6f4 v[74:77], v[10:17], v[204:211], v[74:77], v194, v194 op_sel_hi:[0,0,0]
	v_mfma_scale_f32_16x16x128_f8f6f4 v[66:69], v[2:9], v[212:219], v[66:69], v194, v194 op_sel_hi:[0,0,0]
	v_mfma_scale_f32_16x16x128_f8f6f4 v[58:61], v[10:17], v[212:219], v[58:61], v194, v194 op_sel_hi:[0,0,0]
	v_mfma_scale_f32_16x16x128_f8f6f4 v[50:53], v[2:9], v[220:227], v[50:53], v194, v194 op_sel_hi:[0,0,0]
	v_mfma_scale_f32_16x16x128_f8f6f4 v[42:45], v[10:17], v[220:227], v[42:45], v194, v194 op_sel_hi:[0,0,0]
	s_nop 3
	s_setprio 0
	s_setprio 2
	v_mfma_scale_f32_16x16x128_f8f6f4 v[86:89], v[18:25], v[196:203], v[86:89], v194, v194 op_sel_hi:[0,0,0]
	v_mfma_scale_f32_16x16x128_f8f6f4 v[78:81], v[26:33], v[196:203], v[78:81], v194, v194 op_sel_hi:[0,0,0]
	v_mfma_scale_f32_16x16x128_f8f6f4 v[70:73], v[18:25], v[204:211], v[70:73], v194, v194 op_sel_hi:[0,0,0]
	v_mfma_scale_f32_16x16x128_f8f6f4 v[62:65], v[26:33], v[204:211], v[62:65], v194, v194 op_sel_hi:[0,0,0]
	v_mfma_scale_f32_16x16x128_f8f6f4 v[54:57], v[18:25], v[212:219], v[54:57], v194, v194 op_sel_hi:[0,0,0]
	v_mfma_scale_f32_16x16x128_f8f6f4 v[46:49], v[26:33], v[212:219], v[46:49], v194, v194 op_sel_hi:[0,0,0]
	v_mfma_scale_f32_16x16x128_f8f6f4 v[38:41], v[18:25], v[220:227], v[38:41], v194, v194 op_sel_hi:[0,0,0]
	v_mfma_scale_f32_16x16x128_f8f6f4 v[34:37], v[26:33], v[220:227], v[34:37], v194, v194 op_sel_hi:[0,0,0]
	s_nop 3
	s_setprio 0
	s_add_i32 s65, s65, 2
	s_add_u32 s19, s19, 0x10000
	s_addc_u32 s21, s21, 0
	s_add_u32 s28, s28, 0x10000
	s_addc_u32 s29, s29, 0
	s_cmp_gt_u32 s65, 13
	s_cbranch_scc0 .Lh1_911

; __device__ __forceinline__ unsigned pk4_fp8(float a, float b, float c, float d) { int w = 0; w = __builtin_amdgcn_cvt_pk_fp8_f32(clamp8(a), clamp8(b), w, false); w = __builtin_amdgcn_cvt_pk_fp8_f32(clamp8(c), clamp8(d), w, true); return (unsigned)w; }
; template <class Epi, class Sched, bool ALIGN_EPI = true, bool F8 = false>
; __device__ __forceinline__ void gemm_phase(PG8_LAS unsigned char* lds, const Sched& S, const Epi& E) {
;     ...
;         if constexpr (F8) {
; #pragma unroll
;             for (int a = 0; a < 2; ++a)
; #pragma unroll
;                 for (int b = 0; b < 2; ++b)
;                     asm volatile("s_nop 15\n\ts_nop 7" : "+v"(acc[a][b][0][0]), "+v"(acc[a][b][0][1]), "+v"(acc[a][b][1][0]), "+v"(acc[a][b][1][1]), "+v"(acc[a][b][2][0]), "+v"(acc[a][b][2][1]), "+v"(acc[a][b][3][0]), "+v"(acc[a][b][3][1]));
;     __device__ __forceinline__ void operator()(AccRef acc, const GUnit& u, int wr, int wc, int fr, int fq) const {
;         const int pm = u.x0, pn = u.x1; const float* gate = modv + (size_t)(pm >> 5) * 12288 + 2 * D;
;         const int col0 = pn * 256 + wc * 64 + 16 * fq;
;         f32x4 gv[4];
; #pragma unroll
;         for (int q = 0; q < 4; ++q) gv[q] = *(const f32x4*)(gate + col0 + 4 * q) * (W8_INV * MG8_SCALE);
; #pragma unroll
;         for (int ai = 0; ai < 2; ++ai)
; #pragma unroll
;             for (int m = 0; m < 4; ++m) { u32x4 w;
; #pragma unroll
;                 for (int q = 0; q < 4; ++q) { const f32x4 v = acc[ai][q >> 1][m][q & 1] * gv[q]; w[q] = pk4_fp8(v[0], v[1], v[2], v[3]); }
;                 *(u32x4*)(MG + (size_t)(pm * 256 + ai * 128 + wr * 64 + m * 16 + fr) * D + col0) = w; }
.LBB0_914:
	s_ashr_i32 s19, s26, 5
	s_mul_hi_i32 s21, s19, 0xc000
	s_mul_i32 s19, s19, 0xc000
	s_add_u32 s28, s36, s19
	v_lshl_or_b32 v2, s64, 8, v190
	s_addc_u32 s29, s37, s21
	v_ashrrev_i32_e32 v3, 31, v2
	v_lshl_add_u64 v[4:5], v[2:3], 2, s[28:29]
	v_add_co_u32_e32 v6, vcc, s62, v4
	s_nop 15
	s_nop 7
	s_nop 1
	v_addc_co_u32_e32 v7, vcc, 0, v5, vcc
	flat_load_dwordx4 v[6:9], v[6:7]
	v_lshl_add_u64 v[4:5], v[4:5], 0, s[14:15]
	flat_load_dwordx4 v[10:13], v[4:5] offset:16
	flat_load_dwordx4 v[22:25], v[4:5] offset:32
	flat_load_dwordx4 v[26:29], v[4:5] offset:48
	v_lshl_add_u32 v4, s26, 8, v188
	v_ashrrev_i32_e32 v5, 31, v4
	v_mov_b32_e32 v30, 0
	v_lshlrev_b64 v[14:15], 11, v[4:5]
	v_lshl_add_u64 v[14:15], s[10:11], 0, v[14:15]
	v_lshl_add_u64 v[200:201], v[14:15], 0, v[2:3]
	v_mov_b32_e32 v199, 0
	v_mov_b32_e32 v196, 0
	v_mov_b32_e32 v197, 0
	v_mov_b32_e32 v198, 0
	v_mov_b32_e32 v31, 0
	v_mov_b32_e32 v32, 0
	v_mov_b32_e32 v33, 0
	s_andn2_b64 vcc, exec, s[0:1]
	s_mov_b64 s[0:1], -1
	s_waitcnt vmcnt(0) lgkmcnt(0)
	v_pk_mul_f32 v[16:17], v[10:11], s[16:17] op_sel_hi:[1,0]
	v_pk_mul_f32 v[20:21], v[6:7], s[16:17] op_sel_hi:[1,0]
	v_pk_mul_f32 v[10:11], v[24:25], s[16:17] op_sel_hi:[1,0]
	v_pk_mul_f32 v[24:25], v[158:159], v[20:21]
	v_pk_mul_f32 v[18:19], v[8:9], s[16:17] op_sel_hi:[1,0]
	v_med3_f32 v5, v24, s63, v195
	v_med3_f32 v24, v25, s63, v195
	v_cvt_pk_fp8_f32 v30, v5, v24
	v_pk_mul_f32 v[14:15], v[12:13], s[16:17] op_sel_hi:[1,0]
	v_pk_mul_f32 v[12:13], v[22:23], s[16:17] op_sel_hi:[1,0]
	v_pk_mul_f32 v[22:23], v[160:161], v[18:19]
	v_pk_mul_f32 v[8:9], v[26:27], s[16:17] op_sel_hi:[1,0]
	v_med3_f32 v22, v22, s63, v195
	v_med3_f32 v23, v23, s63, v195
	v_cvt_pk_fp8_f32 v30, v22, v23 op_sel:[0,0,1]
	v_pk_mul_f32 v[22:23], v[126:127], v[8:9]
	v_pk_mul_f32 v[6:7], v[28:29], s[16:17] op_sel_hi:[1,0]
	v_pk_mul_f32 v[28:29], v[154:155], v[16:17]
	v_pk_mul_f32 v[144:145], v[144:145], v[10:11]
	v_pk_mul_f32 v[142:143], v[142:143], v[12:13]
	v_pk_mul_f32 v[150:151], v[150:151], v[20:21]
	v_pk_mul_f32 v[146:147], v[146:147], v[16:17]
	v_pk_mul_f32 v[134:135], v[134:135], v[12:13]
	v_med3_f32 v5, v22, s63, v195
	v_med3_f32 v22, v23, s63, v195
	v_med3_f32 v25, v28, s63, v195
	v_med3_f32 v28, v29, s63, v195
	v_med3_f32 v29, v142, s63, v195
	v_med3_f32 v142, v143, s63, v195
	v_med3_f32 v143, v144, s63, v195
	v_med3_f32 v144, v145, s63, v195
	v_med3_f32 v145, v150, s63, v195
	v_med3_f32 v150, v151, s63, v195
	v_med3_f32 v146, v146, s63, v195
	v_med3_f32 v147, v147, s63, v195
	v_med3_f32 v134, v134, s63, v195
	v_med3_f32 v135, v135, s63, v195
	v_cvt_pk_fp8_f32 v199, v5, v22
	v_cvt_pk_fp8_f32 v196, v145, v150
	v_cvt_pk_fp8_f32 v197, v146, v147
	v_cvt_pk_fp8_f32 v198, v134, v135
	v_pk_mul_f32 v[22:23], v[128:129], v[6:7]
	v_pk_mul_f32 v[152:153], v[152:153], v[18:19]
	v_pk_mul_f32 v[148:149], v[148:149], v[14:15]
	v_pk_mul_f32 v[136:137], v[136:137], v[10:11]
	v_med3_f32 v5, v22, s63, v195
	v_med3_f32 v22, v23, s63, v195
	v_med3_f32 v151, v152, s63, v195
	v_med3_f32 v152, v153, s63, v195
	v_med3_f32 v148, v148, s63, v195
	v_med3_f32 v149, v149, s63, v195
	v_med3_f32 v136, v136, s63, v195
	v_med3_f32 v137, v137, s63, v195
	v_cvt_pk_fp8_f32 v199, v5, v22 op_sel:[0,0,1]
	v_or_b32_e32 v22, 16, v4
	v_cvt_pk_fp8_f32 v196, v151, v152 op_sel:[0,0,1]
	v_cvt_pk_fp8_f32 v197, v148, v149 op_sel:[0,0,1]
	v_cvt_pk_fp8_f32 v198, v136, v137 op_sel:[0,0,1]
	v_ashrrev_i32_e32 v23, 31, v22
	v_lshlrev_b64 v[22:23], 11, v[22:23]
	v_lshl_add_u64 v[22:23], s[10:11], 0, v[22:23]
	v_lshl_add_u64 v[22:23], v[22:23], 0, v[2:3]
	flat_store_dwordx4 v[22:23], v[196:199]
	v_pk_mul_f32 v[22:23], v[130:131], v[20:21]
	v_cvt_pk_fp8_f32 v31, v25, v28
	v_med3_f32 v5, v22, s63, v195
	v_med3_f32 v23, v23, s63, v195
	v_mov_b32_e32 v22, 0
	v_cvt_pk_fp8_f32 v22, v5, v23
	v_pk_mul_f32 v[24:25], v[132:133], v[18:19]
	v_pk_mul_f32 v[26:27], v[156:157], v[14:15]
	v_med3_f32 v5, v24, s63, v195
	v_med3_f32 v23, v25, s63, v195
	v_pk_mul_f32 v[24:25], v[122:123], v[16:17]
	v_cvt_pk_fp8_f32 v22, v5, v23 op_sel:[0,0,1]
	v_med3_f32 v5, v24, s63, v195
	v_med3_f32 v24, v25, s63, v195
	v_mov_b32_e32 v23, 0
	v_cvt_pk_fp8_f32 v23, v5, v24
	v_pk_mul_f32 v[24:25], v[124:125], v[14:15]
	v_med3_f32 v26, v26, s63, v195
	v_med3_f32 v5, v24, s63, v195
	v_med3_f32 v24, v25, s63, v195
	v_cvt_pk_fp8_f32 v23, v5, v24 op_sel:[0,0,1]
	v_pk_mul_f32 v[24:25], v[118:119], v[12:13]
	v_med3_f32 v27, v27, s63, v195
	v_med3_f32 v5, v24, s63, v195
	v_med3_f32 v25, v25, s63, v195
	v_mov_b32_e32 v24, 0
	v_cvt_pk_fp8_f32 v24, v5, v25
	v_cvt_pk_fp8_f32 v31, v26, v27 op_sel:[0,0,1]
	v_pk_mul_f32 v[26:27], v[120:121], v[10:11]
	v_cvt_pk_fp8_f32 v32, v29, v142
	v_med3_f32 v5, v26, s63, v195
	v_med3_f32 v25, v27, s63, v195
	v_pk_mul_f32 v[26:27], v[110:111], v[8:9]
	v_cvt_pk_fp8_f32 v24, v5, v25 op_sel:[0,0,1]
	v_med3_f32 v5, v26, s63, v195
	v_med3_f32 v26, v27, s63, v195
	v_mov_b32_e32 v25, 0
	v_cvt_pk_fp8_f32 v25, v5, v26
	v_pk_mul_f32 v[26:27], v[112:113], v[6:7]
	v_pk_mul_f32 v[28:29], v[88:89], v[10:11]
	v_med3_f32 v5, v26, s63, v195
	v_med3_f32 v26, v27, s63, v195
	v_cvt_pk_fp8_f32 v25, v5, v26 op_sel:[0,0,1]
	v_or_b32_e32 v26, 32, v4
	v_ashrrev_i32_e32 v27, 31, v26
	v_lshlrev_b64 v[26:27], 11, v[26:27]
	v_lshl_add_u64 v[26:27], s[10:11], 0, v[26:27]
	v_lshl_add_u64 v[26:27], v[26:27], 0, v[2:3]
	flat_store_dwordx4 v[26:27], v[22:25]
	v_pk_mul_f32 v[26:27], v[104:105], v[10:11]
	v_pk_mul_f32 v[138:139], v[138:139], v[8:9]
	v_pk_mul_f32 v[22:23], v[114:115], v[20:21]
	v_pk_mul_f32 v[24:25], v[116:117], v[18:19]
	v_med3_f32 v5, v22, s63, v195
	v_med3_f32 v23, v23, s63, v195
	v_mov_b32_e32 v22, 0
	v_cvt_pk_fp8_f32 v22, v5, v23
; __device__ __forceinline__ unsigned pk4_fp8(float a, float b, float c, float d) { int w = 0; w = __builtin_amdgcn_cvt_pk_fp8_f32(clamp8(a), clamp8(b), w, false); w = __builtin_amdgcn_cvt_pk_fp8_f32(clamp8(c), clamp8(d), w, true); return (unsigned)w; }
;     __device__ __forceinline__ void operator()(AccRef acc, const GUnit& u, int wr, int wc, int fr, int fq) const {
;     ...
;         for (int ai = 0; ai < 2; ++ai)
; #pragma unroll
;             for (int m = 0; m < 4; ++m) { u32x4 w;
; #pragma unroll
;                 for (int q = 0; q < 4; ++q) { const f32x4 v = acc[ai][q >> 1][m][q & 1] * gv[q]; w[q] = pk4_fp8(v[0], v[1], v[2], v[3]); }
;                 *(u32x4*)(MG + (size_t)(pm * 256 + ai * 128 + wr * 64 + m * 16 + fr) * D + col0) = w; }
	v_med3_f32 v5, v24, s63, v195
	v_med3_f32 v23, v25, s63, v195
	v_pk_mul_f32 v[24:25], v[106:107], v[16:17]
	v_cvt_pk_fp8_f32 v22, v5, v23 op_sel:[0,0,1]
	v_med3_f32 v5, v24, s63, v195
	v_med3_f32 v24, v25, s63, v195
	v_mov_b32_e32 v23, 0
	v_cvt_pk_fp8_f32 v23, v5, v24
	v_pk_mul_f32 v[24:25], v[108:109], v[14:15]
	v_med3_f32 v138, v138, s63, v195
	v_med3_f32 v5, v24, s63, v195
	v_med3_f32 v24, v25, s63, v195
	v_cvt_pk_fp8_f32 v23, v5, v24 op_sel:[0,0,1]
	v_pk_mul_f32 v[24:25], v[102:103], v[12:13]
	v_med3_f32 v139, v139, s63, v195
	v_med3_f32 v5, v24, s63, v195
	v_med3_f32 v25, v25, s63, v195
	v_mov_b32_e32 v24, 0
	v_cvt_pk_fp8_f32 v24, v5, v25
	v_med3_f32 v5, v26, s63, v195
	v_med3_f32 v25, v27, s63, v195
	v_pk_mul_f32 v[26:27], v[98:99], v[8:9]
	v_cvt_pk_fp8_f32 v24, v5, v25 op_sel:[0,0,1]
	v_med3_f32 v5, v26, s63, v195
	v_med3_f32 v26, v27, s63, v195
	v_mov_b32_e32 v25, 0
	v_cvt_pk_fp8_f32 v25, v5, v26
	v_pk_mul_f32 v[26:27], v[100:101], v[6:7]
	v_cvt_pk_fp8_f32 v33, v138, v139
	v_med3_f32 v5, v26, s63, v195
	v_med3_f32 v26, v27, s63, v195
	v_cvt_pk_fp8_f32 v25, v5, v26 op_sel:[0,0,1]
	v_or_b32_e32 v26, 48, v4
	v_ashrrev_i32_e32 v27, 31, v26
	v_lshlrev_b64 v[26:27], 11, v[26:27]
	v_lshl_add_u64 v[26:27], s[10:11], 0, v[26:27]
	v_lshl_add_u64 v[26:27], v[26:27], 0, v[2:3]
	flat_store_dwordx4 v[26:27], v[22:25]
	v_add_u32_e32 v26, 0x80, v4
	v_pk_mul_f32 v[140:141], v[140:141], v[6:7]
	v_pk_mul_f32 v[22:23], v[94:95], v[20:21]
	v_pk_mul_f32 v[24:25], v[96:97], v[18:19]
	v_med3_f32 v5, v22, s63, v195
	v_med3_f32 v23, v23, s63, v195
	v_mov_b32_e32 v22, 0
	v_cvt_pk_fp8_f32 v22, v5, v23
	v_med3_f32 v5, v24, s63, v195
	v_med3_f32 v23, v25, s63, v195
	v_pk_mul_f32 v[24:25], v[90:91], v[16:17]
	v_cvt_pk_fp8_f32 v22, v5, v23 op_sel:[0,0,1]
	v_med3_f32 v5, v24, s63, v195
	v_med3_f32 v24, v25, s63, v195
	v_mov_b32_e32 v23, 0
	v_cvt_pk_fp8_f32 v23, v5, v24
	v_pk_mul_f32 v[24:25], v[92:93], v[14:15]
	v_med3_f32 v140, v140, s63, v195
	v_med3_f32 v5, v24, s63, v195
	v_med3_f32 v24, v25, s63, v195
	v_cvt_pk_fp8_f32 v23, v5, v24 op_sel:[0,0,1]
	v_pk_mul_f32 v[24:25], v[86:87], v[12:13]
	v_med3_f32 v141, v141, s63, v195
	v_med3_f32 v5, v24, s63, v195
	v_med3_f32 v25, v25, s63, v195
	v_mov_b32_e32 v24, 0
	v_cvt_pk_fp8_f32 v24, v5, v25
	v_med3_f32 v5, v28, s63, v195
	v_med3_f32 v25, v29, s63, v195
	v_pk_mul_f32 v[28:29], v[78:79], v[8:9]
	v_cvt_pk_fp8_f32 v24, v5, v25 op_sel:[0,0,1]
	v_med3_f32 v5, v28, s63, v195
	v_med3_f32 v27, v29, s63, v195
	v_mov_b32_e32 v25, 0
	v_cvt_pk_fp8_f32 v25, v5, v27
	v_pk_mul_f32 v[28:29], v[80:81], v[6:7]
	v_cvt_pk_fp8_f32 v32, v143, v144 op_sel:[0,0,1]
	v_med3_f32 v5, v28, s63, v195
	v_med3_f32 v27, v29, s63, v195
	v_cvt_pk_fp8_f32 v25, v5, v27 op_sel:[0,0,1]
	v_ashrrev_i32_e32 v27, 31, v26
	v_lshlrev_b64 v[26:27], 11, v[26:27]
	v_lshl_add_u64 v[26:27], s[10:11], 0, v[26:27]
	v_lshl_add_u64 v[26:27], v[26:27], 0, v[2:3]
	flat_store_dwordx4 v[26:27], v[22:25]
	v_pk_mul_f32 v[26:27], v[72:73], v[10:11]
	v_cvt_pk_fp8_f32 v33, v140, v141 op_sel:[0,0,1]
	v_pk_mul_f32 v[22:23], v[82:83], v[20:21]
	v_pk_mul_f32 v[24:25], v[84:85], v[18:19]
	v_med3_f32 v5, v22, s63, v195
	v_med3_f32 v23, v23, s63, v195
	v_mov_b32_e32 v22, 0
	v_cvt_pk_fp8_f32 v22, v5, v23
	v_med3_f32 v5, v24, s63, v195
	v_med3_f32 v23, v25, s63, v195
	v_pk_mul_f32 v[24:25], v[74:75], v[16:17]
	v_cvt_pk_fp8_f32 v22, v5, v23 op_sel:[0,0,1]
	v_med3_f32 v5, v24, s63, v195
	v_med3_f32 v24, v25, s63, v195
	v_mov_b32_e32 v23, 0
	v_cvt_pk_fp8_f32 v23, v5, v24
	v_pk_mul_f32 v[24:25], v[76:77], v[14:15]
	flat_store_dwordx4 v[200:201], v[30:33]
	v_med3_f32 v5, v24, s63, v195
	v_med3_f32 v24, v25, s63, v195
	v_cvt_pk_fp8_f32 v23, v5, v24 op_sel:[0,0,1]
	v_pk_mul_f32 v[24:25], v[70:71], v[12:13]
	s_nop 0
	v_med3_f32 v5, v24, s63, v195
; __device__ __forceinline__ unsigned pk4_fp8(float a, float b, float c, float d) { int w = 0; w = __builtin_amdgcn_cvt_pk_fp8_f32(clamp8(a), clamp8(b), w, false); w = __builtin_amdgcn_cvt_pk_fp8_f32(clamp8(c), clamp8(d), w, true); return (unsigned)w; }
;     __device__ __forceinline__ void operator()(AccRef acc, const GUnit& u, int wr, int wc, int fr, int fq) const {
;     ...
;         for (int ai = 0; ai < 2; ++ai)
; #pragma unroll
;             for (int m = 0; m < 4; ++m) { u32x4 w;
; #pragma unroll
;                 for (int q = 0; q < 4; ++q) { const f32x4 v = acc[ai][q >> 1][m][q & 1] * gv[q]; w[q] = pk4_fp8(v[0], v[1], v[2], v[3]); }
;                 *(u32x4*)(MG + (size_t)(pm * 256 + ai * 128 + wr * 64 + m * 16 + fr) * D + col0) = w; }
	v_med3_f32 v25, v25, s63, v195
	v_mov_b32_e32 v24, 0
	v_cvt_pk_fp8_f32 v24, v5, v25
	v_med3_f32 v5, v26, s63, v195
	v_med3_f32 v25, v27, s63, v195
	v_pk_mul_f32 v[26:27], v[62:63], v[8:9]
	v_cvt_pk_fp8_f32 v24, v5, v25 op_sel:[0,0,1]
	v_med3_f32 v5, v26, s63, v195
	v_med3_f32 v26, v27, s63, v195
	v_mov_b32_e32 v25, 0
	v_cvt_pk_fp8_f32 v25, v5, v26
	v_pk_mul_f32 v[26:27], v[64:65], v[6:7]
	s_nop 0
	v_med3_f32 v5, v26, s63, v195
	v_med3_f32 v26, v27, s63, v195
	v_cvt_pk_fp8_f32 v25, v5, v26 op_sel:[0,0,1]
	v_add_u32_e32 v26, 0x90, v4
	v_ashrrev_i32_e32 v27, 31, v26
	v_lshlrev_b64 v[26:27], 11, v[26:27]
	v_lshl_add_u64 v[26:27], s[10:11], 0, v[26:27]
	v_lshl_add_u64 v[26:27], v[26:27], 0, v[2:3]
	flat_store_dwordx4 v[26:27], v[22:25]
	v_pk_mul_f32 v[26:27], v[56:57], v[10:11]
	v_pk_mul_f32 v[10:11], v[40:41], v[10:11]
	v_pk_mul_f32 v[22:23], v[66:67], v[20:21]
	v_pk_mul_f32 v[24:25], v[68:69], v[18:19]
	v_med3_f32 v5, v22, s63, v195
	v_med3_f32 v23, v23, s63, v195
	v_mov_b32_e32 v22, 0
	v_cvt_pk_fp8_f32 v22, v5, v23
	v_med3_f32 v5, v24, s63, v195
	v_med3_f32 v23, v25, s63, v195
	v_pk_mul_f32 v[24:25], v[58:59], v[16:17]
	v_cvt_pk_fp8_f32 v22, v5, v23 op_sel:[0,0,1]
	v_med3_f32 v5, v24, s63, v195
	v_med3_f32 v24, v25, s63, v195
	v_mov_b32_e32 v23, 0
	v_cvt_pk_fp8_f32 v23, v5, v24
	v_pk_mul_f32 v[24:25], v[60:61], v[14:15]
	v_pk_mul_f32 v[20:21], v[50:51], v[20:21]
	v_med3_f32 v5, v24, s63, v195
	v_med3_f32 v24, v25, s63, v195
	v_cvt_pk_fp8_f32 v23, v5, v24 op_sel:[0,0,1]
	v_pk_mul_f32 v[24:25], v[54:55], v[12:13]
	v_med3_f32 v21, v21, s63, v195
	v_med3_f32 v5, v24, s63, v195
	v_med3_f32 v25, v25, s63, v195
	v_mov_b32_e32 v24, 0
	v_cvt_pk_fp8_f32 v24, v5, v25
	v_med3_f32 v5, v26, s63, v195
	v_med3_f32 v25, v27, s63, v195
	v_pk_mul_f32 v[26:27], v[46:47], v[8:9]
	v_cvt_pk_fp8_f32 v24, v5, v25 op_sel:[0,0,1]
	v_med3_f32 v5, v26, s63, v195
	v_med3_f32 v26, v27, s63, v195
	v_mov_b32_e32 v25, 0
	v_cvt_pk_fp8_f32 v25, v5, v26
	v_pk_mul_f32 v[26:27], v[48:49], v[6:7]
	v_pk_mul_f32 v[18:19], v[52:53], v[18:19]
	v_med3_f32 v5, v26, s63, v195
	v_med3_f32 v26, v27, s63, v195
	v_cvt_pk_fp8_f32 v25, v5, v26 op_sel:[0,0,1]
	v_med3_f32 v5, v20, s63, v195
	v_mov_b32_e32 v20, 0
	v_cvt_pk_fp8_f32 v20, v5, v21
	v_med3_f32 v5, v18, s63, v195
	v_med3_f32 v18, v19, s63, v195
	v_pk_mul_f32 v[16:17], v[42:43], v[16:17]
	v_add_u32_e32 v26, 0xa0, v4
	v_cvt_pk_fp8_f32 v20, v5, v18 op_sel:[0,0,1]
	v_med3_f32 v5, v16, s63, v195
	v_med3_f32 v16, v17, s63, v195
	v_mov_b32_e32 v21, 0
	v_ashrrev_i32_e32 v27, 31, v26
	v_cvt_pk_fp8_f32 v21, v5, v16
	v_lshlrev_b64 v[26:27], 11, v[26:27]
	v_lshl_add_u64 v[26:27], s[10:11], 0, v[26:27]
	v_pk_mul_f32 v[14:15], v[44:45], v[14:15]
	v_lshl_add_u64 v[26:27], v[26:27], 0, v[2:3]
	v_med3_f32 v5, v14, s63, v195
	v_med3_f32 v14, v15, s63, v195
	v_pk_mul_f32 v[12:13], v[38:39], v[12:13]
	flat_store_dwordx4 v[26:27], v[22:25]
	v_cvt_pk_fp8_f32 v21, v5, v14 op_sel:[0,0,1]
	v_med3_f32 v5, v12, s63, v195
	v_med3_f32 v12, v13, s63, v195
	v_mov_b32_e32 v22, 0
	v_cvt_pk_fp8_f32 v22, v5, v12
	v_med3_f32 v5, v10, s63, v195
	v_med3_f32 v10, v11, s63, v195
	v_pk_mul_f32 v[8:9], v[34:35], v[8:9]
	v_cvt_pk_fp8_f32 v22, v5, v10 op_sel:[0,0,1]
	v_med3_f32 v5, v8, s63, v195
	v_med3_f32 v8, v9, s63, v195
	v_mov_b32_e32 v23, 0
	v_cvt_pk_fp8_f32 v23, v5, v8
	v_pk_mul_f32 v[6:7], v[36:37], v[6:7]
	v_add_u32_e32 v4, 0xb0, v4
	v_med3_f32 v5, v6, s63, v195
	v_med3_f32 v6, v7, s63, v195
	v_cvt_pk_fp8_f32 v23, v5, v6 op_sel:[0,0,1]
	v_ashrrev_i32_e32 v5, 31, v4
	v_lshlrev_b64 v[4:5], 11, v[4:5]
	v_lshl_add_u64 v[4:5], s[10:11], 0, v[4:5]
	v_lshl_add_u64 v[2:3], v[4:5], 0, v[2:3]
	flat_store_dwordx4 v[2:3], v[20:23]
	s_cbranch_vccnz .LBB0_903
	s_andn2_b64 vcc, exec, s[8:9]
	s_cbranch_vccnz .LBB0_902
	s_branch .LBB0_902

; #define LAS __attribute__((address_space(3)))
; __device__ __forceinline__ void ph10(LAS unsigned char* lds, int tid, int lane, int wave, int G, int bid) {
;     ...
;             if (tid < 16) {
;                 const LAS float* L = Lg + tid * 36;
;                 float lg[4]; int gi = 0; float gm;
; #pragma unroll
;                 for (int i = 0; i < 4; ++i) lg[i] = L[i] + bgrp[i];
;                 gm = lg[0];
; #pragma unroll
;                 for (int i = 1; i < 4; ++i) if (lg[i] > gm) { gm = lg[i]; gi = i; }
;                 float gz = 0.f;
; #pragma unroll
;                 for (int i = 0; i < 4; ++i) gz += expf(lg[i] - gm);
;                 const float gtop = 1.0f / gz;
;                 float le[8]; int j0 = 0; float m0;
; #pragma unroll
;                 for (int j = 0; j < 8; ++j) le[j] = L[4 + gi * 8 + j] + bexp[gi * 8 + j];
;                 m0 = le[0];
; #pragma unroll
;                 for (int j = 1; j < 8; ++j) if (le[j] > m0) { m0 = le[j]; j0 = j; }
;                 int j1 = (j0 == 0) ? 1 : 0; float m1 = -3.0e38f;
; #pragma unroll
;                 for (int j = 0; j < 8; ++j) if (j != j0 && le[j] > m1) { m1 = le[j]; j1 = j; }
;                 const float e1 = expf(m1 - m0), w0 = gtop / (1.0f + e1), w1 = gtop * e1 / (1.0f + e1);
.LBB0_979:
	s_or_b64 exec, exec, s[10:11]
	s_waitcnt lgkmcnt(0)
	s_barrier
	s_and_saveexec_b64 s[52:53], s[4:5]
	s_cbranch_execz .LBB0_973
	s_load_dwordx2 s[98:99], s[28:29], 0x0
	s_load_dwordx2 s[100:101], s[28:29], 0x8
	ds_read_b128 v[134:137], v200
	v_or_b32_e32 v138, s18, v0
	v_mov_b32_e32 v139, v163
	v_lshl_add_u32 v146, v138, 3, 0
	v_add_u32_e32 v148, 0x20b00, v146
	v_add_u32_e32 v149, 0x20f00, v146
	s_waitcnt lgkmcnt(0)
	v_pk_add_f32 v[140:141], v[134:135], s[98:99]
	s_nop 0
	v_cmp_gt_f32_e32 vcc, v141, v140
	v_add_f32_e32 v142, s100, v136
	v_add_f32_e32 v143, s101, v137
	v_cndmask_b32_e32 v130, v140, v141, vcc
	v_cmp_gt_f32_e64 s[10:11], v142, v130
	v_cndmask_b32_e64 v131, 0, 8, vcc
	s_nop 0
	v_cndmask_b32_e64 v130, v130, v142, s[10:11]
	v_cmp_gt_f32_e32 vcc, v143, v130
	s_nop 1
	v_cndmask_b32_e32 v144, v130, v143, vcc
	v_cndmask_b32_e64 v130, v131, 16, s[10:11]
	v_cndmask_b32_e64 v147, v130, 24, vcc
	v_lshlrev_b32_e32 v138, 2, v147
	v_lshl_add_u64 v[134:135], s[30:31], 0, v[138:139]
	flat_load_dwordx4 v[130:133], v[134:135]
	v_sub_f32_e32 v139, v140, v144
	flat_load_dwordx4 v[134:137], v[134:135] offset:16
	v_sub_f32_e32 v140, v141, v144
	v_sub_f32_e32 v141, v142, v144
	v_sub_f32_e32 v142, v143, v144
	v_mul_f32_e32 v143, 0x3fb8aa3b, v140
	v_mul_f32_e32 v144, 0x3fb8aa3b, v141
	v_fma_f32 v151, v140, s72, -v143
	v_rndne_f32_e32 v152, v143
	v_mul_f32_e32 v145, 0x3fb8aa3b, v142
	v_fma_f32 v153, v141, s72, -v144
	v_rndne_f32_e32 v154, v144
	v_fmac_f32_e32 v151, 0x32a5705f, v140
	v_sub_f32_e32 v143, v143, v152
	v_mul_f32_e32 v150, 0x3fb8aa3b, v139
	v_fma_f32 v155, v142, s72, -v145
	v_rndne_f32_e32 v156, v145
	v_fmac_f32_e32 v153, 0x32a5705f, v141
	v_sub_f32_e32 v144, v144, v154
	v_add_f32_e32 v143, v143, v151
	v_add_u32_e32 v157, v200, v138
	v_fma_f32 v138, v139, s72, -v150
	v_rndne_f32_e32 v158, v150
	v_cvt_i32_f32_e32 v152, v152
	v_fmac_f32_e32 v155, 0x32a5705f, v142
	v_sub_f32_e32 v145, v145, v156
	v_add_f32_e32 v144, v144, v153
	v_exp_f32_e32 v143, v143
	v_cvt_i32_f32_e32 v154, v154
	v_fmac_f32_e32 v138, 0x32a5705f, v139
	v_sub_f32_e32 v150, v150, v158
	v_add_f32_e32 v145, v145, v155
	v_exp_f32_e32 v144, v144
	v_cvt_i32_f32_e32 v156, v156
	v_add_f32_e32 v138, v150, v138
	v_exp_f32_e32 v145, v145
	v_cvt_i32_f32_e32 v158, v158
	v_exp_f32_e32 v138, v138
	v_ldexp_f32 v143, v143, v152
	v_cmp_ngt_f32_e32 vcc, s73, v140
	v_ldexp_f32 v144, v144, v154
	v_ldexp_f32 v145, v145, v156
	v_cndmask_b32_e32 v143, 0, v143, vcc
	v_cmp_ngt_f32_e32 vcc, s73, v141
	v_ldexp_f32 v138, v138, v158
	s_nop 0
	v_cndmask_b32_e32 v144, 0, v144, vcc
	v_cmp_ngt_f32_e32 vcc, s73, v142
	s_nop 1
	v_cndmask_b32_e32 v145, 0, v145, vcc
	v_cmp_ngt_f32_e32 vcc, s73, v139
	s_nop 1
	v_cndmask_b32_e32 v138, 0, v138, vcc
	v_cmp_nlt_f32_e32 vcc, s74, v140
	s_nop 1
	v_cndmask_b32_e32 v140, v213, v143, vcc
	v_cmp_nlt_f32_e32 vcc, s74, v141
	s_nop 1
	v_cndmask_b32_e32 v141, v213, v144, vcc
	v_cmp_nlt_f32_e32 vcc, s74, v142
	s_nop 1
	v_cndmask_b32_e32 v142, v213, v145, vcc
	v_cmp_nlt_f32_e32 vcc, s74, v139
	s_nop 1
	v_cndmask_b32_e32 v138, v213, v138, vcc
	v_add_f32_e32 v138, v138, v140
	v_add_f32_e32 v138, v141, v138
	v_add_f32_e32 v150, v142, v138
	v_div_scale_f32 v151, s[10:11], v150, v150, 1.0
	v_rcp_f32_e32 v152, v151
	ds_read_b128 v[138:141], v157 offset:16
	ds_read_b128 v[142:145], v157 offset:32
	v_div_scale_f32 v153, vcc, 1.0, v150, 1.0
	v_fma_f32 v154, -v151, v152, 1.0
	v_fmac_f32_e32 v152, v154, v152
	v_mul_f32_e32 v154, v153, v152
	v_fma_f32 v155, -v151, v154, v153
	v_fmac_f32_e32 v154, v155, v152
	v_fma_f32 v151, -v151, v154, v153
	s_waitcnt vmcnt(0) lgkmcnt(0)
; __device__ __forceinline__ void ph10(LAS unsigned char* lds, int tid, int lane, int wave, int G, int bid) {
;     ...
;                 float le[8]; int j0 = 0; float m0;
; #pragma unroll
;                 for (int j = 0; j < 8; ++j) le[j] = L[4 + gi * 8 + j] + bexp[gi * 8 + j];
;                 m0 = le[0];
; #pragma unroll
;                 for (int j = 1; j < 8; ++j) if (le[j] > m0) { m0 = le[j]; j0 = j; }
;                 int j1 = (j0 == 0) ? 1 : 0; float m1 = -3.0e38f;
; #pragma unroll
;                 for (int j = 0; j < 8; ++j) if (j != j0 && le[j] > m1) { m1 = le[j]; j1 = j; }
;                 const float e1 = expf(m1 - m0), w0 = gtop / (1.0f + e1), w1 = gtop * e1 / (1.0f + e1);
;                 const int ex0 = gi * 8 + j0, ex1 = gi * 8 + j1; const int sl = (grp * 16 + tid) * 2;
;                 tokE[sl] = ex0; tokE[sl + 1] = ex1; tokW[sl] = w0; tokW[sl + 1] = w1;
;                 tokLi[sl] = __hip_atomic_fetch_add(lcnt + ex0, 1, __ATOMIC_RELAXED, __HIP_MEMORY_SCOPE_WORKGROUP);
;                 tokLi[sl + 1] = __hip_atomic_fetch_add(lcnt + ex1, 1, __ATOMIC_RELAXED, __HIP_MEMORY_SCOPE_WORKGROUP);
	v_pk_add_f32 v[130:131], v[138:139], v[130:131]
	v_div_fmas_f32 v151, v151, v152, v154
	v_cmp_gt_f32_e32 vcc, v131, v130
	v_add_f32_e32 v138, v140, v132
	v_add_f32_e32 v133, v141, v133
	v_cndmask_b32_e32 v139, v130, v131, vcc
	v_cndmask_b32_e64 v132, 0, 1, vcc
	v_cmp_gt_f32_e32 vcc, v138, v139
	v_add_f32_e32 v134, v142, v134
	v_add_f32_e32 v135, v143, v135
	v_cndmask_b32_e32 v139, v139, v138, vcc
	v_cndmask_b32_e64 v132, v132, 2, vcc
	v_cmp_gt_f32_e32 vcc, v133, v139
	v_add_f32_e32 v136, v144, v136
	v_add_f32_e32 v137, v145, v137
	v_cndmask_b32_e32 v139, v139, v133, vcc
	v_cndmask_b32_e64 v132, v132, 3, vcc
	v_cmp_gt_f32_e32 vcc, v134, v139
	v_cmp_nlt_f32_e64 s[10:11], s75, v130
	v_div_fixup_f32 v150, v151, v150, 1.0
	v_cndmask_b32_e32 v139, v139, v134, vcc
	v_cndmask_b32_e64 v132, v132, 4, vcc
	v_cmp_gt_f32_e32 vcc, v135, v139
	s_nop 1
	v_cndmask_b32_e32 v139, v139, v135, vcc
	v_cndmask_b32_e64 v132, v132, 5, vcc
	v_cmp_gt_f32_e32 vcc, v136, v139
	s_nop 1
	v_cndmask_b32_e32 v139, v139, v136, vcc
	v_cndmask_b32_e64 v132, v132, 6, vcc
	v_cmp_ngt_f32_e64 s[12:13], v137, v139
	s_and_b64 s[76:77], vcc, s[12:13]
	s_nop 0
	v_cndmask_b32_e64 v132, 7, v132, s[12:13]
	v_cmp_eq_u32_e64 s[14:15], 0, v132
	s_or_b64 vcc, s[14:15], s[10:11]
	v_cndmask_b32_e32 v130, v130, v214, vcc
	v_cmp_ne_u32_e64 s[16:17], 1, v132
	v_cmp_gt_f32_e32 vcc, v131, v130
	s_and_b64 vcc, s[16:17], vcc
	v_cmp_ne_u32_e64 s[18:19], 2, v132
	v_cndmask_b32_e32 v130, v130, v131, vcc
	s_or_b64 s[10:11], s[14:15], vcc
	v_cmp_gt_f32_e32 vcc, v138, v130
	s_and_b64 vcc, s[18:19], vcc
	v_cndmask_b32_e64 v131, 0, 1, s[10:11]
	v_cndmask_b32_e32 v130, v130, v138, vcc
	v_cmp_ne_u32_e64 s[20:21], 3, v132
	v_cndmask_b32_e64 v131, v131, 2, vcc
	v_cmp_gt_f32_e32 vcc, v133, v130
	s_and_b64 vcc, s[20:21], vcc
	v_cmp_ne_u32_e64 s[22:23], 4, v132
	v_cndmask_b32_e32 v130, v130, v133, vcc
	v_cndmask_b32_e64 v131, v131, 3, vcc
	v_cmp_gt_f32_e32 vcc, v134, v130
	s_and_b64 vcc, s[22:23], vcc
	v_cmp_ne_u32_e64 s[24:25], 5, v132
	v_cndmask_b32_e32 v130, v130, v134, vcc
	v_cndmask_b32_e64 v131, v131, 4, vcc
	v_cmp_gt_f32_e32 vcc, v135, v130
	s_and_b64 vcc, s[24:25], vcc
	v_cndmask_b32_e64 v139, v137, v139, s[12:13]
	v_cndmask_b32_e32 v130, v130, v135, vcc
	v_cndmask_b32_e64 v131, v131, 5, vcc
	v_cmp_ngt_f32_e32 vcc, v136, v130
	s_or_b64 vcc, s[76:77], vcc
	v_or_b32_e32 v132, v132, v147
	v_cndmask_b32_e32 v130, v136, v130, vcc
	v_cndmask_b32_e32 v131, 6, v131, vcc
	v_cmp_gt_f32_e32 vcc, v137, v130
	s_and_b64 vcc, s[12:13], vcc
	v_lshl_add_u32 v136, v132, 2, s62
	v_cndmask_b32_e32 v130, v130, v137, vcc
	v_sub_f32_e32 v130, v130, v139
	v_mul_f32_e32 v133, 0x3fb8aa3b, v130
	v_fma_f32 v134, v130, s72, -v133
	v_rndne_f32_e32 v135, v133
	v_fmac_f32_e32 v134, 0x32a5705f, v130
	v_sub_f32_e32 v133, v133, v135
	v_add_f32_e32 v133, v133, v134
	v_cvt_i32_f32_e32 v135, v135
	v_exp_f32_e32 v134, v133
	v_cndmask_b32_e64 v131, v131, 7, vcc
	v_add_u32_e32 v133, v131, v147
	v_cmp_ngt_f32_e32 vcc, s73, v130
	v_ldexp_f32 v131, v134, v135
	ds_write_b64 v148, v[132:133]
	v_cndmask_b32_e32 v131, 0, v131, vcc
	v_cmp_nlt_f32_e32 vcc, s74, v130
	s_nop 1
	v_cndmask_b32_e32 v130, v213, v131, vcc
	v_add_f32_e32 v132, 1.0, v130
	v_mul_f32_e32 v130, v150, v130
	v_div_scale_f32 v131, s[10:11], v132, v132, v130
	v_div_scale_f32 v135, s[10:11], v132, v132, v150
	v_rcp_f32_e32 v137, v131
	v_rcp_f32_e32 v138, v135
	v_div_scale_f32 v134, vcc, v130, v132, v130
	v_fma_f32 v140, -v131, v137, 1.0
	v_fma_f32 v141, -v135, v138, 1.0
	v_fmac_f32_e32 v137, v140, v137
	v_div_scale_f32 v139, s[10:11], v150, v132, v150
	v_fmac_f32_e32 v138, v141, v138
	v_mul_f32_e32 v140, v134, v137
	v_mul_f32_e32 v141, v139, v138
	v_fma_f32 v142, -v131, v140, v134
	v_fma_f32 v143, -v135, v141, v139
	v_fmac_f32_e32 v140, v142, v137
	v_fmac_f32_e32 v141, v143, v138
	v_fma_f32 v131, -v131, v140, v134
	v_fma_f32 v134, -v135, v141, v139
	v_div_fmas_f32 v131, v131, v137, v140
	s_mov_b64 vcc, s[10:11]
	v_div_fixup_f32 v131, v131, v132, v130
	v_div_fmas_f32 v130, v134, v138, v141
	v_div_fixup_f32 v130, v130, v132, v150
	ds_write_b64 v149, v[130:131]
	ds_add_rtn_u32 v130, v136, v211
	v_add_u32_e32 v131, 0x21300, v146
	s_waitcnt lgkmcnt(0)
	ds_write_b32 v131, v130
	v_lshl_add_u32 v130, v133, 2, s62
	ds_add_rtn_u32 v130, v130, v211
	s_waitcnt lgkmcnt(0)
	ds_write_b32 v131, v130 offset:4
	s_branch .LBB0_973

; template <class Epi, class Sched, bool ALIGN_EPI = true, bool F8 = false>
; __device__ __forceinline__ void gemm_phase(PG8_LAS unsigned char* lds, const Sched& S, const Epi& E) {
;     ...
;         if constexpr (F8) {
; #pragma unroll
;             for (int a = 0; a < 2; ++a)
; #pragma unroll
;                 for (int b = 0; b < 2; ++b)
;                     asm volatile("s_nop 15\n\ts_nop 7" : "+v"(acc[a][b][0][0]), "+v"(acc[a][b][0][1]), "+v"(acc[a][b][1][0]), "+v"(acc[a][b][1][1]), "+v"(acc[a][b][2][0]), "+v"(acc[a][b][2][1]), "+v"(acc[a][b][3][0]), "+v"(acc[a][b][3][1]));
;     __device__ __forceinline__ void operator()(AccRef acc, const GUnit& u, int wr, int wc, int fr, int fq) const {
;         const int e = u.x0, rt = u.x1, ct = u.x2, cnt = u.x3; const int p0 = rt * 256 + wr * 64 + fr;
;         const int odd = fq & 1;
;         unsigned char* blk = HID + ((size_t)((__builtin_amdgcn_readfirstlane(pre[e]) + rt) * (DE / 128) + ct) << 15) + (wr * 64 + fr) * 128 + wc * 32 + 16 * (fq >> 1);
; #pragma unroll
;         for (int ai = 0; ai < 2; ++ai)
; #pragma unroll
;             for (int mp = 0; mp < 4; mp += 2) {
;                 f32x4 v0, v1, w0, w1;
; #pragma unroll
;                 for (int j = 0; j < 4; ++j) { const float a0 = acc[ai][0][mp][0][j] * W8_INV, a1 = acc[ai][0][mp][1][j] * W8_INV; v0[j] = a0 * fsigmoid(a0) * (acc[ai][1][mp][0][j] * W8_INV); v1[j] = a1 * fsigmoid(a1) * (acc[ai][1][mp][1][j] * W8_INV); }
; #pragma unroll
;                 for (int j = 0; j < 4; ++j) { const float a0 = acc[ai][0][mp + 1][0][j] * W8_INV, a1 = acc[ai][0][mp + 1][1][j] * W8_INV; w0[j] = a0 * fsigmoid(a0) * (acc[ai][1][mp + 1][0][j] * W8_INV); w1[j] = a1 * fsigmoid(a1) * (acc[ai][1][mp + 1][1][j] * W8_INV); }
;                 const unsigned lo0 = pk4_fp8(v0[0], v0[1], v0[2], v0[3]), hi0 = pk4_fp8(v1[0], v1[1], v1[2], v1[3]), lo1 = pk4_fp8(w0[0], w0[1], w0[2], w0[3]), hi1 = pk4_fp8(w1[0], w1[1], w1[2], w1[3]);
;                 const auto sl = __builtin_amdgcn_permlane16_swap(lo0, lo1, false, false), sh = __builtin_amdgcn_permlane16_swap(hi0, hi1, false, false);
;                 const int p = p0 + ai * 128 + (mp + odd) * 16;
;                 if (p < cnt) *(u32x4*)(blk + (ai * 128 + (mp + odd) * 16) * 128) = (u32x4){sl[0], sh[0], sl[1], sh[1]}; }
.LBB0_1064:
	s_lshl_b32 s21, s0, 2
	s_add_i32 s21, s21, 0
	s_add_i32 s21, s21, 0x24100
	v_mov_b32_e32 v2, s21
	s_nop 15
	s_nop 7
	ds_read_b32 v2, v2
	v_mul_f32_e32 v4, 0x3c800000, v138
	v_mul_f32_e32 v5, 0xbfb8aa3b, v4
	v_exp_f32_e32 v5, v5
	v_mul_f32_e32 v9, 0x3c800000, v139
	s_waitcnt lgkmcnt(0)
	v_readfirstlane_b32 s21, v2
	v_mul_f32_e32 v2, 0x3c800000, v142
	v_mul_f32_e32 v3, 0xbfb8aa3b, v2
	v_exp_f32_e32 v3, v3
	v_add_f32_e32 v5, 1.0, v5
	v_rcp_f32_e32 v5, v5
	v_mul_f32_e32 v11, 0xbfb8aa3b, v9
	v_add_f32_e32 v3, 1.0, v3
	v_rcp_f32_e32 v3, v3
	v_exp_f32_e32 v11, v11
	v_mul_f32_e32 v12, 0x3c800000, v140
	v_mul_f32_e32 v13, 0xbfb8aa3b, v12
	v_mul_f32_e32 v2, v2, v3
	v_mul_f32_e32 v3, 0x3c800000, v110
	v_mul_f32_e32 v2, v3, v2
	v_mul_f32_e32 v3, v4, v5
	v_mul_f32_e32 v5, 0x3c800000, v143
	v_mul_f32_e32 v8, 0xbfb8aa3b, v5
	v_exp_f32_e32 v8, v8
	v_mul_f32_e32 v4, 0x3c800000, v106
	v_mul_f32_e32 v3, v4, v3
	v_add_f32_e32 v4, 1.0, v11
	v_add_f32_e32 v8, 1.0, v8
	v_rcp_f32_e32 v8, v8
	v_rcp_f32_e32 v4, v4
	v_exp_f32_e32 v13, v13
	v_mul_f32_e32 v14, 0x3c800000, v141
	v_mul_f32_e32 v5, v5, v8
	v_mul_f32_e32 v8, 0x3c800000, v111
	v_mul_f32_e32 v5, v8, v5
	v_mul_f32_e32 v4, v9, v4
	v_mul_f32_e32 v8, 0x3c800000, v107
	v_mul_f32_e32 v9, 0x3c800000, v144
	v_mul_f32_e32 v11, 0xbfb8aa3b, v9
	v_mul_f32_e32 v4, v8, v4
	v_add_f32_e32 v8, 1.0, v13
	v_exp_f32_e32 v11, v11
	v_rcp_f32_e32 v8, v8
	v_mul_f32_e32 v15, 0xbfb8aa3b, v14
	v_exp_f32_e32 v15, v15
	v_add_f32_e32 v11, 1.0, v11
	v_mul_f32_e32 v8, v12, v8
	v_mul_f32_e32 v12, 0x3c800000, v145
	v_rcp_f32_e32 v11, v11
	v_mul_f32_e32 v13, 0xbfb8aa3b, v12
	v_exp_f32_e32 v13, v13
	v_mul_f32_e32 v16, 0x3c800000, v130
	v_mul_f32_e32 v9, v9, v11
	v_mul_f32_e32 v11, 0x3c800000, v112
	v_mul_f32_e32 v9, v11, v9
	v_mul_f32_e32 v11, 0x3c800000, v108
	v_add_f32_e32 v13, 1.0, v13
	v_rcp_f32_e32 v13, v13
	v_mul_f32_e32 v8, v11, v8
	v_add_f32_e32 v11, 1.0, v15
	v_rcp_f32_e32 v11, v11
	v_mul_f32_e32 v17, 0xbfb8aa3b, v16
	v_exp_f32_e32 v17, v17
	v_mul_f32_e32 v12, v12, v13
	v_mul_f32_e32 v13, 0x3c800000, v113
	v_mul_f32_e32 v12, v13, v12
	v_mul_f32_e32 v11, v14, v11
	v_mul_f32_e32 v13, 0x3c800000, v109
	v_mul_f32_e32 v14, 0x3c800000, v134
	v_mul_f32_e32 v15, 0xbfb8aa3b, v14
	v_mul_f32_e32 v11, v13, v11
	v_add_f32_e32 v13, 1.0, v17
	v_exp_f32_e32 v15, v15
	v_rcp_f32_e32 v13, v13
	v_mul_f32_e32 v18, 0x3c800000, v131
	v_mul_f32_e32 v19, 0xbfb8aa3b, v18
	v_add_f32_e32 v15, 1.0, v15
	v_mul_f32_e32 v13, v16, v13
	v_mul_f32_e32 v16, 0x3c800000, v135
	v_rcp_f32_e32 v15, v15
	v_mul_f32_e32 v17, 0xbfb8aa3b, v16
	v_exp_f32_e32 v17, v17
	v_exp_f32_e32 v19, v19
	v_mul_f32_e32 v14, v14, v15
	v_mul_f32_e32 v15, 0x3c800000, v102
	v_mul_f32_e32 v14, v15, v14
	v_mul_f32_e32 v15, 0x3c800000, v98
	v_add_f32_e32 v17, 1.0, v17
	v_rcp_f32_e32 v17, v17
	v_mul_f32_e32 v13, v15, v13
	v_add_f32_e32 v15, 1.0, v19
	v_mul_f32_e32 v20, 0x3c800000, v132
	v_rcp_f32_e32 v15, v15
	v_mul_f32_e32 v21, 0xbfb8aa3b, v20
	v_exp_f32_e32 v21, v21
	v_mul_f32_e32 v16, v16, v17
	v_mul_f32_e32 v17, 0x3c800000, v103
	v_mul_f32_e32 v16, v17, v16
	v_mul_f32_e32 v15, v18, v15
	v_mul_f32_e32 v17, 0x3c800000, v99
	v_mul_f32_e32 v18, 0x3c800000, v136
	v_mul_f32_e32 v19, 0xbfb8aa3b, v18
	v_mul_f32_e32 v15, v17, v15
	v_add_f32_e32 v17, 1.0, v21
	v_exp_f32_e32 v19, v19
	v_rcp_f32_e32 v17, v17
	v_mul_f32_e32 v22, 0x3c800000, v133
	v_mul_f32_e32 v23, 0xbfb8aa3b, v22
	v_add_f32_e32 v19, 1.0, v19
	v_mul_f32_e32 v17, v20, v17
	v_mul_f32_e32 v20, 0x3c800000, v137
	v_rcp_f32_e32 v19, v19
	v_mul_f32_e32 v21, 0xbfb8aa3b, v20
	v_exp_f32_e32 v21, v21
	v_exp_f32_e32 v23, v23
	v_mul_f32_e32 v18, v18, v19
	v_mul_f32_e32 v19, 0x3c800000, v104
	v_mul_f32_e32 v18, v19, v18
	v_mul_f32_e32 v19, 0x3c800000, v100
	v_add_f32_e32 v21, 1.0, v21
	v_rcp_f32_e32 v21, v21
	v_mul_f32_e32 v17, v19, v17
	v_add_f32_e32 v19, 1.0, v23
	v_rcp_f32_e32 v19, v19
	v_mul_f32_e32 v20, v20, v21
	v_mul_f32_e32 v21, 0x3c800000, v105
	v_mul_f32_e32 v20, v21, v20
	v_mul_f32_e32 v19, v22, v19
	v_mul_f32_e32 v21, 0x3c800000, v101
	v_mul_f32_e32 v19, v21, v19
	v_med3_f32 v21, v2, s63, v215
	v_med3_f32 v5, v5, s63, v215
	v_mov_b32_e32 v2, v171
	v_cvt_pk_fp8_f32 v2, v21, v5
	v_med3_f32 v5, v9, s63, v215
	v_med3_f32 v9, v12, s63, v215
	v_med3_f32 v12, v3, s63, v215
	v_med3_f32 v4, v4, s63, v215
	v_mov_b32_e32 v3, v171
	v_cvt_pk_fp8_f32 v3, v12, v4
	v_cvt_pk_fp8_f32 v2, v5, v9 op_sel:[0,0,1]
	v_med3_f32 v4, v8, s63, v215
	v_med3_f32 v5, v11, s63, v215
	v_cvt_pk_fp8_f32 v3, v4, v5 op_sel:[0,0,1]
	v_med3_f32 v5, v14, s63, v215
	v_med3_f32 v8, v16, s63, v215
	v_mov_b32_e32 v4, v171
	v_cvt_pk_fp8_f32 v4, v5, v8
	v_med3_f32 v11, v13, s63, v215
	v_med3_f32 v12, v15, s63, v215
	v_mov_b32_e32 v5, v171
	v_cvt_pk_fp8_f32 v5, v11, v12
	s_add_i32 s21, s21, s50
	v_med3_f32 v8, v18, s63, v215
	v_med3_f32 v9, v20, s63, v215
	s_lshl_b32 s21, s21, 3
	v_cvt_pk_fp8_f32 v4, v8, v9 op_sel:[0,0,1]
	v_med3_f32 v8, v17, s63, v215
	v_med3_f32 v9, v19, s63, v215
	s_add_i32 s28, s21, s49
	v_cvt_pk_fp8_f32 v5, v8, v9 op_sel:[0,0,1]
	s_ashr_i32 s29, s28, 31
	s_lshl_b64 s[28:29], s[28:29], 15
	v_lshl_add_u32 v10, s50, 8, v209
	v_lshl_add_u64 v[6:7], v[178:179], 0, s[28:29]
	v_or_b32_e32 v8, v10, v173
	v_permlane16_swap_b32_e32 v2, v4
	v_permlane16_swap_b32_e32 v3, v5
	v_cmp_gt_i32_e32 vcc, s51, v8
	v_lshl_add_u64 v[8:9], v[6:7], 0, v[180:181]
	s_and_saveexec_b64 s[28:29], vcc
	s_cbranch_execz .LBB0_1066
	flat_store_dwordx4 v[8:9], v[2:5]

; #define PG8_STAGE(bufoff, gbase, voff) do { _Pragma("unroll") for (int _i = 0; _i < 2; ++_i) \
;         __builtin_amdgcn_global_load_lds((const unsigned*)((const char*)(gbase) + (voff)[_i]), (PG8_LAS unsigned*)(lds + (bufoff) + ldsw + _i * 8192), 16, 0, 0); } while (0)
; #define PG8_WAIT_V(n) asm volatile("s_waitcnt vmcnt(" #n ")" ::: "memory")
; #define PG8_WAIT_L(n) asm volatile("s_waitcnt lgkmcnt(" #n ")" ::: "memory")
; template <class Epi, class Sched, bool ALIGN_EPI = true, bool F8 = false>
; __device__ __forceinline__ void gemm_phase(PG8_LAS unsigned char* lds, const Sched& S, const Epi& E) {
;     ...
;         for (int t = 0; t < nt; t += 2) {
;             const bool last = (t == nt - 2);
;             if constexpr (Sched::GATHER) { if (last && has_next) S.a_off(nxt, Rs, Cs, voffAn); }
;             const char* a1 = cA + (size_t)(t + 1) * kstep;
;             const char* a2 = last ? nA : cA + (size_t)(t + 2) * kstep; const char* b2 = last ? nB : cB + (size_t)(t + 2) * kstepB;
;             const char* a3 = a2 + kstep; const char* b3 = b2 + kstepB;
;             unsigned vA2[2][2];
; #pragma unroll
;             for (int h = 0; h < 2; ++h)
; #pragma unroll
;                 for (int i = 0; i < 2; ++i) { if constexpr (Sched::GATHER) vA2[h][i] = (last && has_next) ? voffAn[h][i] : voffA[h][i]; else vA2[h][i] = voffA[h][i]; }
;             PG8_LDB(B0, 0, 0); PG8_LDB(B1, 0, 1); PG8_SCHED; PG8_LDA(At, 0, 0); PG8_STAGE(PG8_SA(1, 1), a1, voffA[1]);
;             PG8_WAIT_V(8); PG8_WAIT_L(0); PG8_BAR; PG8_MMA(0, 0, At, B0); PG8_MMA(0, 1, At, B1); PG8_BAR; PG8_SCHED;
;             PG8_LDA(At, 0, 1); PG8_STAGE(PG8_SB(0, 0), b2, voffB[0]); PG8_STAGE(PG8_SB(0, 1), b2, voffB[1]); PG8_STAGE(PG8_SA(0, 0), a2, vA2[0]);
;             PG8_WAIT_V(8); PG8_WAIT_L(0); PG8_BAR; PG8_MMA(1, 0, At, B0); PG8_MMA(1, 1, At, B1); PG8_BAR; PG8_SCHED;
;             PG8_LDB(B0, 1, 0); PG8_LDB(B1, 1, 1); PG8_SCHED; PG8_LDA(At, 1, 0); PG8_STAGE(PG8_SA(0, 1), a2, vA2[1]);
;             PG8_WAIT_V(8); PG8_WAIT_L(0); PG8_BAR; PG8_MMA(0, 0, At, B0); PG8_MMA(0, 1, At, B1); PG8_BAR; PG8_SCHED;
;             PG8_LDA(At, 1, 1); PG8_STAGE(PG8_SB(1, 0), b3, voffB[0]); PG8_STAGE(PG8_SB(1, 1), b3, voffB[1]); PG8_STAGE(PG8_SA(1, 0), a3, vA2[0]);
;             PG8_WAIT_V(8); PG8_WAIT_L(0); PG8_BAR; PG8_MMA(1, 0, At, B0); PG8_MMA(1, 1, At, B1); PG8_BAR; PG8_SCHED;
.Lh1e_33571:
.Lh1_1138:
	ds_read_b128 v[18:21], v189
	ds_read_b128 v[22:25], v189 offset:1024
	ds_read_b128 v[26:29], v189 offset:2048
	ds_read_b128 v[30:33], v189 offset:3072
	ds_read_b128 v[2:5], v190
	ds_read_b128 v[6:9], v190 offset:1024
	ds_read_b128 v[10:13], v190 offset:2048
	ds_read_b128 v[14:17], v190 offset:3072
	s_add_u32 s26, s24, 0x8000
	s_addc_u32 s27, s25, 0
	s_cmp_eq_u32 s68, 4
	s_cselect_b32 s30, s16, s26
	s_cselect_b32 s31, s17, s27
	s_cselect_b32 s28, s18, s23
	s_cselect_b32 s29, s19, s67
	s_add_u32 s26, s30, 0x8000
	s_addc_u32 s27, s31, 0
	v_lshl_add_u64 v[226:227], s[24:25], 0, v[184:185]
	s_add_i32 m0, s44, 0xc000
	ds_read_b128 v[194:197], v191
	ds_read_b128 v[198:201], v191 offset:1024
	ds_read_b128 v[202:205], v191 offset:2048
	ds_read_b128 v[206:209], v191 offset:3072
	ds_read_b128 v[210:213], v191 offset:4096
	ds_read_b128 v[214:217], v191 offset:5120
	ds_read_b128 v[218:221], v191 offset:6144
	ds_read_b128 v[222:225], v191 offset:7168
	global_load_lds_dwordx4 v[226:227], off
	v_lshl_add_u64 v[226:227], s[24:25], 0, v[182:183]
	s_add_i32 m0, s44, 0xe000
	s_nop 0
	global_load_lds_dwordx4 v[226:227], off
	s_waitcnt vmcnt(8)
	s_waitcnt lgkmcnt(0)
	s_barrier
	s_setprio 2
	s_waitcnt lgkmcnt(0)
	v_mfma_scale_f32_16x16x128_f8f6f4 v[158:161], v[18:25], v[194:201], v[158:161], v192, v192 op_sel_hi:[0,0,0]
	v_mfma_scale_f32_16x16x128_f8f6f4 v[154:157], v[26:33], v[194:201], v[154:157], v192, v192 op_sel_hi:[0,0,0]
	v_mfma_scale_f32_16x16x128_f8f6f4 v[142:145], v[18:25], v[202:209], v[142:145], v192, v192 op_sel_hi:[0,0,0]
	v_mfma_scale_f32_16x16x128_f8f6f4 v[138:141], v[26:33], v[202:209], v[138:141], v192, v192 op_sel_hi:[0,0,0]
	v_mfma_scale_f32_16x16x128_f8f6f4 v[126:129], v[18:25], v[210:217], v[126:129], v192, v192 op_sel_hi:[0,0,0]
	v_mfma_scale_f32_16x16x128_f8f6f4 v[122:125], v[26:33], v[210:217], v[122:125], v192, v192 op_sel_hi:[0,0,0]
	v_mfma_scale_f32_16x16x128_f8f6f4 v[110:113], v[18:25], v[218:225], v[110:113], v192, v192 op_sel_hi:[0,0,0]
	v_mfma_scale_f32_16x16x128_f8f6f4 v[106:109], v[26:33], v[218:225], v[106:109], v192, v192 op_sel_hi:[0,0,0]
	s_nop 3
	s_setprio 0
	s_setprio 2
	v_mfma_scale_f32_16x16x128_f8f6f4 v[150:153], v[2:9], v[194:201], v[150:153], v192, v192 op_sel_hi:[0,0,0]
	v_mfma_scale_f32_16x16x128_f8f6f4 v[146:149], v[10:17], v[194:201], v[146:149], v192, v192 op_sel_hi:[0,0,0]
	v_mfma_scale_f32_16x16x128_f8f6f4 v[134:137], v[2:9], v[202:209], v[134:137], v192, v192 op_sel_hi:[0,0,0]
	v_mfma_scale_f32_16x16x128_f8f6f4 v[130:133], v[10:17], v[202:209], v[130:133], v192, v192 op_sel_hi:[0,0,0]
	v_mfma_scale_f32_16x16x128_f8f6f4 v[118:121], v[2:9], v[210:217], v[118:121], v192, v192 op_sel_hi:[0,0,0]
	v_mfma_scale_f32_16x16x128_f8f6f4 v[114:117], v[10:17], v[210:217], v[114:117], v192, v192 op_sel_hi:[0,0,0]
	v_mfma_scale_f32_16x16x128_f8f6f4 v[102:105], v[2:9], v[218:225], v[102:105], v192, v192 op_sel_hi:[0,0,0]
	v_mfma_scale_f32_16x16x128_f8f6f4 v[98:101], v[10:17], v[218:225], v[98:101], v192, v192 op_sel_hi:[0,0,0]
	s_nop 3
	s_setprio 0
	s_add_i32 s69, s53, s43
	v_lshl_add_u64 v[226:227], s[28:29], 0, v[164:165]
	s_mov_b32 m0, s69
	ds_read_b128 v[194:197], v191 offset:16384
	ds_read_b128 v[198:201], v191 offset:17408
	ds_read_b128 v[202:205], v191 offset:18432
	ds_read_b128 v[206:209], v191 offset:19456
	ds_read_b128 v[210:213], v191 offset:20480
	ds_read_b128 v[214:217], v191 offset:21504
	ds_read_b128 v[218:221], v191 offset:22528
	ds_read_b128 v[222:225], v191 offset:23552
	global_load_lds_dwordx4 v[226:227], off
	v_lshl_add_u64 v[228:229], s[28:29], 0, v[166:167]
	s_add_i32 m0, s69, 0x2000
	s_add_i32 s69, s58, s43
	global_load_lds_dwordx4 v[228:229], off
	v_lshl_add_u64 v[226:227], v[226:227], 0, s[4:5]
	s_mov_b32 m0, s69
	s_nop 0
	global_load_lds_dwordx4 v[226:227], off
	v_lshl_add_u64 v[226:227], v[228:229], 0, s[4:5]
	s_add_i32 m0, s69, 0x2000
	s_nop 0
	global_load_lds_dwordx4 v[226:227], off
	v_lshl_add_u64 v[226:227], s[30:31], 0, v[168:169]
	s_mov_b32 m0, s44
	s_nop 0
	global_load_lds_dwordx4 v[226:227], off
	v_lshl_add_u64 v[226:227], s[30:31], 0, v[170:171]
	s_mov_b32 m0, s45
	s_nop 0
	global_load_lds_dwordx4 v[226:227], off
	s_waitcnt vmcnt(8)
	s_waitcnt lgkmcnt(0)
	s_barrier
	s_setprio 2
	s_waitcnt lgkmcnt(0)
	v_mfma_scale_f32_16x16x128_f8f6f4 v[94:97], v[18:25], v[194:201], v[94:97], v192, v192 op_sel_hi:[0,0,0]
	v_mfma_scale_f32_16x16x128_f8f6f4 v[90:93], v[26:33], v[194:201], v[90:93], v192, v192 op_sel_hi:[0,0,0]
	v_mfma_scale_f32_16x16x128_f8f6f4 v[78:81], v[18:25], v[202:209], v[78:81], v192, v192 op_sel_hi:[0,0,0]
	v_mfma_scale_f32_16x16x128_f8f6f4 v[74:77], v[26:33], v[202:209], v[74:77], v192, v192 op_sel_hi:[0,0,0]
	v_mfma_scale_f32_16x16x128_f8f6f4 v[62:65], v[18:25], v[210:217], v[62:65], v192, v192 op_sel_hi:[0,0,0]
	v_mfma_scale_f32_16x16x128_f8f6f4 v[58:61], v[26:33], v[210:217], v[58:61], v192, v192 op_sel_hi:[0,0,0]
	v_mfma_scale_f32_16x16x128_f8f6f4 v[46:49], v[18:25], v[218:225], v[46:49], v192, v192 op_sel_hi:[0,0,0]
	v_mfma_scale_f32_16x16x128_f8f6f4 v[42:45], v[26:33], v[218:225], v[42:45], v192, v192 op_sel_hi:[0,0,0]
	s_nop 3
	s_setprio 0
	s_setprio 2
	v_mfma_scale_f32_16x16x128_f8f6f4 v[86:89], v[2:9], v[194:201], v[86:89], v192, v192 op_sel_hi:[0,0,0]
	v_mfma_scale_f32_16x16x128_f8f6f4 v[82:85], v[10:17], v[194:201], v[82:85], v192, v192 op_sel_hi:[0,0,0]
	v_mfma_scale_f32_16x16x128_f8f6f4 v[70:73], v[2:9], v[202:209], v[70:73], v192, v192 op_sel_hi:[0,0,0]
	v_mfma_scale_f32_16x16x128_f8f6f4 v[66:69], v[10:17], v[202:209], v[66:69], v192, v192 op_sel_hi:[0,0,0]
	v_mfma_scale_f32_16x16x128_f8f6f4 v[54:57], v[2:9], v[210:217], v[54:57], v192, v192 op_sel_hi:[0,0,0]
	v_mfma_scale_f32_16x16x128_f8f6f4 v[50:53], v[10:17], v[210:217], v[50:53], v192, v192 op_sel_hi:[0,0,0]
	v_mfma_scale_f32_16x16x128_f8f6f4 v[38:41], v[2:9], v[218:225], v[38:41], v192, v192 op_sel_hi:[0,0,0]
	v_mfma_scale_f32_16x16x128_f8f6f4 v[34:37], v[10:17], v[218:225], v[34:37], v192, v192 op_sel_hi:[0,0,0]
	s_nop 3
	s_setprio 0
	s_add_i32 s69, 0, 0x18000
	s_add_i32 s70, 0, 0x1c000
	v_add_u32_e32 v14, s69, v187
	v_add_u32_e32 v30, s70, v187
	ds_read_b128 v[2:5], v14
	ds_read_b128 v[6:9], v14 offset:1024
	ds_read_b128 v[10:13], v14 offset:2048
	ds_read_b128 v[14:17], v14 offset:3072
	ds_read_b128 v[18:21], v30
	ds_read_b128 v[22:25], v30 offset:1024
	ds_read_b128 v[26:29], v30 offset:2048
	ds_read_b128 v[30:33], v30 offset:3072
	s_mov_b32 m0, s46
	v_lshl_add_u64 v[226:227], s[30:31], 0, v[172:173]
	ds_read_b128 v[194:197], v191 offset:32768
	ds_read_b128 v[198:201], v191 offset:33792
	ds_read_b128 v[202:205], v191 offset:34816
	ds_read_b128 v[206:209], v191 offset:35840
	ds_read_b128 v[210:213], v191 offset:36864
	ds_read_b128 v[214:217], v191 offset:37888
	ds_read_b128 v[218:221], v191 offset:38912
	ds_read_b128 v[222:225], v191 offset:39936
	global_load_lds_dwordx4 v[226:227], off
	v_lshl_add_u64 v[226:227], s[30:31], 0, v[174:175]
	s_mov_b32 m0, s47
	s_nop 0
	global_load_lds_dwordx4 v[226:227], off
	s_waitcnt vmcnt(8)
	s_waitcnt lgkmcnt(0)
	s_barrier
; #define PG8_STAGE(bufoff, gbase, voff) do { _Pragma("unroll") for (int _i = 0; _i < 2; ++_i) \
;         __builtin_amdgcn_global_load_lds((const unsigned*)((const char*)(gbase) + (voff)[_i]), (PG8_LAS unsigned*)(lds + (bufoff) + ldsw + _i * 8192), 16, 0, 0); } while (0)
; #define PG8_WAIT_V(n) asm volatile("s_waitcnt vmcnt(" #n ")" ::: "memory")
; #define PG8_WAIT_L(n) asm volatile("s_waitcnt lgkmcnt(" #n ")" ::: "memory")
; template <class Epi, class Sched, bool ALIGN_EPI = true, bool F8 = false>
; __device__ __forceinline__ void gemm_phase(PG8_LAS unsigned char* lds, const Sched& S, const Epi& E) {
;     ...
;         for (int t = 0; t < nt; t += 2) {
;             const bool last = (t == nt - 2);
;             if constexpr (Sched::GATHER) { if (last && has_next) S.a_off(nxt, Rs, Cs, voffAn); }
;             const char* a1 = cA + (size_t)(t + 1) * kstep;
;             const char* a2 = last ? nA : cA + (size_t)(t + 2) * kstep; const char* b2 = last ? nB : cB + (size_t)(t + 2) * kstepB;
;             const char* a3 = a2 + kstep; const char* b3 = b2 + kstepB;
;             unsigned vA2[2][2];
; #pragma unroll
;             for (int h = 0; h < 2; ++h)
; #pragma unroll
;                 for (int i = 0; i < 2; ++i) { if constexpr (Sched::GATHER) vA2[h][i] = (last && has_next) ? voffAn[h][i] : voffA[h][i]; else vA2[h][i] = voffA[h][i]; }
;             PG8_LDB(B0, 0, 0); PG8_LDB(B1, 0, 1); PG8_SCHED; PG8_LDA(At, 0, 0); PG8_STAGE(PG8_SA(1, 1), a1, voffA[1]);
;             PG8_WAIT_V(8); PG8_WAIT_L(0); PG8_BAR; PG8_MMA(0, 0, At, B0); PG8_MMA(0, 1, At, B1); PG8_BAR; PG8_SCHED;
;             PG8_LDA(At, 0, 1); PG8_STAGE(PG8_SB(0, 0), b2, voffB[0]); PG8_STAGE(PG8_SB(0, 1), b2, voffB[1]); PG8_STAGE(PG8_SA(0, 0), a2, vA2[0]);
;             PG8_WAIT_V(8); PG8_WAIT_L(0); PG8_BAR; PG8_MMA(1, 0, At, B0); PG8_MMA(1, 1, At, B1); PG8_BAR; PG8_SCHED;
;             PG8_LDB(B0, 1, 0); PG8_LDB(B1, 1, 1); PG8_SCHED; PG8_LDA(At, 1, 0); PG8_STAGE(PG8_SA(0, 1), a2, vA2[1]);
;             PG8_WAIT_V(8); PG8_WAIT_L(0); PG8_BAR; PG8_MMA(0, 0, At, B0); PG8_MMA(0, 1, At, B1); PG8_BAR; PG8_SCHED;
;             PG8_LDA(At, 1, 1); PG8_STAGE(PG8_SB(1, 0), b3, voffB[0]); PG8_STAGE(PG8_SB(1, 1), b3, voffB[1]); PG8_STAGE(PG8_SA(1, 0), a3, vA2[0]);
;             PG8_WAIT_V(8); PG8_WAIT_L(0); PG8_BAR; PG8_MMA(1, 0, At, B0); PG8_MMA(1, 1, At, B1); PG8_BAR; PG8_SCHED;
	s_setprio 2
	s_waitcnt lgkmcnt(0)
	v_mfma_scale_f32_16x16x128_f8f6f4 v[158:161], v[2:9], v[194:201], v[158:161], v192, v192 op_sel_hi:[0,0,0]
	v_mfma_scale_f32_16x16x128_f8f6f4 v[154:157], v[10:17], v[194:201], v[154:157], v192, v192 op_sel_hi:[0,0,0]
	v_mfma_scale_f32_16x16x128_f8f6f4 v[142:145], v[2:9], v[202:209], v[142:145], v192, v192 op_sel_hi:[0,0,0]
	v_mfma_scale_f32_16x16x128_f8f6f4 v[138:141], v[10:17], v[202:209], v[138:141], v192, v192 op_sel_hi:[0,0,0]
	v_mfma_scale_f32_16x16x128_f8f6f4 v[126:129], v[2:9], v[210:217], v[126:129], v192, v192 op_sel_hi:[0,0,0]
	v_mfma_scale_f32_16x16x128_f8f6f4 v[122:125], v[10:17], v[210:217], v[122:125], v192, v192 op_sel_hi:[0,0,0]
	v_mfma_scale_f32_16x16x128_f8f6f4 v[110:113], v[2:9], v[218:225], v[110:113], v192, v192 op_sel_hi:[0,0,0]
	v_mfma_scale_f32_16x16x128_f8f6f4 v[106:109], v[10:17], v[218:225], v[106:109], v192, v192 op_sel_hi:[0,0,0]
	s_nop 3
	s_setprio 0
	s_setprio 2
	v_mfma_scale_f32_16x16x128_f8f6f4 v[150:153], v[18:25], v[194:201], v[150:153], v192, v192 op_sel_hi:[0,0,0]
	v_mfma_scale_f32_16x16x128_f8f6f4 v[146:149], v[26:33], v[194:201], v[146:149], v192, v192 op_sel_hi:[0,0,0]
	v_mfma_scale_f32_16x16x128_f8f6f4 v[134:137], v[18:25], v[202:209], v[134:137], v192, v192 op_sel_hi:[0,0,0]
	v_mfma_scale_f32_16x16x128_f8f6f4 v[130:133], v[26:33], v[202:209], v[130:133], v192, v192 op_sel_hi:[0,0,0]
	v_mfma_scale_f32_16x16x128_f8f6f4 v[118:121], v[18:25], v[210:217], v[118:121], v192, v192 op_sel_hi:[0,0,0]
	v_mfma_scale_f32_16x16x128_f8f6f4 v[114:117], v[26:33], v[210:217], v[114:117], v192, v192 op_sel_hi:[0,0,0]
	v_mfma_scale_f32_16x16x128_f8f6f4 v[102:105], v[18:25], v[218:225], v[102:105], v192, v192 op_sel_hi:[0,0,0]
	v_mfma_scale_f32_16x16x128_f8f6f4 v[98:101], v[26:33], v[218:225], v[98:101], v192, v192 op_sel_hi:[0,0,0]
	s_nop 3
	s_setprio 0
	s_add_u32 s28, s28, 0x8000
	s_addc_u32 s29, s29, 0
	s_add_i32 s30, s69, s43
	v_lshl_add_u64 v[226:227], s[28:29], 0, v[164:165]
	s_mov_b32 m0, s30
	ds_read_b128 v[194:197], v191 offset:49152
	ds_read_b128 v[198:201], v191 offset:50176
	ds_read_b128 v[202:205], v191 offset:51200
	ds_read_b128 v[206:209], v191 offset:52224
	ds_read_b128 v[210:213], v191 offset:53248
	ds_read_b128 v[214:217], v191 offset:54272
	ds_read_b128 v[218:221], v191 offset:55296
	ds_read_b128 v[222:225], v191 offset:56320
	global_load_lds_dwordx4 v[226:227], off
	v_lshl_add_u64 v[226:227], s[28:29], 0, v[166:167]
	s_add_i32 m0, s30, 0x2000
	s_add_i32 s30, s70, s43
	global_load_lds_dwordx4 v[226:227], off
	v_lshl_add_u64 v[226:227], s[28:29], 0, v[178:179]
	s_mov_b32 m0, s30
	s_nop 0
	global_load_lds_dwordx4 v[226:227], off
	v_lshl_add_u64 v[226:227], s[28:29], 0, v[180:181]
	s_add_i32 m0, s30, 0x2000
	s_nop 0
	global_load_lds_dwordx4 v[226:227], off
	v_lshl_add_u64 v[226:227], s[26:27], 0, v[168:169]
	s_mov_b32 m0, s51
	s_nop 0
	global_load_lds_dwordx4 v[226:227], off
	v_lshl_add_u64 v[226:227], s[26:27], 0, v[170:171]
	s_mov_b32 m0, s52
	s_nop 0
	global_load_lds_dwordx4 v[226:227], off
	s_waitcnt vmcnt(8)
	s_waitcnt lgkmcnt(0)
	s_barrier
	s_setprio 2
	s_waitcnt lgkmcnt(0)
	v_mfma_scale_f32_16x16x128_f8f6f4 v[94:97], v[2:9], v[194:201], v[94:97], v192, v192 op_sel_hi:[0,0,0]
	v_mfma_scale_f32_16x16x128_f8f6f4 v[90:93], v[10:17], v[194:201], v[90:93], v192, v192 op_sel_hi:[0,0,0]
	v_mfma_scale_f32_16x16x128_f8f6f4 v[78:81], v[2:9], v[202:209], v[78:81], v192, v192 op_sel_hi:[0,0,0]
	v_mfma_scale_f32_16x16x128_f8f6f4 v[74:77], v[10:17], v[202:209], v[74:77], v192, v192 op_sel_hi:[0,0,0]
	v_mfma_scale_f32_16x16x128_f8f6f4 v[62:65], v[2:9], v[210:217], v[62:65], v192, v192 op_sel_hi:[0,0,0]
	v_mfma_scale_f32_16x16x128_f8f6f4 v[58:61], v[10:17], v[210:217], v[58:61], v192, v192 op_sel_hi:[0,0,0]
	v_mfma_scale_f32_16x16x128_f8f6f4 v[46:49], v[2:9], v[218:225], v[46:49], v192, v192 op_sel_hi:[0,0,0]
	v_mfma_scale_f32_16x16x128_f8f6f4 v[42:45], v[10:17], v[218:225], v[42:45], v192, v192 op_sel_hi:[0,0,0]
	s_nop 3
	s_setprio 0
	s_setprio 2
	v_mfma_scale_f32_16x16x128_f8f6f4 v[86:89], v[18:25], v[194:201], v[86:89], v192, v192 op_sel_hi:[0,0,0]
	v_mfma_scale_f32_16x16x128_f8f6f4 v[82:85], v[26:33], v[194:201], v[82:85], v192, v192 op_sel_hi:[0,0,0]
	v_mfma_scale_f32_16x16x128_f8f6f4 v[70:73], v[18:25], v[202:209], v[70:73], v192, v192 op_sel_hi:[0,0,0]
	v_mfma_scale_f32_16x16x128_f8f6f4 v[66:69], v[26:33], v[202:209], v[66:69], v192, v192 op_sel_hi:[0,0,0]
	v_mfma_scale_f32_16x16x128_f8f6f4 v[54:57], v[18:25], v[210:217], v[54:57], v192, v192 op_sel_hi:[0,0,0]
	v_mfma_scale_f32_16x16x128_f8f6f4 v[50:53], v[26:33], v[210:217], v[50:53], v192, v192 op_sel_hi:[0,0,0]
	v_mfma_scale_f32_16x16x128_f8f6f4 v[38:41], v[18:25], v[218:225], v[38:41], v192, v192 op_sel_hi:[0,0,0]
	v_mfma_scale_f32_16x16x128_f8f6f4 v[34:37], v[26:33], v[218:225], v[34:37], v192, v192 op_sel_hi:[0,0,0]
	s_nop 3
	s_setprio 0
	s_add_i32 s68, s68, 2
	s_add_u32 s23, s23, 0x10000
	s_addc_u32 s67, s67, 0
	s_add_u32 s24, s24, 0x10000
	s_addc_u32 s25, s25, 0
	s_cmp_gt_u32 s68, 5
	s_cbranch_scc0 .Lh1_1138

; __device__ __forceinline__ unsigned pk4_fp8(float a, float b, float c, float d) { int w = 0; w = __builtin_amdgcn_cvt_pk_fp8_f32(clamp8(a), clamp8(b), w, false); w = __builtin_amdgcn_cvt_pk_fp8_f32(clamp8(c), clamp8(d), w, true); return (unsigned)w; }
; template <class Epi, class Sched, bool ALIGN_EPI = true, bool F8 = false>
; __device__ __forceinline__ void gemm_phase(PG8_LAS unsigned char* lds, const Sched& S, const Epi& E) {
;     ...
;         if constexpr (F8) {
; #pragma unroll
;             for (int a = 0; a < 2; ++a)
; #pragma unroll
;                 for (int b = 0; b < 2; ++b)
;                     asm volatile("s_nop 15\n\ts_nop 7" : "+v"(acc[a][b][0][0]), "+v"(acc[a][b][0][1]), "+v"(acc[a][b][1][0]), "+v"(acc[a][b][1][1]), "+v"(acc[a][b][2][0]), "+v"(acc[a][b][2][1]), "+v"(acc[a][b][3][0]), "+v"(acc[a][b][3][1]));
;     __device__ __forceinline__ void operator()(AccRef acc, const GUnit& u, int wr, int wc, int fr, int fq) const {
;         const int e = u.x0, rt = u.x1, ct = u.x2, cnt = u.x3; const int* rl = rowlist + (size_t)e * ECAP; const int p0 = rt * 256 + wr * 64 + fr;
;         unsigned ent[2][4];
; #pragma unroll
;         for (int ai = 0; ai < 2; ++ai)
; #pragma unroll
;             for (int m = 0; m < 4; ++m) { int p = p0 + ai * 128 + m * 16; p = p < cnt ? p : cnt - 1; ent[ai][m] = (unsigned)rl[p]; }
; #pragma unroll
;         for (int ai = 0; ai < 2; ++ai)
; #pragma unroll
;             for (int m = 0; m < 4; ++m) { const int p = p0 + ai * 128 + m * 16;
;                 if (p < cnt) { u32x4 w;
; #pragma unroll
;                     for (int q = 0; q < 4; ++q) { const f32x4 v = acc[ai][q >> 1][m][q & 1] * (W8_INV * Y8_SCALE); w[q] = pk4_fp8(v[0], v[1], v[2], v[3]); }
;                     *(u32x4*)(Y + (size_t)ent[ai][m] * D + ct * 256 + wc * 64 + 16 * fq) = w; } }
.LBB0_1141:
	s_ashr_i32 s23, s22, 31
	s_lshl_b64 s[22:23], s[22:23], 17
	s_add_u32 s26, s49, s22
	v_lshl_add_u32 v16, s66, 8, v186
	s_addc_u32 s27, s50, s23
	s_add_i32 s22, s48, -1
	v_or_b32_e32 v15, 16, v16
	v_min_i32_e32 v2, s22, v15
	v_ashrrev_i32_e32 v3, 31, v2
	v_or_b32_e32 v13, 32, v16
	v_lshl_add_u64 v[18:19], v[2:3], 2, s[26:27]
	v_min_i32_e32 v2, s22, v13
	v_ashrrev_i32_e32 v3, 31, v2
	v_or_b32_e32 v11, 48, v16
	v_lshl_add_u64 v[20:21], v[2:3], 2, s[26:27]
	v_min_i32_e32 v2, s22, v11
	v_ashrrev_i32_e32 v3, 31, v2
	v_add_u32_e32 v9, 0x80, v16
	v_lshl_add_u64 v[22:23], v[2:3], 2, s[26:27]
	v_min_i32_e32 v2, s22, v9
	v_ashrrev_i32_e32 v3, 31, v2
	v_add_u32_e32 v7, 0x90, v16
	v_lshl_add_u64 v[24:25], v[2:3], 2, s[26:27]
	v_min_i32_e32 v2, s22, v7
	v_ashrrev_i32_e32 v3, 31, v2
	v_add_u32_e32 v5, 0xa0, v16
	v_lshl_add_u64 v[26:27], v[2:3], 2, s[26:27]
	v_min_i32_e32 v2, s22, v5
	v_ashrrev_i32_e32 v3, 31, v2
	v_lshl_add_u64 v[28:29], v[2:3], 2, s[26:27]
	v_add_u32_e32 v3, 0xb0, v16
	v_min_i32_e32 v30, s22, v3
	v_ashrrev_i32_e32 v31, 31, v30
	s_nop 15
	s_nop 7
	v_lshl_add_u64 v[30:31], v[30:31], 2, s[26:27]
	flat_load_dword v14, v[18:19]
	flat_load_dword v12, v[20:21]
	flat_load_dword v10, v[22:23]
	flat_load_dword v8, v[24:25]
	flat_load_dword v6, v[26:27]
	flat_load_dword v4, v[28:29]
	flat_load_dword v2, v[30:31]
	s_lshl_b32 s22, s65, 8
	s_ashr_i32 s23, s22, 31
	v_cmp_gt_i32_e32 vcc, s48, v16
	s_and_saveexec_b64 s[24:25], vcc
	s_cbranch_execz .LBB0_1150
	v_ashrrev_i32_e32 v17, 31, v16
	v_lshl_add_u64 v[16:17], v[16:17], 2, s[26:27]
	flat_load_dword v176, v[16:17]
	v_pk_mul_f32 v[16:17], v[158:159], s[14:15] op_sel_hi:[1,0]
	s_nop 0
	v_med3_f32 v18, v16, s59, v193
	v_med3_f32 v17, v17, s59, v193
	v_mov_b32_e32 v16, v177
	v_cvt_pk_fp8_f32 v16, v18, v17
	v_pk_mul_f32 v[18:19], v[160:161], s[14:15] op_sel_hi:[1,0]
	s_nop 0
	v_med3_f32 v17, v18, s59, v193
	v_med3_f32 v18, v19, s59, v193
	v_cvt_pk_fp8_f32 v16, v17, v18 op_sel:[0,0,1]
	v_pk_mul_f32 v[18:19], v[154:155], s[14:15] op_sel_hi:[1,0]
	v_mov_b32_e32 v17, v177
	v_med3_f32 v18, v18, s59, v193
	v_med3_f32 v19, v19, s59, v193
	v_cvt_pk_fp8_f32 v17, v18, v19
	v_pk_mul_f32 v[18:19], v[156:157], s[14:15] op_sel_hi:[1,0]
	s_nop 0
	v_med3_f32 v18, v18, s59, v193
	v_med3_f32 v19, v19, s59, v193
	v_cvt_pk_fp8_f32 v17, v18, v19 op_sel:[0,0,1]
	v_pk_mul_f32 v[18:19], v[150:151], s[14:15] op_sel_hi:[1,0]
	s_nop 0
	v_med3_f32 v20, v18, s59, v193
	v_med3_f32 v19, v19, s59, v193
	v_mov_b32_e32 v18, v177
	v_cvt_pk_fp8_f32 v18, v20, v19
	v_pk_mul_f32 v[20:21], v[152:153], s[14:15] op_sel_hi:[1,0]
	s_nop 0
	v_med3_f32 v19, v20, s59, v193
	v_med3_f32 v20, v21, s59, v193
	v_cvt_pk_fp8_f32 v18, v19, v20 op_sel:[0,0,1]
	v_pk_mul_f32 v[20:21], v[146:147], s[14:15] op_sel_hi:[1,0]
	v_mov_b32_e32 v19, v177
	v_med3_f32 v20, v20, s59, v193
	v_med3_f32 v21, v21, s59, v193
	v_cvt_pk_fp8_f32 v19, v20, v21
	v_pk_mul_f32 v[20:21], v[148:149], s[14:15] op_sel_hi:[1,0]
	s_nop 0
	v_med3_f32 v20, v20, s59, v193
	v_med3_f32 v21, v21, s59, v193
	v_cvt_pk_fp8_f32 v19, v20, v21 op_sel:[0,0,1]
	s_waitcnt vmcnt(0) lgkmcnt(0)
	v_lshlrev_b64 v[20:21], 11, v[176:177]
	v_lshl_add_u64 v[20:21], s[10:11], 0, v[20:21]
	v_lshl_add_u64 v[20:21], v[20:21], 0, s[22:23]
	v_lshl_add_u64 v[20:21], v[20:21], 0, s[6:7]
	v_lshl_add_u64 v[20:21], v[20:21], 0, v[162:163]
	flat_store_dwordx4 v[20:21], v[16:19]
	s_or_b64 exec, exec, s[24:25]
	v_cmp_gt_i32_e32 vcc, s48, v15
	s_and_saveexec_b64 s[24:25], vcc
	s_cbranch_execnz .LBB0_1151
